# v69 + mid-segment s_setprio 0/1 pairs between the two MFMA groups removed
# baseline (speedup 1.0000x reference)
.LBB0_286:
	s_lshl_b32 s10, s51, 19
	s_add_u32 s10, s20, s10
	s_addc_u32 s11, s21, 0
	s_and_b64 s[16:17], s[4:5], exec
	s_cselect_b32 s54, s11, s31
	s_cselect_b32 s55, s10, s30
	s_lshl_b32 s14, s50, 19
	s_add_u32 s16, s15, s14
	s_addc_u32 s17, s26, 0
	s_and_b64 s[36:37], s[4:5], exec
	s_cselect_b32 s56, s17, s23
	s_cselect_b32 s57, s16, s22
	s_add_i32 s60, 0, 0x10000
	v_add_u32_e32 v198, s60, v196
	s_add_i32 s62, 0, 0x14000
	v_add_u32_e32 v199, s62, v196
	ds_read_b128 v[160:163], v198
	ds_read_b128 v[152:155], v198 offset:1024
	ds_read_b128 v[156:159], v198 offset:2048
	ds_read_b128 v[148:151], v198 offset:3072
	ds_read_b128 v[144:147], v199
	ds_read_b128 v[136:139], v199 offset:1024
	ds_read_b128 v[140:143], v199 offset:2048
	ds_read_b128 v[132:135], v199 offset:3072
	s_add_u32 s36, s30, 0x40080
	s_addc_u32 s37, s31, 0
	s_add_i32 s58, s41, 0xc000
	v_lshl_add_u64 v[174:175], s[36:37], 0, v[168:169]
	s_mov_b32 m0, s58
	s_add_i32 s59, s41, 0xe000
	ds_read_b128 v[178:181], v197
	ds_read_b128 v[182:185], v197 offset:1024
	ds_read_b128 v[190:193], v197 offset:2048
	ds_read_b128 v[200:203], v197 offset:3072
	ds_read_b128 v[204:207], v197 offset:4096
	ds_read_b128 v[208:211], v197 offset:5120
	ds_read_b128 v[212:215], v197 offset:6144
	ds_read_b128 v[216:219], v197 offset:7168
	global_load_lds_dwordx4 v[174:175], off
	v_lshl_add_u64 v[174:175], s[36:37], 0, v[166:167]
	s_mov_b32 m0, s59
	s_nop 0
	global_load_lds_dwordx4 v[174:175], off
	s_waitcnt vmcnt(8)
	s_waitcnt lgkmcnt(0)
	s_barrier
	v_mfma_f32_16x16x32_bf16 v[128:131], v[160:163], v[178:181], 0
	s_setprio 1
	v_mfma_f32_16x16x32_bf16 v[124:127], v[156:159], v[178:181], 0
	v_mfma_f32_16x16x32_bf16 v[116:119], v[156:159], v[190:193], 0
	v_mfma_f32_16x16x32_bf16 v[120:123], v[160:163], v[190:193], 0
	v_mfma_f32_16x16x32_bf16 v[112:115], v[160:163], v[204:207], 0
	v_mfma_f32_16x16x32_bf16 v[108:111], v[156:159], v[204:207], 0
	v_mfma_f32_16x16x32_bf16 v[100:103], v[156:159], v[212:215], 0
	v_mfma_f32_16x16x32_bf16 v[104:107], v[160:163], v[212:215], 0
	s_nop 0
	v_mfma_f32_16x16x32_bf16 v[128:131], v[152:155], v[182:185], v[128:131]
	v_mfma_f32_16x16x32_bf16 v[124:127], v[148:151], v[182:185], v[124:127]
	v_mfma_f32_16x16x32_bf16 v[116:119], v[148:151], v[200:203], v[116:119]
	v_mfma_f32_16x16x32_bf16 v[120:123], v[152:155], v[200:203], v[120:123]
	v_mfma_f32_16x16x32_bf16 v[112:115], v[152:155], v[208:211], v[112:115]
	v_mfma_f32_16x16x32_bf16 v[108:111], v[148:151], v[208:211], v[108:111]
	v_mfma_f32_16x16x32_bf16 v[100:103], v[148:151], v[216:219], v[100:103]
	v_mfma_f32_16x16x32_bf16 v[104:107], v[152:155], v[216:219], v[104:107]
	v_mfma_f32_16x16x32_bf16 v[96:99], v[144:147], v[178:181], 0
	v_mfma_f32_16x16x32_bf16 v[92:95], v[140:143], v[178:181], 0
	v_mfma_f32_16x16x32_bf16 v[84:87], v[140:143], v[190:193], 0
	v_mfma_f32_16x16x32_bf16 v[88:91], v[144:147], v[190:193], 0
	v_mfma_f32_16x16x32_bf16 v[80:83], v[144:147], v[204:207], 0
	v_mfma_f32_16x16x32_bf16 v[76:79], v[140:143], v[204:207], 0
	v_mfma_f32_16x16x32_bf16 v[68:71], v[140:143], v[212:215], 0
	v_mfma_f32_16x16x32_bf16 v[72:75], v[144:147], v[212:215], 0
	s_nop 0
	v_mfma_f32_16x16x32_bf16 v[96:99], v[136:139], v[182:185], v[96:99]
	v_mfma_f32_16x16x32_bf16 v[92:95], v[132:135], v[182:185], v[92:95]
	v_mfma_f32_16x16x32_bf16 v[84:87], v[132:135], v[200:203], v[84:87]
	v_mfma_f32_16x16x32_bf16 v[88:91], v[136:139], v[200:203], v[88:91]
	v_mfma_f32_16x16x32_bf16 v[80:83], v[136:139], v[208:211], v[80:83]
	v_mfma_f32_16x16x32_bf16 v[76:79], v[132:135], v[208:211], v[76:79]
	v_mfma_f32_16x16x32_bf16 v[68:71], v[132:135], v[216:219], v[68:71]
	s_barrier
	v_mfma_f32_16x16x32_bf16 v[72:75], v[136:139], v[216:219], v[72:75]
	s_setprio 0
	v_lshl_add_u64 v[174:175], s[22:23], 0, v[34:35]
	s_add_i32 s60, s60, s40
	v_lshl_add_u64 v[190:191], v[174:175], 0, s[28:29]
	s_mov_b32 m0, s60
	s_add_i32 s61, s60, 0x2000
	ds_read_b128 v[178:181], v197 offset:16384
	ds_read_b128 v[182:185], v197 offset:17408
	ds_read_b128 v[200:203], v197 offset:18432
	ds_read_b128 v[204:207], v197 offset:19456
	ds_read_b128 v[208:211], v197 offset:20480
	ds_read_b128 v[212:215], v197 offset:21504
	ds_read_b128 v[216:219], v197 offset:22528
	ds_read_b128 v[222:225], v197 offset:23552
	global_load_lds_dwordx4 v[190:191], off
	v_lshl_add_u64 v[190:191], s[22:23], 0, v[164:165]
	s_add_u32 s36, s22, 0x40100
	v_lshl_add_u64 v[192:193], v[190:191], 0, s[28:29]
	s_mov_b32 m0, s61
	s_addc_u32 s37, s23, 0
	s_add_i32 s62, s62, s40
	global_load_lds_dwordx4 v[192:193], off
	v_lshl_add_u64 v[192:193], s[36:37], 0, v[34:35]
	s_mov_b32 m0, s62
	s_add_i32 s63, s62, 0x2000
	global_load_lds_dwordx4 v[192:193], off
	v_lshl_add_u64 v[192:193], s[36:37], 0, v[164:165]
	s_mov_b32 m0, s63
	s_nop 0
	global_load_lds_dwordx4 v[192:193], off
	v_lshl_add_u64 v[192:193], s[30:31], 0, v[168:169]
	v_lshl_add_u64 v[194:195], v[192:193], 0, s[28:29]
	s_mov_b32 m0, s41
	s_nop 0
	global_load_lds_dwordx4 v[194:195], off
	v_lshl_add_u64 v[194:195], s[30:31], 0, v[166:167]
	v_lshl_add_u64 v[226:227], v[194:195], 0, s[28:29]
	s_mov_b32 m0, s42
	s_nop 0
	global_load_lds_dwordx4 v[226:227], off
	s_waitcnt vmcnt(8)
	s_waitcnt lgkmcnt(0)
	s_barrier
	v_mfma_f32_16x16x32_bf16 v[64:67], v[160:163], v[178:181], 0
	s_setprio 1
	v_mfma_f32_16x16x32_bf16 v[60:63], v[156:159], v[178:181], 0
	v_mfma_f32_16x16x32_bf16 v[52:55], v[156:159], v[200:203], 0
	v_mfma_f32_16x16x32_bf16 v[56:59], v[160:163], v[200:203], 0
	v_mfma_f32_16x16x32_bf16 v[48:51], v[160:163], v[208:211], 0
	v_mfma_f32_16x16x32_bf16 v[44:47], v[156:159], v[208:211], 0
	v_mfma_f32_16x16x32_bf16 v[36:39], v[156:159], v[216:219], 0
	v_mfma_f32_16x16x32_bf16 v[40:43], v[160:163], v[216:219], 0
	s_nop 0
	v_mfma_f32_16x16x32_bf16 v[64:67], v[152:155], v[182:185], v[64:67]
	v_mfma_f32_16x16x32_bf16 v[60:63], v[148:151], v[182:185], v[60:63]
	v_mfma_f32_16x16x32_bf16 v[52:55], v[148:151], v[204:207], v[52:55]
	v_mfma_f32_16x16x32_bf16 v[56:59], v[152:155], v[204:207], v[56:59]
	v_mfma_f32_16x16x32_bf16 v[48:51], v[152:155], v[212:215], v[48:51]
	v_mfma_f32_16x16x32_bf16 v[44:47], v[148:151], v[212:215], v[44:47]
	v_mfma_f32_16x16x32_bf16 v[36:39], v[148:151], v[222:225], v[36:39]
	v_mfma_f32_16x16x32_bf16 v[40:43], v[152:155], v[222:225], v[40:43]
	v_mfma_f32_16x16x32_bf16 v[30:33], v[144:147], v[178:181], 0
	v_mfma_f32_16x16x32_bf16 v[26:29], v[140:143], v[178:181], 0
	v_mfma_f32_16x16x32_bf16 v[18:21], v[140:143], v[200:203], 0
	v_mfma_f32_16x16x32_bf16 v[22:25], v[144:147], v[200:203], 0
	v_mfma_f32_16x16x32_bf16 v[14:17], v[144:147], v[208:211], 0
	v_mfma_f32_16x16x32_bf16 v[10:13], v[140:143], v[208:211], 0
	v_mfma_f32_16x16x32_bf16 v[2:5], v[140:143], v[216:219], 0
	v_mfma_f32_16x16x32_bf16 v[6:9], v[144:147], v[216:219], 0
	s_nop 0
	v_mfma_f32_16x16x32_bf16 v[30:33], v[136:139], v[182:185], v[30:33]
	v_mfma_f32_16x16x32_bf16 v[26:29], v[132:135], v[182:185], v[26:29]
	v_mfma_f32_16x16x32_bf16 v[18:21], v[132:135], v[204:207], v[18:21]
	v_mfma_f32_16x16x32_bf16 v[22:25], v[136:139], v[204:207], v[22:25]
	v_mfma_f32_16x16x32_bf16 v[14:17], v[136:139], v[212:215], v[14:17]
	v_mfma_f32_16x16x32_bf16 v[10:13], v[132:135], v[212:215], v[10:13]
	v_mfma_f32_16x16x32_bf16 v[2:5], v[132:135], v[222:225], v[2:5]
	s_barrier
	v_mfma_f32_16x16x32_bf16 v[6:9], v[136:139], v[222:225], v[6:9]
	s_setprio 0
	s_add_i32 s64, 0, 0x18000
	s_add_i32 s66, 0, 0x1c000
	v_add_u32_e32 v132, s64, v196
	v_add_u32_e32 v133, s66, v196
	ds_read_b128 v[134:137], v132
	ds_read_b128 v[138:141], v132 offset:1024
	ds_read_b128 v[142:145], v132 offset:2048
	ds_read_b128 v[146:149], v132 offset:3072
	ds_read_b128 v[150:153], v133
	ds_read_b128 v[154:157], v133 offset:1024
	ds_read_b128 v[158:161], v133 offset:2048
	ds_read_b128 v[178:181], v133 offset:3072
	s_add_u32 s36, s30, 0x40100
	s_addc_u32 s37, s31, 0
	s_mov_b32 m0, s43
	v_lshl_add_u64 v[162:163], s[36:37], 0, v[168:169]
	ds_read_b128 v[182:185], v197 offset:32768
	ds_read_b128 v[200:203], v197 offset:33792
	ds_read_b128 v[204:207], v197 offset:34816
	ds_read_b128 v[208:211], v197 offset:35840
	ds_read_b128 v[212:215], v197 offset:36864
	ds_read_b128 v[216:219], v197 offset:37888
	ds_read_b128 v[222:225], v197 offset:38912
	ds_read_b128 v[226:229], v197 offset:39936
	global_load_lds_dwordx4 v[162:163], off
	v_lshl_add_u64 v[162:163], s[36:37], 0, v[166:167]
	s_mov_b32 m0, s44
	s_nop 0
	global_load_lds_dwordx4 v[162:163], off
	s_waitcnt vmcnt(8)
	s_waitcnt lgkmcnt(0)
	s_barrier
	v_mfma_f32_16x16x32_bf16 v[128:131], v[134:137], v[182:185], v[128:131]
	s_setprio 1
	v_mfma_f32_16x16x32_bf16 v[124:127], v[142:145], v[182:185], v[124:127]
	v_mfma_f32_16x16x32_bf16 v[116:119], v[142:145], v[204:207], v[116:119]
	v_mfma_f32_16x16x32_bf16 v[120:123], v[134:137], v[204:207], v[120:123]
	v_mfma_f32_16x16x32_bf16 v[112:115], v[134:137], v[212:215], v[112:115]
	v_mfma_f32_16x16x32_bf16 v[108:111], v[142:145], v[212:215], v[108:111]
	v_mfma_f32_16x16x32_bf16 v[100:103], v[142:145], v[222:225], v[100:103]
	v_mfma_f32_16x16x32_bf16 v[104:107], v[134:137], v[222:225], v[104:107]
	v_mfma_f32_16x16x32_bf16 v[128:131], v[138:141], v[200:203], v[128:131]
	v_mfma_f32_16x16x32_bf16 v[124:127], v[146:149], v[200:203], v[124:127]
	v_mfma_f32_16x16x32_bf16 v[116:119], v[146:149], v[208:211], v[116:119]
	v_mfma_f32_16x16x32_bf16 v[120:123], v[138:141], v[208:211], v[120:123]
	v_mfma_f32_16x16x32_bf16 v[112:115], v[138:141], v[216:219], v[112:115]
	v_mfma_f32_16x16x32_bf16 v[108:111], v[146:149], v[216:219], v[108:111]
	v_mfma_f32_16x16x32_bf16 v[100:103], v[146:149], v[226:229], v[100:103]
	v_mfma_f32_16x16x32_bf16 v[104:107], v[138:141], v[226:229], v[104:107]
	v_mfma_f32_16x16x32_bf16 v[96:99], v[150:153], v[182:185], v[96:99]
	v_mfma_f32_16x16x32_bf16 v[92:95], v[158:161], v[182:185], v[92:95]
	v_mfma_f32_16x16x32_bf16 v[84:87], v[158:161], v[204:207], v[84:87]
	v_mfma_f32_16x16x32_bf16 v[88:91], v[150:153], v[204:207], v[88:91]
	v_mfma_f32_16x16x32_bf16 v[80:83], v[150:153], v[212:215], v[80:83]
	v_mfma_f32_16x16x32_bf16 v[76:79], v[158:161], v[212:215], v[76:79]
	v_mfma_f32_16x16x32_bf16 v[68:71], v[158:161], v[222:225], v[68:71]
	v_mfma_f32_16x16x32_bf16 v[72:75], v[150:153], v[222:225], v[72:75]
	v_mfma_f32_16x16x32_bf16 v[96:99], v[154:157], v[200:203], v[96:99]
	v_mfma_f32_16x16x32_bf16 v[92:95], v[178:181], v[200:203], v[92:95]
	v_mfma_f32_16x16x32_bf16 v[84:87], v[178:181], v[208:211], v[84:87]
	v_mfma_f32_16x16x32_bf16 v[88:91], v[154:157], v[208:211], v[88:91]
	v_mfma_f32_16x16x32_bf16 v[80:83], v[154:157], v[216:219], v[80:83]
	v_mfma_f32_16x16x32_bf16 v[76:79], v[178:181], v[216:219], v[76:79]
	v_mfma_f32_16x16x32_bf16 v[68:71], v[178:181], v[226:229], v[68:71]
	s_barrier
	v_mfma_f32_16x16x32_bf16 v[72:75], v[154:157], v[226:229], v[72:75]
	s_setprio 0
	s_add_i32 s64, s64, s40
	s_mov_b64 s[24:25], 0x180
	s_add_i32 s65, s64, 0x2000
	v_lshl_add_u64 v[162:163], v[174:175], 0, s[24:25]
	s_mov_b32 m0, s64
	s_add_u32 s36, s22, 0x40180
	ds_read_b128 v[182:185], v197 offset:49152
	ds_read_b128 v[200:203], v197 offset:50176
	ds_read_b128 v[204:207], v197 offset:51200
	ds_read_b128 v[208:211], v197 offset:52224
	ds_read_b128 v[212:215], v197 offset:53248
	ds_read_b128 v[216:219], v197 offset:54272
	ds_read_b128 v[222:225], v197 offset:55296
	ds_read_b128 v[226:229], v197 offset:56320
	global_load_lds_dwordx4 v[162:163], off
	v_lshl_add_u64 v[162:163], v[190:191], 0, s[24:25]
	s_mov_b32 m0, s65
	s_addc_u32 s37, s23, 0
	s_add_i32 s66, s66, s40
	global_load_lds_dwordx4 v[162:163], off
	v_lshl_add_u64 v[162:163], s[36:37], 0, v[34:35]
	s_mov_b32 m0, s66
	s_add_i32 s67, s66, 0x2000
	global_load_lds_dwordx4 v[162:163], off
	v_lshl_add_u64 v[162:163], s[36:37], 0, v[164:165]
	s_mov_b32 m0, s67
	s_nop 0
	global_load_lds_dwordx4 v[162:163], off
	v_lshl_add_u64 v[162:163], v[192:193], 0, s[24:25]
	s_mov_b32 m0, s47
	s_nop 0
	global_load_lds_dwordx4 v[162:163], off
	v_lshl_add_u64 v[162:163], v[194:195], 0, s[24:25]
	s_mov_b32 m0, s48
	s_nop 0
	global_load_lds_dwordx4 v[162:163], off
	s_waitcnt vmcnt(8)
	s_waitcnt lgkmcnt(0)
	s_barrier
	v_mfma_f32_16x16x32_bf16 v[64:67], v[134:137], v[182:185], v[64:67]
	s_setprio 1
	v_mfma_f32_16x16x32_bf16 v[60:63], v[142:145], v[182:185], v[60:63]
	v_mfma_f32_16x16x32_bf16 v[52:55], v[142:145], v[204:207], v[52:55]
	v_mfma_f32_16x16x32_bf16 v[56:59], v[134:137], v[204:207], v[56:59]
	v_mfma_f32_16x16x32_bf16 v[48:51], v[134:137], v[212:215], v[48:51]
	v_mfma_f32_16x16x32_bf16 v[44:47], v[142:145], v[212:215], v[44:47]
	v_mfma_f32_16x16x32_bf16 v[36:39], v[142:145], v[222:225], v[36:39]
	v_mfma_f32_16x16x32_bf16 v[40:43], v[134:137], v[222:225], v[40:43]
	v_mfma_f32_16x16x32_bf16 v[64:67], v[138:141], v[200:203], v[64:67]
	v_mfma_f32_16x16x32_bf16 v[60:63], v[146:149], v[200:203], v[60:63]
	v_mfma_f32_16x16x32_bf16 v[52:55], v[146:149], v[208:211], v[52:55]
	v_mfma_f32_16x16x32_bf16 v[56:59], v[138:141], v[208:211], v[56:59]
	v_mfma_f32_16x16x32_bf16 v[48:51], v[138:141], v[216:219], v[48:51]
	v_mfma_f32_16x16x32_bf16 v[44:47], v[146:149], v[216:219], v[44:47]
	v_mfma_f32_16x16x32_bf16 v[36:39], v[146:149], v[226:229], v[36:39]
	v_mfma_f32_16x16x32_bf16 v[40:43], v[138:141], v[226:229], v[40:43]
	v_mfma_f32_16x16x32_bf16 v[30:33], v[150:153], v[182:185], v[30:33]
	v_mfma_f32_16x16x32_bf16 v[26:29], v[158:161], v[182:185], v[26:29]
	v_mfma_f32_16x16x32_bf16 v[18:21], v[158:161], v[204:207], v[18:21]
	v_mfma_f32_16x16x32_bf16 v[22:25], v[150:153], v[204:207], v[22:25]
	v_mfma_f32_16x16x32_bf16 v[14:17], v[150:153], v[212:215], v[14:17]
	v_mfma_f32_16x16x32_bf16 v[10:13], v[158:161], v[212:215], v[10:13]
	v_mfma_f32_16x16x32_bf16 v[2:5], v[158:161], v[222:225], v[2:5]
	v_mfma_f32_16x16x32_bf16 v[6:9], v[150:153], v[222:225], v[6:9]
	v_mfma_f32_16x16x32_bf16 v[30:33], v[154:157], v[200:203], v[30:33]
	v_mfma_f32_16x16x32_bf16 v[26:29], v[178:181], v[200:203], v[26:29]
	v_mfma_f32_16x16x32_bf16 v[18:21], v[178:181], v[208:211], v[18:21]
	v_mfma_f32_16x16x32_bf16 v[22:25], v[154:157], v[208:211], v[22:25]
	v_mfma_f32_16x16x32_bf16 v[14:17], v[154:157], v[216:219], v[14:17]
	v_mfma_f32_16x16x32_bf16 v[10:13], v[178:181], v[216:219], v[10:13]
	v_mfma_f32_16x16x32_bf16 v[2:5], v[178:181], v[226:229], v[2:5]
	s_barrier
	v_mfma_f32_16x16x32_bf16 v[6:9], v[154:157], v[226:229], v[6:9]
	s_setprio 0
	s_add_u32 s30, s30, 0x40180
	s_addc_u32 s31, s31, 0
	s_add_u32 s68, s22, 0x200
	s_addc_u32 s69, s23, 0
	s_mov_b32 s70, 0
.LBB0_287:
	ds_read_b128 v[134:137], v198
	ds_read_b128 v[138:141], v198 offset:1024
	ds_read_b128 v[142:145], v198 offset:2048
	ds_read_b128 v[146:149], v198 offset:3072
	ds_read_b128 v[150:153], v199
	ds_read_b128 v[154:157], v199 offset:1024
	ds_read_b128 v[158:161], v199 offset:2048
	ds_read_b128 v[178:181], v199 offset:3072
	s_add_u32 s14, s30, 0xfffc0080
	s_addc_u32 s22, s31, -1
	s_cmp_eq_u32 s70, 12
	s_cselect_b32 s37, s54, s22
	s_cselect_b32 s36, s55, s14
	s_cselect_b32 s23, s56, s69
	s_cselect_b32 s22, s57, s68
	s_mov_b32 m0, s58
	v_lshl_add_u64 v[162:163], s[30:31], 0, v[170:171]
	ds_read_b128 v[182:185], v197
	ds_read_b128 v[190:193], v197 offset:1024
	ds_read_b128 v[200:203], v197 offset:2048
	ds_read_b128 v[204:207], v197 offset:3072
	ds_read_b128 v[208:211], v197 offset:4096
	ds_read_b128 v[212:215], v197 offset:5120
	ds_read_b128 v[216:219], v197 offset:6144
	ds_read_b128 v[222:225], v197 offset:7168
	global_load_lds_dwordx4 v[162:163], off
	v_lshl_add_u64 v[162:163], s[30:31], 0, v[172:173]
	s_mov_b32 m0, s59
	s_nop 0
	global_load_lds_dwordx4 v[162:163], off
	s_waitcnt vmcnt(8)
	s_waitcnt lgkmcnt(0)
	s_barrier
	v_mfma_f32_16x16x32_bf16 v[128:131], v[134:137], v[182:185], v[128:131]
	s_setprio 1
	v_mfma_f32_16x16x32_bf16 v[124:127], v[142:145], v[182:185], v[124:127]
	v_mfma_f32_16x16x32_bf16 v[116:119], v[142:145], v[200:203], v[116:119]
	v_mfma_f32_16x16x32_bf16 v[120:123], v[134:137], v[200:203], v[120:123]
	v_mfma_f32_16x16x32_bf16 v[112:115], v[134:137], v[208:211], v[112:115]
	v_mfma_f32_16x16x32_bf16 v[108:111], v[142:145], v[208:211], v[108:111]
	v_mfma_f32_16x16x32_bf16 v[100:103], v[142:145], v[216:219], v[100:103]
	v_mfma_f32_16x16x32_bf16 v[104:107], v[134:137], v[216:219], v[104:107]
	v_mfma_f32_16x16x32_bf16 v[128:131], v[138:141], v[190:193], v[128:131]
	v_mfma_f32_16x16x32_bf16 v[124:127], v[146:149], v[190:193], v[124:127]
	v_mfma_f32_16x16x32_bf16 v[116:119], v[146:149], v[204:207], v[116:119]
	v_mfma_f32_16x16x32_bf16 v[120:123], v[138:141], v[204:207], v[120:123]
	v_mfma_f32_16x16x32_bf16 v[112:115], v[138:141], v[212:215], v[112:115]
	v_mfma_f32_16x16x32_bf16 v[108:111], v[146:149], v[212:215], v[108:111]
	v_mfma_f32_16x16x32_bf16 v[100:103], v[146:149], v[222:225], v[100:103]
	v_mfma_f32_16x16x32_bf16 v[104:107], v[138:141], v[222:225], v[104:107]
	v_mfma_f32_16x16x32_bf16 v[96:99], v[150:153], v[182:185], v[96:99]
	v_mfma_f32_16x16x32_bf16 v[92:95], v[158:161], v[182:185], v[92:95]
	v_mfma_f32_16x16x32_bf16 v[84:87], v[158:161], v[200:203], v[84:87]
	v_mfma_f32_16x16x32_bf16 v[88:91], v[150:153], v[200:203], v[88:91]
	v_mfma_f32_16x16x32_bf16 v[80:83], v[150:153], v[208:211], v[80:83]
	v_mfma_f32_16x16x32_bf16 v[76:79], v[158:161], v[208:211], v[76:79]
	v_mfma_f32_16x16x32_bf16 v[68:71], v[158:161], v[216:219], v[68:71]
	v_mfma_f32_16x16x32_bf16 v[72:75], v[150:153], v[216:219], v[72:75]
	v_mfma_f32_16x16x32_bf16 v[96:99], v[154:157], v[190:193], v[96:99]
	v_mfma_f32_16x16x32_bf16 v[92:95], v[178:181], v[190:193], v[92:95]
	v_mfma_f32_16x16x32_bf16 v[84:87], v[178:181], v[204:207], v[84:87]
	v_mfma_f32_16x16x32_bf16 v[88:91], v[154:157], v[204:207], v[88:91]
	v_mfma_f32_16x16x32_bf16 v[80:83], v[154:157], v[212:215], v[80:83]
	v_mfma_f32_16x16x32_bf16 v[76:79], v[178:181], v[212:215], v[76:79]
	v_mfma_f32_16x16x32_bf16 v[68:71], v[178:181], v[222:225], v[68:71]
	s_barrier
	v_mfma_f32_16x16x32_bf16 v[72:75], v[154:157], v[222:225], v[72:75]
	s_setprio 0
	s_mov_b32 m0, s60
	v_lshl_add_u64 v[162:163], s[22:23], 0, v[34:35]
	s_add_u32 s72, s22, 0x40000
	ds_read_b128 v[182:185], v197 offset:16384
	ds_read_b128 v[190:193], v197 offset:17408
	ds_read_b128 v[200:203], v197 offset:18432
	ds_read_b128 v[204:207], v197 offset:19456
	ds_read_b128 v[208:211], v197 offset:20480
	ds_read_b128 v[212:215], v197 offset:21504
	ds_read_b128 v[216:219], v197 offset:22528
	ds_read_b128 v[222:225], v197 offset:23552
	global_load_lds_dwordx4 v[162:163], off
	v_lshl_add_u64 v[174:175], s[22:23], 0, v[164:165]
	s_mov_b32 m0, s61
	s_addc_u32 s73, s23, 0
	global_load_lds_dwordx4 v[174:175], off
	v_lshl_add_u64 v[194:195], s[72:73], 0, v[34:35]
	s_mov_b32 m0, s62
	v_lshl_add_u64 v[226:227], s[36:37], 0, v[166:167]
	global_load_lds_dwordx4 v[194:195], off
	v_lshl_add_u64 v[194:195], s[72:73], 0, v[164:165]
	s_mov_b32 m0, s63
	s_nop 0
	global_load_lds_dwordx4 v[194:195], off
	v_lshl_add_u64 v[194:195], s[36:37], 0, v[168:169]
	s_mov_b32 m0, s41
	s_nop 0
	global_load_lds_dwordx4 v[194:195], off
	s_mov_b32 m0, s42
	s_nop 0
	global_load_lds_dwordx4 v[226:227], off
	s_waitcnt vmcnt(8)
	s_waitcnt lgkmcnt(0)
	s_barrier
	v_mfma_f32_16x16x32_bf16 v[64:67], v[134:137], v[182:185], v[64:67]
	s_setprio 1
	v_mfma_f32_16x16x32_bf16 v[60:63], v[142:145], v[182:185], v[60:63]
	v_mfma_f32_16x16x32_bf16 v[52:55], v[142:145], v[200:203], v[52:55]
	v_mfma_f32_16x16x32_bf16 v[56:59], v[134:137], v[200:203], v[56:59]
	v_mfma_f32_16x16x32_bf16 v[48:51], v[134:137], v[208:211], v[48:51]
	v_mfma_f32_16x16x32_bf16 v[44:47], v[142:145], v[208:211], v[44:47]
	v_mfma_f32_16x16x32_bf16 v[36:39], v[142:145], v[216:219], v[36:39]
	v_mfma_f32_16x16x32_bf16 v[40:43], v[134:137], v[216:219], v[40:43]
	v_mfma_f32_16x16x32_bf16 v[64:67], v[138:141], v[190:193], v[64:67]
	v_mfma_f32_16x16x32_bf16 v[60:63], v[146:149], v[190:193], v[60:63]
	v_mfma_f32_16x16x32_bf16 v[52:55], v[146:149], v[204:207], v[52:55]
	v_mfma_f32_16x16x32_bf16 v[56:59], v[138:141], v[204:207], v[56:59]
	v_mfma_f32_16x16x32_bf16 v[48:51], v[138:141], v[212:215], v[48:51]
	v_mfma_f32_16x16x32_bf16 v[44:47], v[146:149], v[212:215], v[44:47]
	v_mfma_f32_16x16x32_bf16 v[36:39], v[146:149], v[222:225], v[36:39]
	v_mfma_f32_16x16x32_bf16 v[40:43], v[138:141], v[222:225], v[40:43]
	v_mfma_f32_16x16x32_bf16 v[30:33], v[150:153], v[182:185], v[30:33]
	v_mfma_f32_16x16x32_bf16 v[26:29], v[158:161], v[182:185], v[26:29]
	v_mfma_f32_16x16x32_bf16 v[18:21], v[158:161], v[200:203], v[18:21]
	v_mfma_f32_16x16x32_bf16 v[22:25], v[150:153], v[200:203], v[22:25]
	v_mfma_f32_16x16x32_bf16 v[14:17], v[150:153], v[208:211], v[14:17]
	v_mfma_f32_16x16x32_bf16 v[10:13], v[158:161], v[208:211], v[10:13]
	v_mfma_f32_16x16x32_bf16 v[2:5], v[158:161], v[216:219], v[2:5]
	v_mfma_f32_16x16x32_bf16 v[6:9], v[150:153], v[216:219], v[6:9]
	v_mfma_f32_16x16x32_bf16 v[30:33], v[154:157], v[190:193], v[30:33]
	v_mfma_f32_16x16x32_bf16 v[26:29], v[178:181], v[190:193], v[26:29]
	v_mfma_f32_16x16x32_bf16 v[18:21], v[178:181], v[204:207], v[18:21]
	v_mfma_f32_16x16x32_bf16 v[22:25], v[154:157], v[204:207], v[22:25]
	v_mfma_f32_16x16x32_bf16 v[14:17], v[154:157], v[212:215], v[14:17]
	v_mfma_f32_16x16x32_bf16 v[10:13], v[178:181], v[212:215], v[10:13]
	v_mfma_f32_16x16x32_bf16 v[2:5], v[178:181], v[222:225], v[2:5]
	s_barrier
	v_mfma_f32_16x16x32_bf16 v[6:9], v[154:157], v[222:225], v[6:9]
	s_setprio 0
	ds_read_b128 v[134:137], v132
	ds_read_b128 v[138:141], v132 offset:1024
	ds_read_b128 v[142:145], v132 offset:2048
	ds_read_b128 v[146:149], v132 offset:3072
	ds_read_b128 v[150:153], v133
	ds_read_b128 v[154:157], v133 offset:1024
	ds_read_b128 v[158:161], v133 offset:2048
	ds_read_b128 v[178:181], v133 offset:3072
	s_add_u32 s36, s36, 0x40000
	s_addc_u32 s37, s37, 0
	s_mov_b32 m0, s43
	v_lshl_add_u64 v[228:229], s[36:37], 0, v[168:169]
	ds_read_b128 v[182:185], v197 offset:32768
	ds_read_b128 v[190:193], v197 offset:33792
	ds_read_b128 v[200:203], v197 offset:34816
	ds_read_b128 v[204:207], v197 offset:35840
	ds_read_b128 v[208:211], v197 offset:36864
	ds_read_b128 v[212:215], v197 offset:37888
	ds_read_b128 v[216:219], v197 offset:38912
	ds_read_b128 v[222:225], v197 offset:39936
	global_load_lds_dwordx4 v[228:229], off
	v_lshl_add_u64 v[228:229], s[36:37], 0, v[166:167]
	s_mov_b32 m0, s44
	s_nop 0
	global_load_lds_dwordx4 v[228:229], off
	s_waitcnt vmcnt(8)
	s_waitcnt lgkmcnt(0)
	s_barrier
	v_mfma_f32_16x16x32_bf16 v[128:131], v[134:137], v[182:185], v[128:131]
	s_setprio 1
	v_mfma_f32_16x16x32_bf16 v[124:127], v[142:145], v[182:185], v[124:127]
	v_mfma_f32_16x16x32_bf16 v[116:119], v[142:145], v[200:203], v[116:119]
	v_mfma_f32_16x16x32_bf16 v[120:123], v[134:137], v[200:203], v[120:123]
	v_mfma_f32_16x16x32_bf16 v[112:115], v[134:137], v[208:211], v[112:115]
	v_mfma_f32_16x16x32_bf16 v[108:111], v[142:145], v[208:211], v[108:111]
	v_mfma_f32_16x16x32_bf16 v[100:103], v[142:145], v[216:219], v[100:103]
	v_mfma_f32_16x16x32_bf16 v[104:107], v[134:137], v[216:219], v[104:107]
	v_mfma_f32_16x16x32_bf16 v[128:131], v[138:141], v[190:193], v[128:131]
	v_mfma_f32_16x16x32_bf16 v[124:127], v[146:149], v[190:193], v[124:127]
	v_mfma_f32_16x16x32_bf16 v[116:119], v[146:149], v[204:207], v[116:119]
	v_mfma_f32_16x16x32_bf16 v[120:123], v[138:141], v[204:207], v[120:123]
	v_mfma_f32_16x16x32_bf16 v[112:115], v[138:141], v[212:215], v[112:115]
	v_mfma_f32_16x16x32_bf16 v[108:111], v[146:149], v[212:215], v[108:111]
	v_mfma_f32_16x16x32_bf16 v[100:103], v[146:149], v[222:225], v[100:103]
	v_mfma_f32_16x16x32_bf16 v[104:107], v[138:141], v[222:225], v[104:107]
	v_mfma_f32_16x16x32_bf16 v[96:99], v[150:153], v[182:185], v[96:99]
	v_mfma_f32_16x16x32_bf16 v[92:95], v[158:161], v[182:185], v[92:95]
	v_mfma_f32_16x16x32_bf16 v[84:87], v[158:161], v[200:203], v[84:87]
	v_mfma_f32_16x16x32_bf16 v[88:91], v[150:153], v[200:203], v[88:91]
	v_mfma_f32_16x16x32_bf16 v[80:83], v[150:153], v[208:211], v[80:83]
	v_mfma_f32_16x16x32_bf16 v[76:79], v[158:161], v[208:211], v[76:79]
	v_mfma_f32_16x16x32_bf16 v[68:71], v[158:161], v[216:219], v[68:71]
	v_mfma_f32_16x16x32_bf16 v[72:75], v[150:153], v[216:219], v[72:75]
	v_mfma_f32_16x16x32_bf16 v[96:99], v[154:157], v[190:193], v[96:99]
	v_mfma_f32_16x16x32_bf16 v[92:95], v[178:181], v[190:193], v[92:95]
	v_mfma_f32_16x16x32_bf16 v[84:87], v[178:181], v[204:207], v[84:87]
	v_mfma_f32_16x16x32_bf16 v[88:91], v[154:157], v[204:207], v[88:91]
	v_mfma_f32_16x16x32_bf16 v[80:83], v[154:157], v[212:215], v[80:83]
	v_mfma_f32_16x16x32_bf16 v[76:79], v[178:181], v[212:215], v[76:79]
	v_mfma_f32_16x16x32_bf16 v[68:71], v[178:181], v[222:225], v[68:71]
	s_barrier
	v_mfma_f32_16x16x32_bf16 v[72:75], v[154:157], v[222:225], v[72:75]
	s_setprio 0
	s_mov_b32 m0, s64
	v_lshl_add_u64 v[162:163], v[162:163], 0, s[18:19]
	s_add_u32 s22, s22, 0x40080
	ds_read_b128 v[182:185], v197 offset:49152
	ds_read_b128 v[190:193], v197 offset:50176
	ds_read_b128 v[200:203], v197 offset:51200
	ds_read_b128 v[204:207], v197 offset:52224
	ds_read_b128 v[208:211], v197 offset:53248
	ds_read_b128 v[212:215], v197 offset:54272
	ds_read_b128 v[216:219], v197 offset:55296
	ds_read_b128 v[222:225], v197 offset:56320
	global_load_lds_dwordx4 v[162:163], off
	v_lshl_add_u64 v[162:163], v[174:175], 0, s[18:19]
	s_mov_b32 m0, s65
	s_addc_u32 s23, s23, 0
	global_load_lds_dwordx4 v[162:163], off
	v_lshl_add_u64 v[162:163], s[22:23], 0, v[34:35]
	s_mov_b32 m0, s66
	s_nop 0
	global_load_lds_dwordx4 v[162:163], off
	v_lshl_add_u64 v[162:163], s[22:23], 0, v[164:165]
	s_mov_b32 m0, s67
	s_nop 0
	global_load_lds_dwordx4 v[162:163], off
	v_lshl_add_u64 v[162:163], v[194:195], 0, s[18:19]
	s_mov_b32 m0, s47
	s_nop 0
	global_load_lds_dwordx4 v[162:163], off
	v_lshl_add_u64 v[162:163], v[226:227], 0, s[18:19]
	s_mov_b32 m0, s48
	s_nop 0
	global_load_lds_dwordx4 v[162:163], off
	s_waitcnt vmcnt(8)
	s_waitcnt lgkmcnt(0)
	s_barrier
	v_mfma_f32_16x16x32_bf16 v[64:67], v[134:137], v[182:185], v[64:67]
	s_setprio 1
	v_mfma_f32_16x16x32_bf16 v[60:63], v[142:145], v[182:185], v[60:63]
	v_mfma_f32_16x16x32_bf16 v[52:55], v[142:145], v[200:203], v[52:55]
	v_mfma_f32_16x16x32_bf16 v[56:59], v[134:137], v[200:203], v[56:59]
	v_mfma_f32_16x16x32_bf16 v[48:51], v[134:137], v[208:211], v[48:51]
	v_mfma_f32_16x16x32_bf16 v[44:47], v[142:145], v[208:211], v[44:47]
	v_mfma_f32_16x16x32_bf16 v[36:39], v[142:145], v[216:219], v[36:39]
	v_mfma_f32_16x16x32_bf16 v[40:43], v[134:137], v[216:219], v[40:43]
	v_mfma_f32_16x16x32_bf16 v[64:67], v[138:141], v[190:193], v[64:67]
	v_mfma_f32_16x16x32_bf16 v[60:63], v[146:149], v[190:193], v[60:63]
	v_mfma_f32_16x16x32_bf16 v[52:55], v[146:149], v[204:207], v[52:55]
	v_mfma_f32_16x16x32_bf16 v[56:59], v[138:141], v[204:207], v[56:59]
	v_mfma_f32_16x16x32_bf16 v[48:51], v[138:141], v[212:215], v[48:51]
	v_mfma_f32_16x16x32_bf16 v[44:47], v[146:149], v[212:215], v[44:47]
	v_mfma_f32_16x16x32_bf16 v[36:39], v[146:149], v[222:225], v[36:39]
	v_mfma_f32_16x16x32_bf16 v[40:43], v[138:141], v[222:225], v[40:43]
	v_mfma_f32_16x16x32_bf16 v[30:33], v[150:153], v[182:185], v[30:33]
	v_mfma_f32_16x16x32_bf16 v[26:29], v[158:161], v[182:185], v[26:29]
	v_mfma_f32_16x16x32_bf16 v[18:21], v[158:161], v[200:203], v[18:21]
	v_mfma_f32_16x16x32_bf16 v[22:25], v[150:153], v[200:203], v[22:25]
	v_mfma_f32_16x16x32_bf16 v[14:17], v[150:153], v[208:211], v[14:17]
	v_mfma_f32_16x16x32_bf16 v[10:13], v[158:161], v[208:211], v[10:13]
	v_mfma_f32_16x16x32_bf16 v[2:5], v[158:161], v[216:219], v[2:5]
	v_mfma_f32_16x16x32_bf16 v[6:9], v[150:153], v[216:219], v[6:9]
	v_mfma_f32_16x16x32_bf16 v[30:33], v[154:157], v[190:193], v[30:33]
	v_mfma_f32_16x16x32_bf16 v[26:29], v[178:181], v[190:193], v[26:29]
	v_mfma_f32_16x16x32_bf16 v[18:21], v[178:181], v[204:207], v[18:21]
	v_mfma_f32_16x16x32_bf16 v[22:25], v[154:157], v[204:207], v[22:25]
	v_mfma_f32_16x16x32_bf16 v[14:17], v[154:157], v[212:215], v[14:17]
	v_mfma_f32_16x16x32_bf16 v[10:13], v[178:181], v[212:215], v[10:13]
	v_mfma_f32_16x16x32_bf16 v[2:5], v[178:181], v[222:225], v[2:5]
	s_barrier
	v_mfma_f32_16x16x32_bf16 v[6:9], v[154:157], v[222:225], v[6:9]
	s_setprio 0
	s_add_i32 s70, s70, 2
	s_add_u32 s30, s30, 0x100
	s_addc_u32 s31, s31, 0
	s_add_u32 s68, s68, 0x100
	s_addc_u32 s69, s69, 0
	s_cmp_gt_u32 s70, 13
	s_cbranch_scc0 .LBB0_287
	s_and_b64 vcc, exec, s[8:9]
	s_cbranch_vccz .LBB0_290
	s_barrier

.LBB0_540:
	s_lshl_b32 s14, s55, 19
	v_readlane_b32 s16, v253, 53
	v_readlane_b32 s17, v253, 54
	s_add_u32 s16, s16, s14
	s_addc_u32 s17, s17, 0
	s_and_b64 s[22:23], s[4:5], exec
	s_cselect_b32 s58, s17, s37
	s_cselect_b32 s59, s16, s36
	s_lshl_b32 s14, s54, 19
	s_add_u32 s22, s15, s14
	s_addc_u32 s23, s26, 0
	s_and_b64 s[40:41], s[4:5], exec
	s_cselect_b32 s60, s23, s31
	s_cselect_b32 s61, s22, s30
	s_add_i32 s64, 0, 0x10000
	v_add_u32_e32 v172, s64, v222
	s_add_i32 s66, 0, 0x14000
	v_add_u32_e32 v173, s66, v222
	ds_read_b128 v[160:163], v172
	ds_read_b128 v[152:155], v172 offset:1024
	ds_read_b128 v[156:159], v172 offset:2048
	ds_read_b128 v[148:151], v172 offset:3072
	ds_read_b128 v[144:147], v173
	ds_read_b128 v[136:139], v173 offset:1024
	ds_read_b128 v[140:143], v173 offset:2048
	ds_read_b128 v[132:135], v173 offset:3072
	s_add_u32 s40, s36, 0x40080
	s_addc_u32 s41, s37, 0
	s_add_i32 s62, s43, 0xc000
	v_lshl_add_u64 v[174:175], s[40:41], 0, v[194:195]
	s_mov_b32 m0, s62
	s_add_i32 s63, s43, 0xe000
	ds_read_b128 v[164:167], v223
	ds_read_b128 v[168:171], v223 offset:1024
	ds_read_b128 v[178:181], v223 offset:2048
	ds_read_b128 v[182:185], v223 offset:3072
	ds_read_b128 v[200:203], v223 offset:4096
	ds_read_b128 v[204:207], v223 offset:5120
	ds_read_b128 v[208:211], v223 offset:6144
	ds_read_b128 v[212:215], v223 offset:7168
	global_load_lds_dwordx4 v[174:175], off
	v_lshl_add_u64 v[174:175], s[40:41], 0, v[192:193]
	s_mov_b32 m0, s63
	s_nop 0
	global_load_lds_dwordx4 v[174:175], off
	s_waitcnt vmcnt(8)
	s_waitcnt lgkmcnt(0)
	s_barrier
	v_mfma_f32_16x16x32_bf16 v[128:131], v[160:163], v[164:167], 0
	s_setprio 1
	v_mfma_f32_16x16x32_bf16 v[124:127], v[156:159], v[164:167], 0
	v_mfma_f32_16x16x32_bf16 v[116:119], v[156:159], v[178:181], 0
	v_mfma_f32_16x16x32_bf16 v[120:123], v[160:163], v[178:181], 0
	v_mfma_f32_16x16x32_bf16 v[112:115], v[160:163], v[200:203], 0
	v_mfma_f32_16x16x32_bf16 v[108:111], v[156:159], v[200:203], 0
	v_mfma_f32_16x16x32_bf16 v[100:103], v[156:159], v[208:211], 0
	v_mfma_f32_16x16x32_bf16 v[104:107], v[160:163], v[208:211], 0
	s_nop 0
	v_mfma_f32_16x16x32_bf16 v[128:131], v[152:155], v[168:171], v[128:131]
	v_mfma_f32_16x16x32_bf16 v[124:127], v[148:151], v[168:171], v[124:127]
	v_mfma_f32_16x16x32_bf16 v[116:119], v[148:151], v[182:185], v[116:119]
	v_mfma_f32_16x16x32_bf16 v[120:123], v[152:155], v[182:185], v[120:123]
	v_mfma_f32_16x16x32_bf16 v[112:115], v[152:155], v[204:207], v[112:115]
	v_mfma_f32_16x16x32_bf16 v[108:111], v[148:151], v[204:207], v[108:111]
	v_mfma_f32_16x16x32_bf16 v[100:103], v[148:151], v[212:215], v[100:103]
	v_mfma_f32_16x16x32_bf16 v[104:107], v[152:155], v[212:215], v[104:107]
	v_mfma_f32_16x16x32_bf16 v[96:99], v[144:147], v[164:167], 0
	v_mfma_f32_16x16x32_bf16 v[92:95], v[140:143], v[164:167], 0
	v_mfma_f32_16x16x32_bf16 v[84:87], v[140:143], v[178:181], 0
	v_mfma_f32_16x16x32_bf16 v[88:91], v[144:147], v[178:181], 0
	v_mfma_f32_16x16x32_bf16 v[80:83], v[144:147], v[200:203], 0
	v_mfma_f32_16x16x32_bf16 v[76:79], v[140:143], v[200:203], 0
	v_mfma_f32_16x16x32_bf16 v[68:71], v[140:143], v[208:211], 0
	v_mfma_f32_16x16x32_bf16 v[72:75], v[144:147], v[208:211], 0
	s_nop 0
	v_mfma_f32_16x16x32_bf16 v[96:99], v[136:139], v[168:171], v[96:99]
	v_mfma_f32_16x16x32_bf16 v[92:95], v[132:135], v[168:171], v[92:95]
	v_mfma_f32_16x16x32_bf16 v[84:87], v[132:135], v[182:185], v[84:87]
	v_mfma_f32_16x16x32_bf16 v[88:91], v[136:139], v[182:185], v[88:91]
	v_mfma_f32_16x16x32_bf16 v[80:83], v[136:139], v[204:207], v[80:83]
	v_mfma_f32_16x16x32_bf16 v[76:79], v[132:135], v[204:207], v[76:79]
	v_mfma_f32_16x16x32_bf16 v[68:71], v[132:135], v[212:215], v[68:71]
	s_barrier
	v_mfma_f32_16x16x32_bf16 v[72:75], v[136:139], v[212:215], v[72:75]
	s_setprio 0
	v_lshl_add_u64 v[164:165], s[30:31], 0, v[34:35]
	s_add_i32 s64, s64, s42
	v_lshl_add_u64 v[166:167], v[164:165], 0, s[28:29]
	s_mov_b32 m0, s64
	s_add_i32 s65, s64, 0x2000
	ds_read_b128 v[178:181], v223 offset:16384
	ds_read_b128 v[182:185], v223 offset:17408
	ds_read_b128 v[200:203], v223 offset:18432
	ds_read_b128 v[204:207], v223 offset:19456
	ds_read_b128 v[208:211], v223 offset:20480
	ds_read_b128 v[212:215], v223 offset:21504
	ds_read_b128 v[216:219], v223 offset:22528
	ds_read_b128 v[224:227], v223 offset:23552
	global_load_lds_dwordx4 v[166:167], off
	v_lshl_add_u64 v[166:167], s[30:31], 0, v[190:191]
	s_add_u32 s40, s30, 0x40100
	v_lshl_add_u64 v[168:169], v[166:167], 0, s[28:29]
	s_mov_b32 m0, s65
	s_addc_u32 s41, s31, 0
	s_add_i32 s66, s66, s42
	global_load_lds_dwordx4 v[168:169], off
	v_lshl_add_u64 v[168:169], s[40:41], 0, v[34:35]
	s_mov_b32 m0, s66
	s_add_i32 s67, s66, 0x2000
	global_load_lds_dwordx4 v[168:169], off
	v_lshl_add_u64 v[168:169], s[40:41], 0, v[190:191]
	s_mov_b32 m0, s67
	s_nop 0
	global_load_lds_dwordx4 v[168:169], off
	v_lshl_add_u64 v[168:169], s[36:37], 0, v[194:195]
	v_lshl_add_u64 v[170:171], v[168:169], 0, s[28:29]
	s_mov_b32 m0, s43
	s_nop 0
	global_load_lds_dwordx4 v[170:171], off
	v_lshl_add_u64 v[170:171], s[36:37], 0, v[192:193]
	v_lshl_add_u64 v[174:175], v[170:171], 0, s[28:29]
	s_mov_b32 m0, s44
	s_nop 0
	global_load_lds_dwordx4 v[174:175], off
	s_waitcnt vmcnt(8)
	s_waitcnt lgkmcnt(0)
	s_barrier
	v_mfma_f32_16x16x32_bf16 v[64:67], v[160:163], v[178:181], 0
	s_setprio 1
	v_mfma_f32_16x16x32_bf16 v[60:63], v[156:159], v[178:181], 0
	v_mfma_f32_16x16x32_bf16 v[52:55], v[156:159], v[200:203], 0
	v_mfma_f32_16x16x32_bf16 v[56:59], v[160:163], v[200:203], 0
	v_mfma_f32_16x16x32_bf16 v[48:51], v[160:163], v[208:211], 0
	v_mfma_f32_16x16x32_bf16 v[44:47], v[156:159], v[208:211], 0
	v_mfma_f32_16x16x32_bf16 v[36:39], v[156:159], v[216:219], 0
	v_mfma_f32_16x16x32_bf16 v[40:43], v[160:163], v[216:219], 0
	s_nop 0
	v_mfma_f32_16x16x32_bf16 v[64:67], v[152:155], v[182:185], v[64:67]
	v_mfma_f32_16x16x32_bf16 v[60:63], v[148:151], v[182:185], v[60:63]
	v_mfma_f32_16x16x32_bf16 v[52:55], v[148:151], v[204:207], v[52:55]
	v_mfma_f32_16x16x32_bf16 v[56:59], v[152:155], v[204:207], v[56:59]
	v_mfma_f32_16x16x32_bf16 v[48:51], v[152:155], v[212:215], v[48:51]
	v_mfma_f32_16x16x32_bf16 v[44:47], v[148:151], v[212:215], v[44:47]
	v_mfma_f32_16x16x32_bf16 v[36:39], v[148:151], v[224:227], v[36:39]
	v_mfma_f32_16x16x32_bf16 v[40:43], v[152:155], v[224:227], v[40:43]
	v_mfma_f32_16x16x32_bf16 v[30:33], v[144:147], v[178:181], 0
	v_mfma_f32_16x16x32_bf16 v[26:29], v[140:143], v[178:181], 0
	v_mfma_f32_16x16x32_bf16 v[18:21], v[140:143], v[200:203], 0
	v_mfma_f32_16x16x32_bf16 v[22:25], v[144:147], v[200:203], 0
	v_mfma_f32_16x16x32_bf16 v[14:17], v[144:147], v[208:211], 0
	v_mfma_f32_16x16x32_bf16 v[10:13], v[140:143], v[208:211], 0
	v_mfma_f32_16x16x32_bf16 v[2:5], v[140:143], v[216:219], 0
	v_mfma_f32_16x16x32_bf16 v[6:9], v[144:147], v[216:219], 0
	s_nop 0
	v_mfma_f32_16x16x32_bf16 v[30:33], v[136:139], v[182:185], v[30:33]
	v_mfma_f32_16x16x32_bf16 v[26:29], v[132:135], v[182:185], v[26:29]
	v_mfma_f32_16x16x32_bf16 v[18:21], v[132:135], v[204:207], v[18:21]
	v_mfma_f32_16x16x32_bf16 v[22:25], v[136:139], v[204:207], v[22:25]
	v_mfma_f32_16x16x32_bf16 v[14:17], v[136:139], v[212:215], v[14:17]
	v_mfma_f32_16x16x32_bf16 v[10:13], v[132:135], v[212:215], v[10:13]
	v_mfma_f32_16x16x32_bf16 v[2:5], v[132:135], v[224:227], v[2:5]
	s_barrier
	v_mfma_f32_16x16x32_bf16 v[6:9], v[136:139], v[224:227], v[6:9]
	s_setprio 0
	s_add_i32 s68, 0, 0x18000
	s_add_i32 s70, 0, 0x1c000
	v_add_u32_e32 v132, s68, v222
	v_add_u32_e32 v133, s70, v222
	ds_read_b128 v[134:137], v132
	ds_read_b128 v[138:141], v132 offset:1024
	ds_read_b128 v[142:145], v132 offset:2048
	ds_read_b128 v[146:149], v132 offset:3072
	ds_read_b128 v[150:153], v133
	ds_read_b128 v[154:157], v133 offset:1024
	ds_read_b128 v[158:161], v133 offset:2048
	ds_read_b128 v[178:181], v133 offset:3072
	s_add_u32 s40, s36, 0x40100
	s_addc_u32 s41, s37, 0
	s_mov_b32 m0, s45
	v_lshl_add_u64 v[162:163], s[40:41], 0, v[194:195]
	ds_read_b128 v[182:185], v223 offset:32768
	ds_read_b128 v[200:203], v223 offset:33792
	ds_read_b128 v[204:207], v223 offset:34816
	ds_read_b128 v[208:211], v223 offset:35840
	ds_read_b128 v[212:215], v223 offset:36864
	ds_read_b128 v[216:219], v223 offset:37888
	ds_read_b128 v[224:227], v223 offset:38912
	ds_read_b128 v[228:231], v223 offset:39936
	global_load_lds_dwordx4 v[162:163], off
	v_lshl_add_u64 v[162:163], s[40:41], 0, v[192:193]
	s_mov_b32 m0, s46
	s_nop 0
	global_load_lds_dwordx4 v[162:163], off
	s_waitcnt vmcnt(8)
	s_waitcnt lgkmcnt(0)
	s_barrier
	v_mfma_f32_16x16x32_bf16 v[128:131], v[134:137], v[182:185], v[128:131]
	s_setprio 1
	v_mfma_f32_16x16x32_bf16 v[124:127], v[142:145], v[182:185], v[124:127]
	v_mfma_f32_16x16x32_bf16 v[116:119], v[142:145], v[204:207], v[116:119]
	v_mfma_f32_16x16x32_bf16 v[120:123], v[134:137], v[204:207], v[120:123]
	v_mfma_f32_16x16x32_bf16 v[112:115], v[134:137], v[212:215], v[112:115]
	v_mfma_f32_16x16x32_bf16 v[108:111], v[142:145], v[212:215], v[108:111]
	v_mfma_f32_16x16x32_bf16 v[100:103], v[142:145], v[224:227], v[100:103]
	v_mfma_f32_16x16x32_bf16 v[104:107], v[134:137], v[224:227], v[104:107]
	v_mfma_f32_16x16x32_bf16 v[128:131], v[138:141], v[200:203], v[128:131]
	v_mfma_f32_16x16x32_bf16 v[124:127], v[146:149], v[200:203], v[124:127]
	v_mfma_f32_16x16x32_bf16 v[116:119], v[146:149], v[208:211], v[116:119]
	v_mfma_f32_16x16x32_bf16 v[120:123], v[138:141], v[208:211], v[120:123]
	v_mfma_f32_16x16x32_bf16 v[112:115], v[138:141], v[216:219], v[112:115]
	v_mfma_f32_16x16x32_bf16 v[108:111], v[146:149], v[216:219], v[108:111]
	v_mfma_f32_16x16x32_bf16 v[100:103], v[146:149], v[228:231], v[100:103]
	v_mfma_f32_16x16x32_bf16 v[104:107], v[138:141], v[228:231], v[104:107]
	v_mfma_f32_16x16x32_bf16 v[96:99], v[150:153], v[182:185], v[96:99]
	v_mfma_f32_16x16x32_bf16 v[92:95], v[158:161], v[182:185], v[92:95]
	v_mfma_f32_16x16x32_bf16 v[84:87], v[158:161], v[204:207], v[84:87]
	v_mfma_f32_16x16x32_bf16 v[88:91], v[150:153], v[204:207], v[88:91]
	v_mfma_f32_16x16x32_bf16 v[80:83], v[150:153], v[212:215], v[80:83]
	v_mfma_f32_16x16x32_bf16 v[76:79], v[158:161], v[212:215], v[76:79]
	v_mfma_f32_16x16x32_bf16 v[68:71], v[158:161], v[224:227], v[68:71]
	v_mfma_f32_16x16x32_bf16 v[72:75], v[150:153], v[224:227], v[72:75]
	v_mfma_f32_16x16x32_bf16 v[96:99], v[154:157], v[200:203], v[96:99]
	v_mfma_f32_16x16x32_bf16 v[92:95], v[178:181], v[200:203], v[92:95]
	v_mfma_f32_16x16x32_bf16 v[84:87], v[178:181], v[208:211], v[84:87]
	v_mfma_f32_16x16x32_bf16 v[88:91], v[154:157], v[208:211], v[88:91]
	v_mfma_f32_16x16x32_bf16 v[80:83], v[154:157], v[216:219], v[80:83]
	v_mfma_f32_16x16x32_bf16 v[76:79], v[178:181], v[216:219], v[76:79]
	v_mfma_f32_16x16x32_bf16 v[68:71], v[178:181], v[228:231], v[68:71]
	s_barrier
	v_mfma_f32_16x16x32_bf16 v[72:75], v[154:157], v[228:231], v[72:75]
	s_setprio 0
	s_add_i32 s68, s68, s42
	s_mov_b64 s[24:25], 0x180
	s_add_i32 s69, s68, 0x2000
	v_lshl_add_u64 v[162:163], v[164:165], 0, s[24:25]
	s_mov_b32 m0, s68
	s_add_u32 s40, s30, 0x40180
	ds_read_b128 v[182:185], v223 offset:49152
	ds_read_b128 v[200:203], v223 offset:50176
	ds_read_b128 v[204:207], v223 offset:51200
	ds_read_b128 v[208:211], v223 offset:52224
	ds_read_b128 v[212:215], v223 offset:53248
	ds_read_b128 v[216:219], v223 offset:54272
	ds_read_b128 v[224:227], v223 offset:55296
	ds_read_b128 v[228:231], v223 offset:56320
	global_load_lds_dwordx4 v[162:163], off
	v_lshl_add_u64 v[162:163], v[166:167], 0, s[24:25]
	s_mov_b32 m0, s69
	s_addc_u32 s41, s31, 0
	s_add_i32 s70, s70, s42
	global_load_lds_dwordx4 v[162:163], off
	v_lshl_add_u64 v[162:163], s[40:41], 0, v[34:35]
	s_mov_b32 m0, s70
	s_add_i32 s71, s70, 0x2000
	global_load_lds_dwordx4 v[162:163], off
	v_lshl_add_u64 v[162:163], s[40:41], 0, v[190:191]
	s_mov_b32 m0, s71
	s_nop 0
	global_load_lds_dwordx4 v[162:163], off
	v_lshl_add_u64 v[162:163], v[168:169], 0, s[24:25]
	s_mov_b32 m0, s51
	s_nop 0
	global_load_lds_dwordx4 v[162:163], off
	v_lshl_add_u64 v[162:163], v[170:171], 0, s[24:25]
	s_mov_b32 m0, s52
	s_nop 0
	global_load_lds_dwordx4 v[162:163], off
	s_waitcnt vmcnt(8)
	s_waitcnt lgkmcnt(0)
	s_barrier
	v_mfma_f32_16x16x32_bf16 v[64:67], v[134:137], v[182:185], v[64:67]
	s_setprio 1
	v_mfma_f32_16x16x32_bf16 v[60:63], v[142:145], v[182:185], v[60:63]
	v_mfma_f32_16x16x32_bf16 v[52:55], v[142:145], v[204:207], v[52:55]
	v_mfma_f32_16x16x32_bf16 v[56:59], v[134:137], v[204:207], v[56:59]
	v_mfma_f32_16x16x32_bf16 v[48:51], v[134:137], v[212:215], v[48:51]
	v_mfma_f32_16x16x32_bf16 v[44:47], v[142:145], v[212:215], v[44:47]
	v_mfma_f32_16x16x32_bf16 v[36:39], v[142:145], v[224:227], v[36:39]
	v_mfma_f32_16x16x32_bf16 v[40:43], v[134:137], v[224:227], v[40:43]
	v_mfma_f32_16x16x32_bf16 v[64:67], v[138:141], v[200:203], v[64:67]
	v_mfma_f32_16x16x32_bf16 v[60:63], v[146:149], v[200:203], v[60:63]
	v_mfma_f32_16x16x32_bf16 v[52:55], v[146:149], v[208:211], v[52:55]
	v_mfma_f32_16x16x32_bf16 v[56:59], v[138:141], v[208:211], v[56:59]
	v_mfma_f32_16x16x32_bf16 v[48:51], v[138:141], v[216:219], v[48:51]
	v_mfma_f32_16x16x32_bf16 v[44:47], v[146:149], v[216:219], v[44:47]
	v_mfma_f32_16x16x32_bf16 v[36:39], v[146:149], v[228:231], v[36:39]
	v_mfma_f32_16x16x32_bf16 v[40:43], v[138:141], v[228:231], v[40:43]
	v_mfma_f32_16x16x32_bf16 v[30:33], v[150:153], v[182:185], v[30:33]
	v_mfma_f32_16x16x32_bf16 v[26:29], v[158:161], v[182:185], v[26:29]
	v_mfma_f32_16x16x32_bf16 v[18:21], v[158:161], v[204:207], v[18:21]
	v_mfma_f32_16x16x32_bf16 v[22:25], v[150:153], v[204:207], v[22:25]
	v_mfma_f32_16x16x32_bf16 v[14:17], v[150:153], v[212:215], v[14:17]
	v_mfma_f32_16x16x32_bf16 v[10:13], v[158:161], v[212:215], v[10:13]
	v_mfma_f32_16x16x32_bf16 v[2:5], v[158:161], v[224:227], v[2:5]
	v_mfma_f32_16x16x32_bf16 v[6:9], v[150:153], v[224:227], v[6:9]
	v_mfma_f32_16x16x32_bf16 v[30:33], v[154:157], v[200:203], v[30:33]
	v_mfma_f32_16x16x32_bf16 v[26:29], v[178:181], v[200:203], v[26:29]
	v_mfma_f32_16x16x32_bf16 v[18:21], v[178:181], v[208:211], v[18:21]
	v_mfma_f32_16x16x32_bf16 v[22:25], v[154:157], v[208:211], v[22:25]
	v_mfma_f32_16x16x32_bf16 v[14:17], v[154:157], v[216:219], v[14:17]
	v_mfma_f32_16x16x32_bf16 v[10:13], v[178:181], v[216:219], v[10:13]
	v_mfma_f32_16x16x32_bf16 v[2:5], v[178:181], v[228:231], v[2:5]
	s_barrier
	v_mfma_f32_16x16x32_bf16 v[6:9], v[154:157], v[228:231], v[6:9]
	s_setprio 0
	s_add_u32 s36, s36, 0x40180
	s_addc_u32 s37, s37, 0
	s_add_u32 s72, s30, 0x200
	s_addc_u32 s73, s31, 0
	s_mov_b32 s74, 0
.LBB0_541:
	ds_read_b128 v[134:137], v172
	ds_read_b128 v[138:141], v172 offset:1024
	ds_read_b128 v[142:145], v172 offset:2048
	ds_read_b128 v[146:149], v172 offset:3072
	ds_read_b128 v[150:153], v173
	ds_read_b128 v[154:157], v173 offset:1024
	ds_read_b128 v[158:161], v173 offset:2048
	ds_read_b128 v[162:165], v173 offset:3072
	s_add_u32 s14, s36, 0xfffc0080
	s_addc_u32 s30, s37, -1
	s_cmp_eq_u32 s74, 12
	s_cselect_b32 s41, s58, s30
	s_cselect_b32 s40, s59, s14
	s_cselect_b32 s31, s60, s73
	s_cselect_b32 s30, s61, s72
	s_mov_b32 m0, s62
	v_lshl_add_u64 v[170:171], s[36:37], 0, v[196:197]
	ds_read_b128 v[166:169], v223
	ds_read_b128 v[178:181], v223 offset:1024
	ds_read_b128 v[182:185], v223 offset:2048
	ds_read_b128 v[200:203], v223 offset:3072
	ds_read_b128 v[204:207], v223 offset:4096
	ds_read_b128 v[208:211], v223 offset:5120
	ds_read_b128 v[212:215], v223 offset:6144
	ds_read_b128 v[216:219], v223 offset:7168
	global_load_lds_dwordx4 v[170:171], off
	v_lshl_add_u64 v[170:171], s[36:37], 0, v[198:199]
	s_mov_b32 m0, s63
	s_nop 0
	global_load_lds_dwordx4 v[170:171], off
	s_waitcnt vmcnt(8)
	s_waitcnt lgkmcnt(0)
	s_barrier
	v_mfma_f32_16x16x32_bf16 v[128:131], v[134:137], v[166:169], v[128:131]
	s_setprio 1
	v_mfma_f32_16x16x32_bf16 v[124:127], v[142:145], v[166:169], v[124:127]
	v_mfma_f32_16x16x32_bf16 v[116:119], v[142:145], v[182:185], v[116:119]
	v_mfma_f32_16x16x32_bf16 v[120:123], v[134:137], v[182:185], v[120:123]
	v_mfma_f32_16x16x32_bf16 v[112:115], v[134:137], v[204:207], v[112:115]
	v_mfma_f32_16x16x32_bf16 v[108:111], v[142:145], v[204:207], v[108:111]
	v_mfma_f32_16x16x32_bf16 v[100:103], v[142:145], v[212:215], v[100:103]
	v_mfma_f32_16x16x32_bf16 v[104:107], v[134:137], v[212:215], v[104:107]
	v_mfma_f32_16x16x32_bf16 v[128:131], v[138:141], v[178:181], v[128:131]
	v_mfma_f32_16x16x32_bf16 v[124:127], v[146:149], v[178:181], v[124:127]
	v_mfma_f32_16x16x32_bf16 v[116:119], v[146:149], v[200:203], v[116:119]
	v_mfma_f32_16x16x32_bf16 v[120:123], v[138:141], v[200:203], v[120:123]
	v_mfma_f32_16x16x32_bf16 v[112:115], v[138:141], v[208:211], v[112:115]
	v_mfma_f32_16x16x32_bf16 v[108:111], v[146:149], v[208:211], v[108:111]
	v_mfma_f32_16x16x32_bf16 v[100:103], v[146:149], v[216:219], v[100:103]
	v_mfma_f32_16x16x32_bf16 v[104:107], v[138:141], v[216:219], v[104:107]
	v_mfma_f32_16x16x32_bf16 v[96:99], v[150:153], v[166:169], v[96:99]
	v_mfma_f32_16x16x32_bf16 v[92:95], v[158:161], v[166:169], v[92:95]
	v_mfma_f32_16x16x32_bf16 v[84:87], v[158:161], v[182:185], v[84:87]
	v_mfma_f32_16x16x32_bf16 v[88:91], v[150:153], v[182:185], v[88:91]
	v_mfma_f32_16x16x32_bf16 v[80:83], v[150:153], v[204:207], v[80:83]
	v_mfma_f32_16x16x32_bf16 v[76:79], v[158:161], v[204:207], v[76:79]
	v_mfma_f32_16x16x32_bf16 v[68:71], v[158:161], v[212:215], v[68:71]
	v_mfma_f32_16x16x32_bf16 v[72:75], v[150:153], v[212:215], v[72:75]
	v_mfma_f32_16x16x32_bf16 v[96:99], v[154:157], v[178:181], v[96:99]
	v_mfma_f32_16x16x32_bf16 v[92:95], v[162:165], v[178:181], v[92:95]
	v_mfma_f32_16x16x32_bf16 v[84:87], v[162:165], v[200:203], v[84:87]
	v_mfma_f32_16x16x32_bf16 v[88:91], v[154:157], v[200:203], v[88:91]
	v_mfma_f32_16x16x32_bf16 v[80:83], v[154:157], v[208:211], v[80:83]
	v_mfma_f32_16x16x32_bf16 v[76:79], v[162:165], v[208:211], v[76:79]
	v_mfma_f32_16x16x32_bf16 v[68:71], v[162:165], v[216:219], v[68:71]
	s_barrier
	v_mfma_f32_16x16x32_bf16 v[72:75], v[154:157], v[216:219], v[72:75]
	s_setprio 0
	s_mov_b32 m0, s64
	v_lshl_add_u64 v[170:171], s[30:31], 0, v[34:35]
	s_add_u32 s76, s30, 0x40000
	ds_read_b128 v[166:169], v223 offset:16384
	ds_read_b128 v[178:181], v223 offset:17408
	ds_read_b128 v[182:185], v223 offset:18432
	ds_read_b128 v[200:203], v223 offset:19456
	ds_read_b128 v[204:207], v223 offset:20480
	ds_read_b128 v[208:211], v223 offset:21504
	ds_read_b128 v[212:215], v223 offset:22528
	ds_read_b128 v[216:219], v223 offset:23552
	global_load_lds_dwordx4 v[170:171], off
	v_lshl_add_u64 v[174:175], s[30:31], 0, v[190:191]
	s_mov_b32 m0, s65
	s_addc_u32 s77, s31, 0
	global_load_lds_dwordx4 v[174:175], off
	v_lshl_add_u64 v[224:225], s[76:77], 0, v[34:35]
	s_mov_b32 m0, s66
	v_lshl_add_u64 v[226:227], s[40:41], 0, v[192:193]
	global_load_lds_dwordx4 v[224:225], off
	v_lshl_add_u64 v[224:225], s[76:77], 0, v[190:191]
	s_mov_b32 m0, s67
	s_nop 0
	global_load_lds_dwordx4 v[224:225], off
	v_lshl_add_u64 v[224:225], s[40:41], 0, v[194:195]
	s_mov_b32 m0, s43
	s_nop 0
	global_load_lds_dwordx4 v[224:225], off
	s_mov_b32 m0, s44
	s_nop 0
	global_load_lds_dwordx4 v[226:227], off
	s_waitcnt vmcnt(8)
	s_waitcnt lgkmcnt(0)
	s_barrier
	v_mfma_f32_16x16x32_bf16 v[64:67], v[134:137], v[166:169], v[64:67]
	s_setprio 1
	v_mfma_f32_16x16x32_bf16 v[60:63], v[142:145], v[166:169], v[60:63]
	v_mfma_f32_16x16x32_bf16 v[52:55], v[142:145], v[182:185], v[52:55]
	v_mfma_f32_16x16x32_bf16 v[56:59], v[134:137], v[182:185], v[56:59]
	v_mfma_f32_16x16x32_bf16 v[48:51], v[134:137], v[204:207], v[48:51]
	v_mfma_f32_16x16x32_bf16 v[44:47], v[142:145], v[204:207], v[44:47]
	v_mfma_f32_16x16x32_bf16 v[36:39], v[142:145], v[212:215], v[36:39]
	v_mfma_f32_16x16x32_bf16 v[40:43], v[134:137], v[212:215], v[40:43]
	v_mfma_f32_16x16x32_bf16 v[64:67], v[138:141], v[178:181], v[64:67]
	v_mfma_f32_16x16x32_bf16 v[60:63], v[146:149], v[178:181], v[60:63]
	v_mfma_f32_16x16x32_bf16 v[52:55], v[146:149], v[200:203], v[52:55]
	v_mfma_f32_16x16x32_bf16 v[56:59], v[138:141], v[200:203], v[56:59]
	v_mfma_f32_16x16x32_bf16 v[48:51], v[138:141], v[208:211], v[48:51]
	v_mfma_f32_16x16x32_bf16 v[44:47], v[146:149], v[208:211], v[44:47]
	v_mfma_f32_16x16x32_bf16 v[36:39], v[146:149], v[216:219], v[36:39]
	v_mfma_f32_16x16x32_bf16 v[40:43], v[138:141], v[216:219], v[40:43]
	v_mfma_f32_16x16x32_bf16 v[30:33], v[150:153], v[166:169], v[30:33]
	v_mfma_f32_16x16x32_bf16 v[26:29], v[158:161], v[166:169], v[26:29]
	v_mfma_f32_16x16x32_bf16 v[18:21], v[158:161], v[182:185], v[18:21]
	v_mfma_f32_16x16x32_bf16 v[22:25], v[150:153], v[182:185], v[22:25]
	v_mfma_f32_16x16x32_bf16 v[14:17], v[150:153], v[204:207], v[14:17]
	v_mfma_f32_16x16x32_bf16 v[10:13], v[158:161], v[204:207], v[10:13]
	v_mfma_f32_16x16x32_bf16 v[2:5], v[158:161], v[212:215], v[2:5]
	v_mfma_f32_16x16x32_bf16 v[6:9], v[150:153], v[212:215], v[6:9]
	v_mfma_f32_16x16x32_bf16 v[30:33], v[154:157], v[178:181], v[30:33]
	v_mfma_f32_16x16x32_bf16 v[26:29], v[162:165], v[178:181], v[26:29]
	v_mfma_f32_16x16x32_bf16 v[18:21], v[162:165], v[200:203], v[18:21]
	v_mfma_f32_16x16x32_bf16 v[22:25], v[154:157], v[200:203], v[22:25]
	v_mfma_f32_16x16x32_bf16 v[14:17], v[154:157], v[208:211], v[14:17]
	v_mfma_f32_16x16x32_bf16 v[10:13], v[162:165], v[208:211], v[10:13]
	v_mfma_f32_16x16x32_bf16 v[2:5], v[162:165], v[216:219], v[2:5]
	s_barrier
	v_mfma_f32_16x16x32_bf16 v[6:9], v[154:157], v[216:219], v[6:9]
	s_setprio 0
	ds_read_b128 v[134:137], v132
	ds_read_b128 v[138:141], v132 offset:1024
	ds_read_b128 v[142:145], v132 offset:2048
	ds_read_b128 v[146:149], v132 offset:3072
	ds_read_b128 v[150:153], v133
	ds_read_b128 v[154:157], v133 offset:1024
	ds_read_b128 v[158:161], v133 offset:2048
	ds_read_b128 v[162:165], v133 offset:3072
	s_add_u32 s40, s40, 0x40000
	s_addc_u32 s41, s41, 0
	s_mov_b32 m0, s45
	v_lshl_add_u64 v[228:229], s[40:41], 0, v[194:195]
	ds_read_b128 v[166:169], v223 offset:32768
	ds_read_b128 v[178:181], v223 offset:33792
	ds_read_b128 v[182:185], v223 offset:34816
	ds_read_b128 v[200:203], v223 offset:35840
	ds_read_b128 v[204:207], v223 offset:36864
	ds_read_b128 v[208:211], v223 offset:37888
	ds_read_b128 v[212:215], v223 offset:38912
	ds_read_b128 v[216:219], v223 offset:39936
	global_load_lds_dwordx4 v[228:229], off
	v_lshl_add_u64 v[228:229], s[40:41], 0, v[192:193]
	s_mov_b32 m0, s46
	s_nop 0
	global_load_lds_dwordx4 v[228:229], off
	s_waitcnt vmcnt(8)
	s_waitcnt lgkmcnt(0)
	s_barrier
	v_mfma_f32_16x16x32_bf16 v[128:131], v[134:137], v[166:169], v[128:131]
	s_setprio 1
	v_mfma_f32_16x16x32_bf16 v[124:127], v[142:145], v[166:169], v[124:127]
	v_mfma_f32_16x16x32_bf16 v[116:119], v[142:145], v[182:185], v[116:119]
	v_mfma_f32_16x16x32_bf16 v[120:123], v[134:137], v[182:185], v[120:123]
	v_mfma_f32_16x16x32_bf16 v[112:115], v[134:137], v[204:207], v[112:115]
	v_mfma_f32_16x16x32_bf16 v[108:111], v[142:145], v[204:207], v[108:111]
	v_mfma_f32_16x16x32_bf16 v[100:103], v[142:145], v[212:215], v[100:103]
	v_mfma_f32_16x16x32_bf16 v[104:107], v[134:137], v[212:215], v[104:107]
	v_mfma_f32_16x16x32_bf16 v[128:131], v[138:141], v[178:181], v[128:131]
	v_mfma_f32_16x16x32_bf16 v[124:127], v[146:149], v[178:181], v[124:127]
	v_mfma_f32_16x16x32_bf16 v[116:119], v[146:149], v[200:203], v[116:119]
	v_mfma_f32_16x16x32_bf16 v[120:123], v[138:141], v[200:203], v[120:123]
	v_mfma_f32_16x16x32_bf16 v[112:115], v[138:141], v[208:211], v[112:115]
	v_mfma_f32_16x16x32_bf16 v[108:111], v[146:149], v[208:211], v[108:111]
	v_mfma_f32_16x16x32_bf16 v[100:103], v[146:149], v[216:219], v[100:103]
	v_mfma_f32_16x16x32_bf16 v[104:107], v[138:141], v[216:219], v[104:107]
	v_mfma_f32_16x16x32_bf16 v[96:99], v[150:153], v[166:169], v[96:99]
	v_mfma_f32_16x16x32_bf16 v[92:95], v[158:161], v[166:169], v[92:95]
	v_mfma_f32_16x16x32_bf16 v[84:87], v[158:161], v[182:185], v[84:87]
	v_mfma_f32_16x16x32_bf16 v[88:91], v[150:153], v[182:185], v[88:91]
	v_mfma_f32_16x16x32_bf16 v[80:83], v[150:153], v[204:207], v[80:83]
	v_mfma_f32_16x16x32_bf16 v[76:79], v[158:161], v[204:207], v[76:79]
	v_mfma_f32_16x16x32_bf16 v[68:71], v[158:161], v[212:215], v[68:71]
	v_mfma_f32_16x16x32_bf16 v[72:75], v[150:153], v[212:215], v[72:75]
	v_mfma_f32_16x16x32_bf16 v[96:99], v[154:157], v[178:181], v[96:99]
	v_mfma_f32_16x16x32_bf16 v[92:95], v[162:165], v[178:181], v[92:95]
	v_mfma_f32_16x16x32_bf16 v[84:87], v[162:165], v[200:203], v[84:87]
	v_mfma_f32_16x16x32_bf16 v[88:91], v[154:157], v[200:203], v[88:91]
	v_mfma_f32_16x16x32_bf16 v[80:83], v[154:157], v[208:211], v[80:83]
	v_mfma_f32_16x16x32_bf16 v[76:79], v[162:165], v[208:211], v[76:79]
	v_mfma_f32_16x16x32_bf16 v[68:71], v[162:165], v[216:219], v[68:71]
	s_barrier
	v_mfma_f32_16x16x32_bf16 v[72:75], v[154:157], v[216:219], v[72:75]
	s_setprio 0
	s_mov_b32 m0, s68
	v_lshl_add_u64 v[170:171], v[170:171], 0, s[18:19]
	s_add_u32 s30, s30, 0x40080
	ds_read_b128 v[166:169], v223 offset:49152
	ds_read_b128 v[178:181], v223 offset:50176
	ds_read_b128 v[182:185], v223 offset:51200
	ds_read_b128 v[200:203], v223 offset:52224
	ds_read_b128 v[204:207], v223 offset:53248
	ds_read_b128 v[208:211], v223 offset:54272
	ds_read_b128 v[212:215], v223 offset:55296
	ds_read_b128 v[216:219], v223 offset:56320
	global_load_lds_dwordx4 v[170:171], off
	v_lshl_add_u64 v[170:171], v[174:175], 0, s[18:19]
	s_mov_b32 m0, s69
	s_addc_u32 s31, s31, 0
	global_load_lds_dwordx4 v[170:171], off
	v_lshl_add_u64 v[170:171], s[30:31], 0, v[34:35]
	s_mov_b32 m0, s70
	s_nop 0
	global_load_lds_dwordx4 v[170:171], off
	v_lshl_add_u64 v[170:171], s[30:31], 0, v[190:191]
	s_mov_b32 m0, s71
	s_nop 0
	global_load_lds_dwordx4 v[170:171], off
	v_lshl_add_u64 v[170:171], v[224:225], 0, s[18:19]
	s_mov_b32 m0, s51
	s_nop 0
	global_load_lds_dwordx4 v[170:171], off
	v_lshl_add_u64 v[170:171], v[226:227], 0, s[18:19]
	s_mov_b32 m0, s52
	s_nop 0
	global_load_lds_dwordx4 v[170:171], off
	s_waitcnt vmcnt(8)
	s_waitcnt lgkmcnt(0)
	s_barrier
	v_mfma_f32_16x16x32_bf16 v[64:67], v[134:137], v[166:169], v[64:67]
	s_setprio 1
	v_mfma_f32_16x16x32_bf16 v[60:63], v[142:145], v[166:169], v[60:63]
	v_mfma_f32_16x16x32_bf16 v[52:55], v[142:145], v[182:185], v[52:55]
	v_mfma_f32_16x16x32_bf16 v[56:59], v[134:137], v[182:185], v[56:59]
	v_mfma_f32_16x16x32_bf16 v[48:51], v[134:137], v[204:207], v[48:51]
	v_mfma_f32_16x16x32_bf16 v[44:47], v[142:145], v[204:207], v[44:47]
	v_mfma_f32_16x16x32_bf16 v[36:39], v[142:145], v[212:215], v[36:39]
	v_mfma_f32_16x16x32_bf16 v[40:43], v[134:137], v[212:215], v[40:43]
	v_mfma_f32_16x16x32_bf16 v[64:67], v[138:141], v[178:181], v[64:67]
	v_mfma_f32_16x16x32_bf16 v[60:63], v[146:149], v[178:181], v[60:63]
	v_mfma_f32_16x16x32_bf16 v[52:55], v[146:149], v[200:203], v[52:55]
	v_mfma_f32_16x16x32_bf16 v[56:59], v[138:141], v[200:203], v[56:59]
	v_mfma_f32_16x16x32_bf16 v[48:51], v[138:141], v[208:211], v[48:51]
	v_mfma_f32_16x16x32_bf16 v[44:47], v[146:149], v[208:211], v[44:47]
	v_mfma_f32_16x16x32_bf16 v[36:39], v[146:149], v[216:219], v[36:39]
	v_mfma_f32_16x16x32_bf16 v[40:43], v[138:141], v[216:219], v[40:43]
	v_mfma_f32_16x16x32_bf16 v[30:33], v[150:153], v[166:169], v[30:33]
	v_mfma_f32_16x16x32_bf16 v[26:29], v[158:161], v[166:169], v[26:29]
	v_mfma_f32_16x16x32_bf16 v[18:21], v[158:161], v[182:185], v[18:21]
	v_mfma_f32_16x16x32_bf16 v[22:25], v[150:153], v[182:185], v[22:25]
	v_mfma_f32_16x16x32_bf16 v[14:17], v[150:153], v[204:207], v[14:17]
	v_mfma_f32_16x16x32_bf16 v[10:13], v[158:161], v[204:207], v[10:13]
	v_mfma_f32_16x16x32_bf16 v[2:5], v[158:161], v[212:215], v[2:5]
	v_mfma_f32_16x16x32_bf16 v[6:9], v[150:153], v[212:215], v[6:9]
	v_mfma_f32_16x16x32_bf16 v[30:33], v[154:157], v[178:181], v[30:33]
	v_mfma_f32_16x16x32_bf16 v[26:29], v[162:165], v[178:181], v[26:29]
	v_mfma_f32_16x16x32_bf16 v[18:21], v[162:165], v[200:203], v[18:21]
	v_mfma_f32_16x16x32_bf16 v[22:25], v[154:157], v[200:203], v[22:25]
	v_mfma_f32_16x16x32_bf16 v[14:17], v[154:157], v[208:211], v[14:17]
	v_mfma_f32_16x16x32_bf16 v[10:13], v[162:165], v[208:211], v[10:13]
	v_mfma_f32_16x16x32_bf16 v[2:5], v[162:165], v[216:219], v[2:5]
	s_barrier
	v_mfma_f32_16x16x32_bf16 v[6:9], v[154:157], v[216:219], v[6:9]
	s_setprio 0
	s_add_i32 s74, s74, 2
	s_add_u32 s36, s36, 0x100
	s_addc_u32 s37, s37, 0
	s_add_u32 s72, s72, 0x100
	s_addc_u32 s73, s73, 0
	s_cmp_gt_u32 s74, 13
	s_cbranch_scc0 .LBB0_541
	v_readlane_b32 s74, v255, 3
	s_and_b64 vcc, exec, s[10:11]
	v_readlane_b32 s75, v255, 4
	s_mov_b32 s58, 0x19b00000
	v_readlane_b32 s59, v255, 10
	s_mov_b32 s60, 0xff61b1e6
	s_mov_b64 s[62:63], 0x800
	s_mov_b32 s64, 0x3b000000
	s_cbranch_vccz .LBB0_544
	s_barrier

.LBB0_819:
	s_add_u32 s81, s30, 0x200
	s_addc_u32 s82, s31, 0
	s_add_i32 s55, 0, 0x14000
	s_add_i32 s52, 0, 0x10000
	v_add_u32_e32 v199, s55, v167
	v_add_u32_e32 v200, s52, v167
	ds_read_b128 v[10:13], v199
	ds_read_b128 v[14:17], v199 offset:1024
	ds_read_b128 v[2:5], v199 offset:2048
	ds_read_b128 v[6:9], v199 offset:3072
	ds_read_b128 v[22:25], v200 offset:3072
	ds_read_b128 v[18:21], v200 offset:2048
	ds_read_b128 v[30:33], v200 offset:1024
	ds_read_b128 v[26:29], v200
	s_lshl_b32 s14, s80, 10
	s_add_i32 s83, s14, 0
	s_add_i32 s83, s83, 0x20400
	v_mov_b32_e32 v191, v35
	v_mov_b32_e32 v175, v35
	s_add_i32 s84, s69, 0xc000
	v_readlane_b32 s26, v253, 28
	s_mov_b32 m0, s84
	v_readlane_b32 s27, v253, 29
	s_add_i32 s53, s69, 0xe000
	ds_read_b128 v[202:205], v169
	ds_read_b128 v[206:209], v169 offset:1024
	ds_read_b128 v[222:225], v169 offset:2048
	ds_read_b128 v[226:229], v169 offset:3072
	ds_read_b128 v[230:233], v169 offset:4096
	ds_read_b128 v[234:237], v169 offset:5120
	ds_read_b128 v[238:241], v169 offset:6144
	ds_read_b128 v[242:245], v169 offset:7168
	global_load_lds_dwordx4 v190, s[26:27]
	s_mov_b32 m0, s53
	s_nop 0
	global_load_lds_dwordx4 v174, s[26:27]
	s_waitcnt vmcnt(8)
	s_waitcnt lgkmcnt(0)
	s_barrier
	v_mfma_f32_16x16x128_f8f6f4 v[160:163], v[26:33], v[202:209], 0
	s_setprio 1
	v_mfma_f32_16x16x128_f8f6f4 v[156:159], v[18:25], v[202:209], 0
	v_mfma_f32_16x16x128_f8f6f4 v[148:151], v[18:25], v[222:229], 0
	v_mfma_f32_16x16x128_f8f6f4 v[152:155], v[26:33], v[222:229], 0
	v_mfma_f32_16x16x128_f8f6f4 v[144:147], v[26:33], v[230:237], 0
	v_mfma_f32_16x16x128_f8f6f4 v[140:143], v[18:25], v[230:237], 0
	v_mfma_f32_16x16x128_f8f6f4 v[132:135], v[18:25], v[238:245], 0
	v_mfma_f32_16x16x128_f8f6f4 v[136:139], v[26:33], v[238:245], 0
	v_mfma_f32_16x16x128_f8f6f4 v[128:131], v[10:17], v[202:209], 0
	v_mfma_f32_16x16x128_f8f6f4 v[124:127], v[2:9], v[202:209], 0
	v_mfma_f32_16x16x128_f8f6f4 v[116:119], v[2:9], v[222:229], 0
	v_mfma_f32_16x16x128_f8f6f4 v[120:123], v[10:17], v[222:229], 0
	v_mfma_f32_16x16x128_f8f6f4 v[112:115], v[10:17], v[230:237], 0
	v_mfma_f32_16x16x128_f8f6f4 v[108:111], v[2:9], v[230:237], 0
	v_mfma_f32_16x16x128_f8f6f4 v[100:103], v[2:9], v[238:245], 0
	s_barrier
	v_mfma_f32_16x16x128_f8f6f4 v[104:107], v[10:17], v[238:245], 0
	s_setprio 0
	s_add_i32 s52, s52, s68
	v_lshl_add_u64 v[194:195], s[30:31], 0, v[170:171]
	s_add_i32 s85, s52, 0x2000
	v_lshl_add_u64 v[178:179], v[194:195], 0, s[28:29]
	s_mov_b32 m0, s52
	v_lshl_add_u64 v[196:197], s[30:31], 0, v[172:173]
	s_add_u32 s36, s30, 0x20100
	ds_read_b128 v[202:205], v169 offset:16384
	ds_read_b128 v[206:209], v169 offset:17408
	ds_read_b128 v[222:225], v169 offset:18432
	ds_read_b128 v[226:229], v169 offset:19456
	ds_read_b128 v[230:233], v169 offset:20480
	ds_read_b128 v[234:237], v169 offset:21504
	ds_read_b128 v[238:241], v169 offset:22528
	ds_read_b128 v[242:245], v169 offset:23552
	global_load_lds_dwordx4 v[178:179], off
	v_lshl_add_u64 v[178:179], v[196:197], 0, s[28:29]
	s_mov_b32 m0, s85
	s_addc_u32 s37, s31, 0
	s_add_i32 s55, s55, s68
	global_load_lds_dwordx4 v[178:179], off
	v_lshl_add_u64 v[178:179], s[36:37], 0, v[170:171]
	s_mov_b32 m0, s55
	s_add_i32 s65, s55, 0x2000
	global_load_lds_dwordx4 v[178:179], off
	v_lshl_add_u64 v[178:179], s[36:37], 0, v[172:173]
	s_mov_b32 m0, s65
	v_readlane_b32 s26, v253, 37
	global_load_lds_dwordx4 v[178:179], off
	s_mov_b32 m0, s69
	v_readlane_b32 s27, v253, 38
	s_nop 4
	global_load_lds_dwordx4 v34, s[26:27]
	s_mov_b32 m0, s70
	s_nop 0
	global_load_lds_dwordx4 v192, s[26:27]
	s_waitcnt vmcnt(8)
	s_waitcnt lgkmcnt(0)
	s_barrier
	v_mfma_f32_16x16x128_f8f6f4 v[96:99], v[26:33], v[202:209], 0
	s_setprio 1
	v_mfma_f32_16x16x128_f8f6f4 v[92:95], v[18:25], v[202:209], 0
	v_mfma_f32_16x16x128_f8f6f4 v[84:87], v[18:25], v[222:229], 0
	v_mfma_f32_16x16x128_f8f6f4 v[88:91], v[26:33], v[222:229], 0
	v_mfma_f32_16x16x128_f8f6f4 v[80:83], v[26:33], v[230:237], 0
	v_mfma_f32_16x16x128_f8f6f4 v[76:79], v[18:25], v[230:237], 0
	v_mfma_f32_16x16x128_f8f6f4 v[68:71], v[18:25], v[238:245], 0
	v_mfma_f32_16x16x128_f8f6f4 v[72:75], v[26:33], v[238:245], 0
	v_mfma_f32_16x16x128_f8f6f4 v[64:67], v[10:17], v[202:209], 0
	v_mfma_f32_16x16x128_f8f6f4 v[60:63], v[2:9], v[202:209], 0
	v_mfma_f32_16x16x128_f8f6f4 v[52:55], v[2:9], v[222:229], 0
	v_mfma_f32_16x16x128_f8f6f4 v[56:59], v[10:17], v[222:229], 0
	v_mfma_f32_16x16x128_f8f6f4 v[48:51], v[10:17], v[230:237], 0
	v_mfma_f32_16x16x128_f8f6f4 v[44:47], v[2:9], v[230:237], 0
	v_mfma_f32_16x16x128_f8f6f4 v[36:39], v[2:9], v[238:245], 0
	s_barrier
	v_mfma_f32_16x16x128_f8f6f4 v[40:43], v[10:17], v[238:245], 0
	s_setprio 0
	s_add_i32 s54, 0, 0x18000
	s_add_i32 s51, 0, 0x1c000
	v_add_u32_e32 v201, s54, v167
	v_add_u32_e32 v202, s51, v167
	ds_read_b128 v[26:29], v201
	ds_read_b128 v[30:33], v201 offset:1024
	ds_read_b128 v[18:21], v201 offset:2048
	ds_read_b128 v[22:25], v201 offset:3072
	ds_read_b128 v[10:13], v202
	ds_read_b128 v[14:17], v202 offset:1024
	ds_read_b128 v[2:5], v202 offset:2048
	ds_read_b128 v[6:9], v202 offset:3072
	s_mov_b32 m0, s71
	ds_read_b128 v[204:207], v169 offset:32768
	ds_read_b128 v[208:211], v169 offset:33792
	ds_read_b128 v[222:225], v169 offset:34816
	ds_read_b128 v[226:229], v169 offset:35840
	ds_read_b128 v[230:233], v169 offset:36864
	ds_read_b128 v[234:237], v169 offset:37888
	ds_read_b128 v[238:241], v169 offset:38912
	ds_read_b128 v[242:245], v169 offset:39936
	global_load_lds_dwordx4 v189, s[26:27]
	s_mov_b32 m0, s72
	s_nop 0
	global_load_lds_dwordx4 v198, s[26:27]
	s_waitcnt vmcnt(8)
	s_waitcnt lgkmcnt(0)
	s_barrier
	v_mfma_f32_16x16x128_f8f6f4 v[160:163], v[26:33], v[204:211], v[160:163]
	s_setprio 1
	v_mfma_f32_16x16x128_f8f6f4 v[156:159], v[18:25], v[204:211], v[156:159]
	v_mfma_f32_16x16x128_f8f6f4 v[148:151], v[18:25], v[222:229], v[148:151]
	v_mfma_f32_16x16x128_f8f6f4 v[152:155], v[26:33], v[222:229], v[152:155]
	v_mfma_f32_16x16x128_f8f6f4 v[144:147], v[26:33], v[230:237], v[144:147]
	v_mfma_f32_16x16x128_f8f6f4 v[140:143], v[18:25], v[230:237], v[140:143]
	v_mfma_f32_16x16x128_f8f6f4 v[132:135], v[18:25], v[238:245], v[132:135]
	v_mfma_f32_16x16x128_f8f6f4 v[136:139], v[26:33], v[238:245], v[136:139]
	v_mfma_f32_16x16x128_f8f6f4 v[128:131], v[10:17], v[204:211], v[128:131]
	v_mfma_f32_16x16x128_f8f6f4 v[124:127], v[2:9], v[204:211], v[124:127]
	v_mfma_f32_16x16x128_f8f6f4 v[116:119], v[2:9], v[222:229], v[116:119]
	v_mfma_f32_16x16x128_f8f6f4 v[120:123], v[10:17], v[222:229], v[120:123]
	v_mfma_f32_16x16x128_f8f6f4 v[112:115], v[10:17], v[230:237], v[112:115]
	v_mfma_f32_16x16x128_f8f6f4 v[108:111], v[2:9], v[230:237], v[108:111]
	v_mfma_f32_16x16x128_f8f6f4 v[100:103], v[2:9], v[238:245], v[100:103]
	s_barrier
	v_mfma_f32_16x16x128_f8f6f4 v[104:107], v[10:17], v[238:245], v[104:107]
	s_setprio 0
	s_add_i32 s54, s54, s68
	s_mov_b64 s[26:27], 0x180
	s_add_i32 s50, s54, 0x2000
	v_lshl_add_u64 v[178:179], v[194:195], 0, s[26:27]
	s_mov_b32 m0, s54
	s_add_u32 s30, s30, 0x20180
	ds_read_b128 v[204:207], v169 offset:49152
	ds_read_b128 v[208:211], v169 offset:50176
	ds_read_b128 v[222:225], v169 offset:51200
	ds_read_b128 v[226:229], v169 offset:52224
	ds_read_b128 v[230:233], v169 offset:53248
	ds_read_b128 v[234:237], v169 offset:54272
	ds_read_b128 v[238:241], v169 offset:55296
	ds_read_b128 v[242:245], v169 offset:56320
	global_load_lds_dwordx4 v[178:179], off
	v_lshl_add_u64 v[178:179], v[196:197], 0, s[26:27]
	s_mov_b32 m0, s50
	s_addc_u32 s31, s31, 0
	s_add_i32 s51, s51, s68
	global_load_lds_dwordx4 v[178:179], off
	v_lshl_add_u64 v[178:179], s[30:31], 0, v[170:171]
	s_mov_b32 m0, s51
	s_add_i32 s64, s51, 0x2000
	global_load_lds_dwordx4 v[178:179], off
	v_lshl_add_u64 v[178:179], s[30:31], 0, v[172:173]
	s_mov_b32 m0, s64
	v_readlane_b32 s26, v253, 39
	global_load_lds_dwordx4 v[178:179], off
	s_mov_b32 m0, s75
	v_readlane_b32 s27, v253, 40
	s_nop 4
	global_load_lds_dwordx4 v34, s[26:27]
	s_mov_b32 m0, s76
	s_nop 0
	global_load_lds_dwordx4 v192, s[26:27]
	s_waitcnt vmcnt(8)
	s_waitcnt lgkmcnt(0)
	s_barrier
	v_mfma_f32_16x16x128_f8f6f4 v[96:99], v[26:33], v[204:211], v[96:99]
	s_setprio 1
	v_mfma_f32_16x16x128_f8f6f4 v[92:95], v[18:25], v[204:211], v[92:95]
	v_mfma_f32_16x16x128_f8f6f4 v[84:87], v[18:25], v[222:229], v[84:87]
	v_mfma_f32_16x16x128_f8f6f4 v[88:91], v[26:33], v[222:229], v[88:91]
	v_mfma_f32_16x16x128_f8f6f4 v[80:83], v[26:33], v[230:237], v[80:83]
	v_mfma_f32_16x16x128_f8f6f4 v[76:79], v[18:25], v[230:237], v[76:79]
	v_mfma_f32_16x16x128_f8f6f4 v[68:71], v[18:25], v[238:245], v[68:71]
	v_mfma_f32_16x16x128_f8f6f4 v[72:75], v[26:33], v[238:245], v[72:75]
	v_mfma_f32_16x16x128_f8f6f4 v[64:67], v[10:17], v[204:211], v[64:67]
	v_mfma_f32_16x16x128_f8f6f4 v[60:63], v[2:9], v[204:211], v[60:63]
	v_mfma_f32_16x16x128_f8f6f4 v[52:55], v[2:9], v[222:229], v[52:55]
	v_mfma_f32_16x16x128_f8f6f4 v[56:59], v[10:17], v[222:229], v[56:59]
	v_mfma_f32_16x16x128_f8f6f4 v[48:51], v[10:17], v[230:237], v[48:51]
	v_mfma_f32_16x16x128_f8f6f4 v[44:47], v[2:9], v[230:237], v[44:47]
	v_mfma_f32_16x16x128_f8f6f4 v[36:39], v[2:9], v[238:245], v[36:39]
	s_barrier
	v_mfma_f32_16x16x128_f8f6f4 v[40:43], v[10:17], v[238:245], v[40:43]
	s_setprio 0
	v_lshl_add_u64 v[18:19], s[26:27], 0, v[174:175]
	v_lshl_add_u64 v[20:21], s[26:27], 0, v[190:191]
	s_mov_b32 s63, 0
	s_mov_b64 s[30:31], 0
	s_branch .LBB0_821
.LBB0_820:
	ds_read_b128 v[204:207], v200
	ds_read_b128 v[208:211], v200 offset:1024
	ds_read_b128 v[222:225], v200 offset:2048
	ds_read_b128 v[226:229], v200 offset:3072
	ds_read_b128 v[10:13], v199
	ds_read_b128 v[14:17], v199 offset:1024
	ds_read_b128 v[2:5], v199 offset:2048
	ds_read_b128 v[6:9], v199 offset:3072
	s_add_u32 s14, s30, 0x200
	s_addc_u32 s86, s31, 0
	s_and_b64 s[40:41], s[36:37], exec
	s_cselect_b32 s14, 0, s14
	s_cselect_b32 s41, 0, s86
	s_add_u32 s40, s20, s14
	s_addc_u32 s41, s21, s41
	s_add_u32 s14, s81, s30
	s_addc_u32 s86, s82, s31
	s_and_b64 s[36:37], s[36:37], exec
	s_cselect_b32 s37, s23, s86
	s_cselect_b32 s36, s22, s14
	s_mov_b32 m0, s84
	v_lshl_add_u64 v[30:31], v[20:21], 0, s[30:31]
	ds_read_b128 v[22:25], v169
	ds_read_b128 v[26:29], v169 offset:1024
	ds_read_b128 v[230:233], v169 offset:2048
	ds_read_b128 v[234:237], v169 offset:3072
	ds_read_b128 v[238:241], v169 offset:4096
	ds_read_b128 v[242:245], v169 offset:5120
	ds_read_b128 v[178:181], v169 offset:6144
	ds_read_b128 v[182:185], v169 offset:7168
	global_load_lds_dwordx4 v[30:31], off
	v_lshl_add_u64 v[30:31], v[18:19], 0, s[30:31]
	s_mov_b32 m0, s53
	s_nop 0
	global_load_lds_dwordx4 v[30:31], off
	s_waitcnt vmcnt(8)
	s_waitcnt lgkmcnt(0)
	s_barrier
	v_mfma_f32_16x16x128_f8f6f4 v[160:163], v[204:211], v[22:29], v[160:163]
	s_setprio 1
	v_mfma_f32_16x16x128_f8f6f4 v[156:159], v[222:229], v[22:29], v[156:159]
	v_mfma_f32_16x16x128_f8f6f4 v[148:151], v[222:229], v[230:237], v[148:151]
	v_mfma_f32_16x16x128_f8f6f4 v[152:155], v[204:211], v[230:237], v[152:155]
	v_mfma_f32_16x16x128_f8f6f4 v[144:147], v[204:211], v[238:245], v[144:147]
	v_mfma_f32_16x16x128_f8f6f4 v[140:143], v[222:229], v[238:245], v[140:143]
	v_mfma_f32_16x16x128_f8f6f4 v[132:135], v[222:229], v[178:185], v[132:135]
	v_mfma_f32_16x16x128_f8f6f4 v[136:139], v[204:211], v[178:185], v[136:139]
	v_mfma_f32_16x16x128_f8f6f4 v[128:131], v[10:17], v[22:29], v[128:131]
	v_mfma_f32_16x16x128_f8f6f4 v[124:127], v[2:9], v[22:29], v[124:127]
	v_mfma_f32_16x16x128_f8f6f4 v[116:119], v[2:9], v[230:237], v[116:119]
	v_mfma_f32_16x16x128_f8f6f4 v[120:123], v[10:17], v[230:237], v[120:123]
	v_mfma_f32_16x16x128_f8f6f4 v[112:115], v[10:17], v[238:245], v[112:115]
	v_mfma_f32_16x16x128_f8f6f4 v[108:111], v[2:9], v[238:245], v[108:111]
	v_mfma_f32_16x16x128_f8f6f4 v[100:103], v[2:9], v[178:185], v[100:103]
	s_barrier
	v_mfma_f32_16x16x128_f8f6f4 v[104:107], v[10:17], v[178:185], v[104:107]
	s_setprio 0
	s_mov_b32 m0, s52
	v_lshl_add_u64 v[22:23], s[36:37], 0, v[170:171]
	s_add_u32 s86, s36, 0x20000
	ds_read_b128 v[178:181], v169 offset:16384
	ds_read_b128 v[182:185], v169 offset:17408
	ds_read_b128 v[230:233], v169 offset:18432
	ds_read_b128 v[234:237], v169 offset:19456
	ds_read_b128 v[238:241], v169 offset:20480
	ds_read_b128 v[242:245], v169 offset:21504
	ds_read_b128 v[212:215], v169 offset:22528
	ds_read_b128 v[216:219], v169 offset:23552
	global_load_lds_dwordx4 v[22:23], off
	v_lshl_add_u64 v[24:25], s[36:37], 0, v[172:173]
	s_mov_b32 m0, s85
	s_addc_u32 s87, s37, 0
	global_load_lds_dwordx4 v[24:25], off
	v_lshl_add_u64 v[26:27], s[86:87], 0, v[170:171]
	s_mov_b32 m0, s55
	v_mov_b32_e32 v193, v35
	global_load_lds_dwordx4 v[26:27], off
	v_lshl_add_u64 v[26:27], s[86:87], 0, v[172:173]
	s_mov_b32 m0, s65
	v_lshl_add_u64 v[28:29], s[40:41], 0, v[34:35]
	global_load_lds_dwordx4 v[26:27], off
	s_mov_b32 m0, s69
	v_lshl_add_u64 v[26:27], s[40:41], 0, v[192:193]
	global_load_lds_dwordx4 v34, s[40:41]
	s_mov_b32 m0, s70
	s_nop 0
	global_load_lds_dwordx4 v192, s[40:41]
	s_waitcnt vmcnt(8)
	s_waitcnt lgkmcnt(0)
	s_barrier
	v_mfma_f32_16x16x128_f8f6f4 v[96:99], v[204:211], v[178:185], v[96:99]
	s_setprio 1
	v_mfma_f32_16x16x128_f8f6f4 v[92:95], v[222:229], v[178:185], v[92:95]
	v_mfma_f32_16x16x128_f8f6f4 v[84:87], v[222:229], v[230:237], v[84:87]
	v_mfma_f32_16x16x128_f8f6f4 v[88:91], v[204:211], v[230:237], v[88:91]
	v_mfma_f32_16x16x128_f8f6f4 v[80:83], v[204:211], v[238:245], v[80:83]
	v_mfma_f32_16x16x128_f8f6f4 v[76:79], v[222:229], v[238:245], v[76:79]
	v_mfma_f32_16x16x128_f8f6f4 v[68:71], v[222:229], v[212:219], v[68:71]
	v_mfma_f32_16x16x128_f8f6f4 v[72:75], v[204:211], v[212:219], v[72:75]
	v_mfma_f32_16x16x128_f8f6f4 v[64:67], v[10:17], v[178:185], v[64:67]
	v_mfma_f32_16x16x128_f8f6f4 v[60:63], v[2:9], v[178:185], v[60:63]
	v_mfma_f32_16x16x128_f8f6f4 v[52:55], v[2:9], v[230:237], v[52:55]
	v_mfma_f32_16x16x128_f8f6f4 v[56:59], v[10:17], v[230:237], v[56:59]
	v_mfma_f32_16x16x128_f8f6f4 v[48:51], v[10:17], v[238:245], v[48:51]
	v_mfma_f32_16x16x128_f8f6f4 v[44:47], v[2:9], v[238:245], v[44:47]
	v_mfma_f32_16x16x128_f8f6f4 v[36:39], v[2:9], v[212:219], v[36:39]
	s_barrier
	v_mfma_f32_16x16x128_f8f6f4 v[40:43], v[10:17], v[212:219], v[40:43]
	s_setprio 0
	ds_read_b128 v[178:181], v201
	ds_read_b128 v[182:185], v201 offset:1024
	ds_read_b128 v[204:207], v201 offset:2048
	ds_read_b128 v[208:211], v201 offset:3072
	ds_read_b128 v[10:13], v202
	ds_read_b128 v[14:17], v202 offset:1024
	ds_read_b128 v[2:5], v202 offset:2048
	ds_read_b128 v[6:9], v202 offset:3072
	s_mov_b32 m0, s71
	ds_read_b128 v[212:215], v169 offset:32768
	ds_read_b128 v[216:219], v169 offset:33792
	ds_read_b128 v[222:225], v169 offset:34816
	ds_read_b128 v[226:229], v169 offset:35840
	ds_read_b128 v[230:233], v169 offset:36864
	ds_read_b128 v[234:237], v169 offset:37888
	ds_read_b128 v[238:241], v169 offset:38912
	ds_read_b128 v[242:245], v169 offset:39936
	global_load_lds_dwordx4 v189, s[40:41]
	s_mov_b32 m0, s72
	s_nop 0
	global_load_lds_dwordx4 v198, s[40:41]
	s_waitcnt vmcnt(8)
	s_waitcnt lgkmcnt(0)
	s_barrier
	v_mfma_f32_16x16x128_f8f6f4 v[160:163], v[178:185], v[212:219], v[160:163]
	s_setprio 1
	v_mfma_f32_16x16x128_f8f6f4 v[156:159], v[204:211], v[212:219], v[156:159]
	v_mfma_f32_16x16x128_f8f6f4 v[148:151], v[204:211], v[222:229], v[148:151]
	v_mfma_f32_16x16x128_f8f6f4 v[152:155], v[178:185], v[222:229], v[152:155]
	v_mfma_f32_16x16x128_f8f6f4 v[144:147], v[178:185], v[230:237], v[144:147]
	v_mfma_f32_16x16x128_f8f6f4 v[140:143], v[204:211], v[230:237], v[140:143]
	v_mfma_f32_16x16x128_f8f6f4 v[132:135], v[204:211], v[238:245], v[132:135]
	v_mfma_f32_16x16x128_f8f6f4 v[136:139], v[178:185], v[238:245], v[136:139]
	v_mfma_f32_16x16x128_f8f6f4 v[128:131], v[10:17], v[212:219], v[128:131]
	v_mfma_f32_16x16x128_f8f6f4 v[124:127], v[2:9], v[212:219], v[124:127]
	v_mfma_f32_16x16x128_f8f6f4 v[116:119], v[2:9], v[222:229], v[116:119]
	v_mfma_f32_16x16x128_f8f6f4 v[120:123], v[10:17], v[222:229], v[120:123]
	v_mfma_f32_16x16x128_f8f6f4 v[112:115], v[10:17], v[230:237], v[112:115]
	v_mfma_f32_16x16x128_f8f6f4 v[108:111], v[2:9], v[230:237], v[108:111]
	v_mfma_f32_16x16x128_f8f6f4 v[100:103], v[2:9], v[238:245], v[100:103]
	s_barrier
	v_mfma_f32_16x16x128_f8f6f4 v[104:107], v[10:17], v[238:245], v[104:107]
	s_setprio 0
	s_mov_b32 m0, s54
	v_lshl_add_u64 v[22:23], v[22:23], 0, s[18:19]
	s_add_u32 s36, s36, 0x20080
	ds_read_b128 v[212:215], v169 offset:49152
	ds_read_b128 v[216:219], v169 offset:50176
	ds_read_b128 v[222:225], v169 offset:51200
	ds_read_b128 v[226:229], v169 offset:52224
	ds_read_b128 v[230:233], v169 offset:53248
	ds_read_b128 v[234:237], v169 offset:54272
	ds_read_b128 v[238:241], v169 offset:55296
	ds_read_b128 v[242:245], v169 offset:56320
	global_load_lds_dwordx4 v[22:23], off
	v_lshl_add_u64 v[22:23], v[24:25], 0, s[18:19]
	s_mov_b32 m0, s50
	s_addc_u32 s37, s37, 0
	global_load_lds_dwordx4 v[22:23], off
	v_lshl_add_u64 v[22:23], s[36:37], 0, v[170:171]
	s_mov_b32 m0, s51
	s_nop 0
	global_load_lds_dwordx4 v[22:23], off
	v_lshl_add_u64 v[22:23], s[36:37], 0, v[172:173]
	s_mov_b32 m0, s64
	s_nop 0
	global_load_lds_dwordx4 v[22:23], off
	v_lshl_add_u64 v[22:23], v[28:29], 0, s[18:19]
	s_mov_b32 m0, s75
	s_nop 0
	global_load_lds_dwordx4 v[22:23], off
	v_lshl_add_u64 v[22:23], v[26:27], 0, s[18:19]
	s_mov_b32 m0, s76
	s_nop 0
	global_load_lds_dwordx4 v[22:23], off
	s_waitcnt vmcnt(8)
	s_waitcnt lgkmcnt(0)
	s_barrier
	v_mfma_f32_16x16x128_f8f6f4 v[96:99], v[178:185], v[212:219], v[96:99]
	s_setprio 1
	v_mfma_f32_16x16x128_f8f6f4 v[92:95], v[204:211], v[212:219], v[92:95]
	v_mfma_f32_16x16x128_f8f6f4 v[84:87], v[204:211], v[222:229], v[84:87]
	v_mfma_f32_16x16x128_f8f6f4 v[88:91], v[178:185], v[222:229], v[88:91]
	v_mfma_f32_16x16x128_f8f6f4 v[80:83], v[178:185], v[230:237], v[80:83]
	v_mfma_f32_16x16x128_f8f6f4 v[76:79], v[204:211], v[230:237], v[76:79]
	v_mfma_f32_16x16x128_f8f6f4 v[68:71], v[204:211], v[238:245], v[68:71]
	v_mfma_f32_16x16x128_f8f6f4 v[72:75], v[178:185], v[238:245], v[72:75]
	v_mfma_f32_16x16x128_f8f6f4 v[64:67], v[10:17], v[212:219], v[64:67]
	v_mfma_f32_16x16x128_f8f6f4 v[60:63], v[2:9], v[212:219], v[60:63]
	v_mfma_f32_16x16x128_f8f6f4 v[52:55], v[2:9], v[222:229], v[52:55]
	v_mfma_f32_16x16x128_f8f6f4 v[56:59], v[10:17], v[222:229], v[56:59]
	v_mfma_f32_16x16x128_f8f6f4 v[48:51], v[10:17], v[230:237], v[48:51]
	v_mfma_f32_16x16x128_f8f6f4 v[44:47], v[2:9], v[230:237], v[44:47]
	v_mfma_f32_16x16x128_f8f6f4 v[36:39], v[2:9], v[238:245], v[36:39]
	s_barrier
	v_mfma_f32_16x16x128_f8f6f4 v[40:43], v[10:17], v[238:245], v[40:43]
	s_setprio 0
	s_add_i32 s63, s63, 2
	s_add_u32 s30, s30, 0x100
	s_addc_u32 s31, s31, 0
	s_cmp_gt_u32 s63, 5
	s_cbranch_scc1 .LBB0_823

.LBB0_899:
	s_mul_i32 s14, s81, 0xe0000
	s_add_u32 s40, s44, s14
	s_addc_u32 s41, s45, 0
	s_and_b64 s[6:7], s[6:7], exec
	s_cselect_b32 s52, s41, s43
	s_cselect_b32 s53, s40, s42
	s_add_i32 s54, 0, 0x10000
	s_add_i32 s65, 0, 0x14000
	v_add_u32_e32 v34, s54, v167
	v_add_u32_e32 v206, s65, v167
	ds_read_b128 v[26:29], v34
	ds_read_b128 v[30:33], v34 offset:1024
	ds_read_b128 v[18:21], v34 offset:2048
	ds_read_b128 v[22:25], v34 offset:3072
	ds_read_b128 v[10:13], v206
	ds_read_b128 v[14:17], v206 offset:1024
	ds_read_b128 v[2:5], v206 offset:2048
	ds_read_b128 v[6:9], v206 offset:3072
	s_add_u32 s6, s42, 0x70080
	s_addc_u32 s7, s43, 0
	s_add_i32 s84, s72, 0xc000
	v_lshl_add_u64 v[216:217], s[6:7], 0, v[174:175]
	s_mov_b32 m0, s84
	s_add_i32 s85, s72, 0xe000
	ds_read_b128 v[178:181], v189
	ds_read_b128 v[182:185], v189 offset:1024
	ds_read_b128 v[198:201], v189 offset:2048
	ds_read_b128 v[202:205], v189 offset:3072
	ds_read_b128 v[208:211], v189 offset:4096
	ds_read_b128 v[212:215], v189 offset:5120
	ds_read_b128 v[222:225], v189 offset:6144
	ds_read_b128 v[226:229], v189 offset:7168
	global_load_lds_dwordx4 v[216:217], off
	v_lshl_add_u64 v[216:217], s[6:7], 0, v[170:171]
	s_mov_b32 m0, s85
	s_nop 0
	global_load_lds_dwordx4 v[216:217], off
	s_waitcnt vmcnt(8)
	s_waitcnt lgkmcnt(0)
	s_barrier
	v_mfma_f32_16x16x128_f8f6f4 v[160:163], v[26:33], v[178:185], 0
	s_setprio 1
	v_mfma_f32_16x16x128_f8f6f4 v[156:159], v[18:25], v[178:185], 0
	v_mfma_f32_16x16x128_f8f6f4 v[148:151], v[18:25], v[198:205], 0
	v_mfma_f32_16x16x128_f8f6f4 v[152:155], v[26:33], v[198:205], 0
	v_mfma_f32_16x16x128_f8f6f4 v[144:147], v[26:33], v[208:215], 0
	v_mfma_f32_16x16x128_f8f6f4 v[140:143], v[18:25], v[208:215], 0
	v_mfma_f32_16x16x128_f8f6f4 v[132:135], v[18:25], v[222:229], 0
	v_mfma_f32_16x16x128_f8f6f4 v[136:139], v[26:33], v[222:229], 0
	v_mfma_f32_16x16x128_f8f6f4 v[128:131], v[10:17], v[178:185], 0
	v_mfma_f32_16x16x128_f8f6f4 v[124:127], v[2:9], v[178:185], 0
	v_mfma_f32_16x16x128_f8f6f4 v[116:119], v[2:9], v[198:205], 0
	v_mfma_f32_16x16x128_f8f6f4 v[120:123], v[10:17], v[198:205], 0
	v_mfma_f32_16x16x128_f8f6f4 v[112:115], v[10:17], v[208:215], 0
	v_mfma_f32_16x16x128_f8f6f4 v[108:111], v[2:9], v[208:215], 0
	v_mfma_f32_16x16x128_f8f6f4 v[100:103], v[2:9], v[222:229], 0
	s_barrier
	v_mfma_f32_16x16x128_f8f6f4 v[104:107], v[10:17], v[222:229], 0
	s_setprio 0
	v_lshl_add_u64 v[198:199], v[196:197], 0, v[172:173]
	s_add_i32 s54, s54, s71
	v_lshl_add_u64 v[200:201], v[198:199], 0, s[28:29]
	s_mov_b32 m0, s54
	ds_read_b128 v[178:181], v189 offset:16384
	ds_read_b128 v[182:185], v189 offset:17408
	ds_read_b128 v[208:211], v189 offset:18432
	ds_read_b128 v[212:215], v189 offset:19456
	ds_read_b128 v[222:225], v189 offset:20480
	ds_read_b128 v[226:229], v189 offset:21504
	ds_read_b128 v[230:233], v189 offset:22528
	ds_read_b128 v[234:237], v189 offset:23552
	global_load_lds_dwordx4 v[200:201], off
	v_lshl_add_u64 v[200:201], v[196:197], 0, v[168:169]
	s_add_i32 s55, s54, 0x2000
	v_lshl_add_u64 v[202:203], v[200:201], 0, s[28:29]
	s_mov_b32 m0, s55
	s_mov_b64 s[6:7], 0x70100
	global_load_lds_dwordx4 v[202:203], off
	v_lshl_add_u64 v[202:203], v[196:197], 0, s[6:7]
	s_add_i32 s65, s65, s71
	v_lshl_add_u64 v[204:205], v[202:203], 0, v[172:173]
	s_mov_b32 m0, s65
	s_add_i32 s67, s65, 0x2000
	global_load_lds_dwordx4 v[204:205], off
	v_lshl_add_u64 v[202:203], v[202:203], 0, v[168:169]
	s_mov_b32 m0, s67
	s_nop 0
	global_load_lds_dwordx4 v[202:203], off
	v_lshl_add_u64 v[202:203], s[42:43], 0, v[174:175]
	v_lshl_add_u64 v[204:205], v[202:203], 0, s[28:29]
	s_mov_b32 m0, s72
	s_nop 0
	global_load_lds_dwordx4 v[204:205], off
	v_lshl_add_u64 v[204:205], s[42:43], 0, v[170:171]
	v_lshl_add_u64 v[216:217], v[204:205], 0, s[28:29]
	s_mov_b32 m0, s73
	s_nop 0
	global_load_lds_dwordx4 v[216:217], off
	s_waitcnt vmcnt(8)
	s_waitcnt lgkmcnt(0)
	s_barrier
	v_mfma_f32_16x16x128_f8f6f4 v[96:99], v[26:33], v[178:185], 0
	s_setprio 1
	v_mfma_f32_16x16x128_f8f6f4 v[92:95], v[18:25], v[178:185], 0
	v_mfma_f32_16x16x128_f8f6f4 v[84:87], v[18:25], v[208:215], 0
	v_mfma_f32_16x16x128_f8f6f4 v[88:91], v[26:33], v[208:215], 0
	v_mfma_f32_16x16x128_f8f6f4 v[80:83], v[26:33], v[222:229], 0
	v_mfma_f32_16x16x128_f8f6f4 v[76:79], v[18:25], v[222:229], 0
	v_mfma_f32_16x16x128_f8f6f4 v[68:71], v[18:25], v[230:237], 0
	v_mfma_f32_16x16x128_f8f6f4 v[72:75], v[26:33], v[230:237], 0
	v_mfma_f32_16x16x128_f8f6f4 v[64:67], v[10:17], v[178:185], 0
	v_mfma_f32_16x16x128_f8f6f4 v[60:63], v[2:9], v[178:185], 0
	v_mfma_f32_16x16x128_f8f6f4 v[52:55], v[2:9], v[208:215], 0
	v_mfma_f32_16x16x128_f8f6f4 v[56:59], v[10:17], v[208:215], 0
	v_mfma_f32_16x16x128_f8f6f4 v[48:51], v[10:17], v[222:229], 0
	v_mfma_f32_16x16x128_f8f6f4 v[44:47], v[2:9], v[222:229], 0
	v_mfma_f32_16x16x128_f8f6f4 v[36:39], v[2:9], v[230:237], 0
	s_barrier
	v_mfma_f32_16x16x128_f8f6f4 v[40:43], v[10:17], v[230:237], 0
	s_setprio 0
	s_add_i32 s50, 0, 0x18000
	s_add_i32 s63, 0, 0x1c000
	v_add_u32_e32 v207, s50, v167
	v_add_u32_e32 v208, s63, v167
	ds_read_b128 v[26:29], v207
	ds_read_b128 v[30:33], v207 offset:1024
	ds_read_b128 v[18:21], v207 offset:2048
	ds_read_b128 v[22:25], v207 offset:3072
	ds_read_b128 v[10:13], v208
	ds_read_b128 v[14:17], v208 offset:1024
	ds_read_b128 v[2:5], v208 offset:2048
	ds_read_b128 v[6:9], v208 offset:3072
	s_add_u32 s6, s42, 0x70100
	s_addc_u32 s7, s43, 0
	s_mov_b32 m0, s74
	v_lshl_add_u64 v[218:219], s[6:7], 0, v[174:175]
	ds_read_b128 v[178:181], v189 offset:32768
	ds_read_b128 v[182:185], v189 offset:33792
	ds_read_b128 v[210:213], v189 offset:34816
	ds_read_b128 v[214:217], v189 offset:35840
	ds_read_b128 v[222:225], v189 offset:36864
	ds_read_b128 v[226:229], v189 offset:37888
	ds_read_b128 v[230:233], v189 offset:38912
	ds_read_b128 v[234:237], v189 offset:39936
	global_load_lds_dwordx4 v[218:219], off
	v_lshl_add_u64 v[218:219], s[6:7], 0, v[170:171]
	s_mov_b32 m0, s75
	s_nop 0
	global_load_lds_dwordx4 v[218:219], off
	s_waitcnt vmcnt(8)
	s_waitcnt lgkmcnt(0)
	s_barrier
	v_mfma_f32_16x16x128_f8f6f4 v[160:163], v[26:33], v[178:185], v[160:163]
	s_setprio 1
	v_mfma_f32_16x16x128_f8f6f4 v[156:159], v[18:25], v[178:185], v[156:159]
	v_mfma_f32_16x16x128_f8f6f4 v[148:151], v[18:25], v[210:217], v[148:151]
	v_mfma_f32_16x16x128_f8f6f4 v[152:155], v[26:33], v[210:217], v[152:155]
	v_mfma_f32_16x16x128_f8f6f4 v[144:147], v[26:33], v[222:229], v[144:147]
	v_mfma_f32_16x16x128_f8f6f4 v[140:143], v[18:25], v[222:229], v[140:143]
	v_mfma_f32_16x16x128_f8f6f4 v[132:135], v[18:25], v[230:237], v[132:135]
	v_mfma_f32_16x16x128_f8f6f4 v[136:139], v[26:33], v[230:237], v[136:139]
	v_mfma_f32_16x16x128_f8f6f4 v[128:131], v[10:17], v[178:185], v[128:131]
	v_mfma_f32_16x16x128_f8f6f4 v[124:127], v[2:9], v[178:185], v[124:127]
	v_mfma_f32_16x16x128_f8f6f4 v[116:119], v[2:9], v[210:217], v[116:119]
	v_mfma_f32_16x16x128_f8f6f4 v[120:123], v[10:17], v[210:217], v[120:123]
	v_mfma_f32_16x16x128_f8f6f4 v[112:115], v[10:17], v[222:229], v[112:115]
	v_mfma_f32_16x16x128_f8f6f4 v[108:111], v[2:9], v[222:229], v[108:111]
	v_mfma_f32_16x16x128_f8f6f4 v[100:103], v[2:9], v[230:237], v[100:103]
	s_barrier
	v_mfma_f32_16x16x128_f8f6f4 v[104:107], v[10:17], v[230:237], v[104:107]
	s_setprio 0
	s_mov_b64 s[6:7], 0x180
	s_add_i32 s50, s50, s71
	v_lshl_add_u64 v[198:199], v[198:199], 0, s[6:7]
	s_mov_b32 m0, s50
	s_add_i32 s51, s50, 0x2000
	ds_read_b128 v[178:181], v189 offset:49152
	ds_read_b128 v[182:185], v189 offset:50176
	ds_read_b128 v[210:213], v189 offset:51200
	ds_read_b128 v[214:217], v189 offset:52224
	ds_read_b128 v[222:225], v189 offset:53248
	ds_read_b128 v[226:229], v189 offset:54272
	ds_read_b128 v[230:233], v189 offset:55296
	ds_read_b128 v[234:237], v189 offset:56320
	global_load_lds_dwordx4 v[198:199], off
	v_lshl_add_u64 v[198:199], v[200:201], 0, s[6:7]
	s_mov_b32 m0, s51
	s_add_i32 s63, s63, s71
	global_load_lds_dwordx4 v[198:199], off
	v_lshl_add_u64 v[198:199], v[196:197], 0, s[26:27]
	v_lshl_add_u64 v[200:201], v[198:199], 0, v[172:173]
	s_mov_b32 m0, s63
	s_add_i32 s64, s63, 0x2000
	global_load_lds_dwordx4 v[200:201], off
	v_lshl_add_u64 v[198:199], v[198:199], 0, v[168:169]
	s_mov_b32 m0, s64
	s_nop 0
	global_load_lds_dwordx4 v[198:199], off
	v_lshl_add_u64 v[198:199], v[202:203], 0, s[6:7]
	s_mov_b32 m0, s77
	s_nop 0
	global_load_lds_dwordx4 v[198:199], off
	v_lshl_add_u64 v[198:199], v[204:205], 0, s[6:7]
	s_mov_b32 m0, s78
	s_nop 0
	global_load_lds_dwordx4 v[198:199], off
	s_waitcnt vmcnt(8)
	s_waitcnt lgkmcnt(0)
	s_barrier
	v_mfma_f32_16x16x128_f8f6f4 v[96:99], v[26:33], v[178:185], v[96:99]
	s_setprio 1
	v_mfma_f32_16x16x128_f8f6f4 v[92:95], v[18:25], v[178:185], v[92:95]
	v_mfma_f32_16x16x128_f8f6f4 v[84:87], v[18:25], v[210:217], v[84:87]
	v_mfma_f32_16x16x128_f8f6f4 v[88:91], v[26:33], v[210:217], v[88:91]
	v_mfma_f32_16x16x128_f8f6f4 v[80:83], v[26:33], v[222:229], v[80:83]
	v_mfma_f32_16x16x128_f8f6f4 v[76:79], v[18:25], v[222:229], v[76:79]
	v_mfma_f32_16x16x128_f8f6f4 v[68:71], v[18:25], v[230:237], v[68:71]
	v_mfma_f32_16x16x128_f8f6f4 v[72:75], v[26:33], v[230:237], v[72:75]
	v_mfma_f32_16x16x128_f8f6f4 v[64:67], v[10:17], v[178:185], v[64:67]
	v_mfma_f32_16x16x128_f8f6f4 v[60:63], v[2:9], v[178:185], v[60:63]
	v_mfma_f32_16x16x128_f8f6f4 v[52:55], v[2:9], v[210:217], v[52:55]
	v_mfma_f32_16x16x128_f8f6f4 v[56:59], v[10:17], v[210:217], v[56:59]
	v_mfma_f32_16x16x128_f8f6f4 v[48:51], v[10:17], v[222:229], v[48:51]
	v_mfma_f32_16x16x128_f8f6f4 v[44:47], v[2:9], v[222:229], v[44:47]
	v_mfma_f32_16x16x128_f8f6f4 v[36:39], v[2:9], v[230:237], v[36:39]
	s_barrier
	v_mfma_f32_16x16x128_f8f6f4 v[40:43], v[10:17], v[230:237], v[40:43]
	s_setprio 0
	s_mov_b64 s[6:7], 0x200
	v_lshl_add_u64 v[18:19], v[196:197], 0, s[6:7]
	s_mov_b32 s86, 0
.LBB0_900:
	ds_read_b128 v[2:5], v34
	ds_read_b128 v[6:9], v34 offset:1024
	ds_read_b128 v[10:13], v34 offset:2048
	ds_read_b128 v[14:17], v34 offset:3072
	ds_read_b128 v[178:181], v206
	ds_read_b128 v[182:185], v206 offset:1024
	ds_read_b128 v[196:199], v206 offset:2048
	ds_read_b128 v[200:203], v206 offset:3072
	s_add_u32 s6, s42, 0x200
	s_addc_u32 s7, s43, 0
	s_cmp_eq_u32 s86, 24
	s_cselect_b64 vcc, -1, 0
	s_cselect_b32 s7, s52, s7
	s_cselect_b32 s6, s53, s6
	v_cndmask_b32_e32 v21, v19, v195, vcc
	v_cndmask_b32_e32 v20, v18, v194, vcc
	s_mov_b32 m0, s84
	v_lshl_add_u64 v[30:31], s[42:43], 0, v[190:191]
	ds_read_b128 v[22:25], v189
	ds_read_b128 v[26:29], v189 offset:1024
	ds_read_b128 v[210:213], v189 offset:2048
	ds_read_b128 v[214:217], v189 offset:3072
	ds_read_b128 v[222:225], v189 offset:4096
	ds_read_b128 v[226:229], v189 offset:5120
	ds_read_b128 v[230:233], v189 offset:6144
	ds_read_b128 v[234:237], v189 offset:7168
	global_load_lds_dwordx4 v[30:31], off
	v_lshl_add_u64 v[30:31], s[42:43], 0, v[192:193]
	s_mov_b32 m0, s85
	s_nop 0
	global_load_lds_dwordx4 v[30:31], off
	s_waitcnt vmcnt(8)
	s_waitcnt lgkmcnt(0)
	s_barrier
	v_mfma_f32_16x16x128_f8f6f4 v[160:163], v[2:9], v[22:29], v[160:163]
	s_setprio 1
	v_mfma_f32_16x16x128_f8f6f4 v[156:159], v[10:17], v[22:29], v[156:159]
	v_mfma_f32_16x16x128_f8f6f4 v[148:151], v[10:17], v[210:217], v[148:151]
	v_mfma_f32_16x16x128_f8f6f4 v[152:155], v[2:9], v[210:217], v[152:155]
	v_mfma_f32_16x16x128_f8f6f4 v[144:147], v[2:9], v[222:229], v[144:147]
	v_mfma_f32_16x16x128_f8f6f4 v[140:143], v[10:17], v[222:229], v[140:143]
	v_mfma_f32_16x16x128_f8f6f4 v[132:135], v[10:17], v[230:237], v[132:135]
	v_mfma_f32_16x16x128_f8f6f4 v[136:139], v[2:9], v[230:237], v[136:139]
	v_mfma_f32_16x16x128_f8f6f4 v[128:131], v[178:185], v[22:29], v[128:131]
	v_mfma_f32_16x16x128_f8f6f4 v[124:127], v[196:203], v[22:29], v[124:127]
	v_mfma_f32_16x16x128_f8f6f4 v[116:119], v[196:203], v[210:217], v[116:119]
	v_mfma_f32_16x16x128_f8f6f4 v[120:123], v[178:185], v[210:217], v[120:123]
	v_mfma_f32_16x16x128_f8f6f4 v[112:115], v[178:185], v[222:229], v[112:115]
	v_mfma_f32_16x16x128_f8f6f4 v[108:111], v[196:203], v[222:229], v[108:111]
	v_mfma_f32_16x16x128_f8f6f4 v[100:103], v[196:203], v[230:237], v[100:103]
	s_barrier
	v_mfma_f32_16x16x128_f8f6f4 v[104:107], v[178:185], v[230:237], v[104:107]
	s_setprio 0
	s_mov_b32 m0, s54
	v_lshl_add_u64 v[22:23], v[20:21], 0, v[172:173]
	ds_read_b128 v[210:213], v189 offset:16384
	ds_read_b128 v[214:217], v189 offset:17408
	ds_read_b128 v[222:225], v189 offset:18432
	ds_read_b128 v[226:229], v189 offset:19456
	ds_read_b128 v[230:233], v189 offset:20480
	ds_read_b128 v[234:237], v189 offset:21504
	ds_read_b128 v[238:241], v189 offset:22528
	ds_read_b128 v[242:245], v189 offset:23552
	global_load_lds_dwordx4 v[22:23], off
	v_lshl_add_u64 v[24:25], v[20:21], 0, v[168:169]
	s_mov_b32 m0, s55
	v_lshl_add_u64 v[26:27], v[20:21], 0, s[2:3]
	global_load_lds_dwordx4 v[24:25], off
	v_lshl_add_u64 v[28:29], v[26:27], 0, v[172:173]
	s_mov_b32 m0, s65
	v_lshl_add_u64 v[26:27], v[26:27], 0, v[168:169]
	global_load_lds_dwordx4 v[28:29], off
	s_mov_b32 m0, s67
	v_lshl_add_u64 v[28:29], s[6:7], 0, v[170:171]
	global_load_lds_dwordx4 v[26:27], off
	v_lshl_add_u64 v[26:27], s[6:7], 0, v[174:175]
	s_mov_b32 m0, s72
	s_nop 0
	global_load_lds_dwordx4 v[26:27], off
	s_mov_b32 m0, s73
	s_nop 0
	global_load_lds_dwordx4 v[28:29], off
	s_waitcnt vmcnt(8)
	s_waitcnt lgkmcnt(0)
	s_barrier
	v_mfma_f32_16x16x128_f8f6f4 v[96:99], v[2:9], v[210:217], v[96:99]
	s_setprio 1
	v_mfma_f32_16x16x128_f8f6f4 v[92:95], v[10:17], v[210:217], v[92:95]
	v_mfma_f32_16x16x128_f8f6f4 v[84:87], v[10:17], v[222:229], v[84:87]
	v_mfma_f32_16x16x128_f8f6f4 v[88:91], v[2:9], v[222:229], v[88:91]
	v_mfma_f32_16x16x128_f8f6f4 v[80:83], v[2:9], v[230:237], v[80:83]
	v_mfma_f32_16x16x128_f8f6f4 v[76:79], v[10:17], v[230:237], v[76:79]
	v_mfma_f32_16x16x128_f8f6f4 v[68:71], v[10:17], v[238:245], v[68:71]
	v_mfma_f32_16x16x128_f8f6f4 v[72:75], v[2:9], v[238:245], v[72:75]
	v_mfma_f32_16x16x128_f8f6f4 v[64:67], v[178:185], v[210:217], v[64:67]
	v_mfma_f32_16x16x128_f8f6f4 v[60:63], v[196:203], v[210:217], v[60:63]
	v_mfma_f32_16x16x128_f8f6f4 v[52:55], v[196:203], v[222:229], v[52:55]
	v_mfma_f32_16x16x128_f8f6f4 v[56:59], v[178:185], v[222:229], v[56:59]
	v_mfma_f32_16x16x128_f8f6f4 v[48:51], v[178:185], v[230:237], v[48:51]
	v_mfma_f32_16x16x128_f8f6f4 v[44:47], v[196:203], v[230:237], v[44:47]
	v_mfma_f32_16x16x128_f8f6f4 v[36:39], v[196:203], v[238:245], v[36:39]
	s_barrier
	v_mfma_f32_16x16x128_f8f6f4 v[40:43], v[178:185], v[238:245], v[40:43]
	s_setprio 0
	ds_read_b128 v[178:181], v207
	ds_read_b128 v[182:185], v207 offset:1024
	ds_read_b128 v[196:199], v207 offset:2048
	ds_read_b128 v[200:203], v207 offset:3072
	ds_read_b128 v[10:13], v208
	ds_read_b128 v[14:17], v208 offset:1024
	ds_read_b128 v[2:5], v208 offset:2048
	ds_read_b128 v[6:9], v208 offset:3072
	s_add_u32 s6, s6, 0x70000
	s_addc_u32 s7, s7, 0
	s_mov_b32 m0, s74
	v_lshl_add_u64 v[30:31], s[6:7], 0, v[174:175]
	ds_read_b128 v[210:213], v189 offset:32768
	ds_read_b128 v[214:217], v189 offset:33792
	ds_read_b128 v[222:225], v189 offset:34816
	ds_read_b128 v[226:229], v189 offset:35840
	ds_read_b128 v[230:233], v189 offset:36864
	ds_read_b128 v[234:237], v189 offset:37888
	ds_read_b128 v[238:241], v189 offset:38912
	ds_read_b128 v[242:245], v189 offset:39936
	global_load_lds_dwordx4 v[30:31], off
	v_lshl_add_u64 v[30:31], s[6:7], 0, v[170:171]
	s_mov_b32 m0, s75
	s_nop 0
	global_load_lds_dwordx4 v[30:31], off
	s_waitcnt vmcnt(8)
	s_waitcnt lgkmcnt(0)
	s_barrier
	v_mfma_f32_16x16x128_f8f6f4 v[160:163], v[178:185], v[210:217], v[160:163]
	s_setprio 1
	v_mfma_f32_16x16x128_f8f6f4 v[156:159], v[196:203], v[210:217], v[156:159]
	v_mfma_f32_16x16x128_f8f6f4 v[148:151], v[196:203], v[222:229], v[148:151]
	v_mfma_f32_16x16x128_f8f6f4 v[152:155], v[178:185], v[222:229], v[152:155]
	v_mfma_f32_16x16x128_f8f6f4 v[144:147], v[178:185], v[230:237], v[144:147]
	v_mfma_f32_16x16x128_f8f6f4 v[140:143], v[196:203], v[230:237], v[140:143]
	v_mfma_f32_16x16x128_f8f6f4 v[132:135], v[196:203], v[238:245], v[132:135]
	v_mfma_f32_16x16x128_f8f6f4 v[136:139], v[178:185], v[238:245], v[136:139]
	v_mfma_f32_16x16x128_f8f6f4 v[128:131], v[10:17], v[210:217], v[128:131]
	v_mfma_f32_16x16x128_f8f6f4 v[124:127], v[2:9], v[210:217], v[124:127]
	v_mfma_f32_16x16x128_f8f6f4 v[116:119], v[2:9], v[222:229], v[116:119]
	v_mfma_f32_16x16x128_f8f6f4 v[120:123], v[10:17], v[222:229], v[120:123]
	v_mfma_f32_16x16x128_f8f6f4 v[112:115], v[10:17], v[230:237], v[112:115]
	v_mfma_f32_16x16x128_f8f6f4 v[108:111], v[2:9], v[230:237], v[108:111]
	v_mfma_f32_16x16x128_f8f6f4 v[100:103], v[2:9], v[238:245], v[100:103]
	s_barrier
	v_mfma_f32_16x16x128_f8f6f4 v[104:107], v[10:17], v[238:245], v[104:107]
	s_setprio 0
	s_mov_b32 m0, s50
	v_lshl_add_u64 v[22:23], v[22:23], 0, s[18:19]
	ds_read_b128 v[210:213], v189 offset:49152
	ds_read_b128 v[214:217], v189 offset:50176
	ds_read_b128 v[222:225], v189 offset:51200
	ds_read_b128 v[226:229], v189 offset:52224
	ds_read_b128 v[230:233], v189 offset:53248
	ds_read_b128 v[234:237], v189 offset:54272
	ds_read_b128 v[238:241], v189 offset:55296
	ds_read_b128 v[242:245], v189 offset:56320
	global_load_lds_dwordx4 v[22:23], off
	v_lshl_add_u64 v[22:23], v[24:25], 0, s[18:19]
	s_mov_b32 m0, s51
	v_lshl_add_u64 v[20:21], v[20:21], 0, s[34:35]
	global_load_lds_dwordx4 v[22:23], off
	v_lshl_add_u64 v[22:23], v[20:21], 0, v[172:173]
	s_mov_b32 m0, s63
	v_lshl_add_u64 v[20:21], v[20:21], 0, v[168:169]
	global_load_lds_dwordx4 v[22:23], off
	s_mov_b32 m0, s64
	s_nop 0
	global_load_lds_dwordx4 v[20:21], off
	v_lshl_add_u64 v[20:21], v[26:27], 0, s[18:19]
	s_mov_b32 m0, s77
	s_nop 0
	global_load_lds_dwordx4 v[20:21], off
	v_lshl_add_u64 v[20:21], v[28:29], 0, s[18:19]
	s_mov_b32 m0, s78
	s_nop 0
	global_load_lds_dwordx4 v[20:21], off
	s_waitcnt vmcnt(8)
	s_waitcnt lgkmcnt(0)
	s_barrier
	v_mfma_f32_16x16x128_f8f6f4 v[96:99], v[178:185], v[210:217], v[96:99]
	s_setprio 1
	v_mfma_f32_16x16x128_f8f6f4 v[92:95], v[196:203], v[210:217], v[92:95]
	v_mfma_f32_16x16x128_f8f6f4 v[84:87], v[196:203], v[222:229], v[84:87]
	v_mfma_f32_16x16x128_f8f6f4 v[88:91], v[178:185], v[222:229], v[88:91]
	v_mfma_f32_16x16x128_f8f6f4 v[80:83], v[178:185], v[230:237], v[80:83]
	v_mfma_f32_16x16x128_f8f6f4 v[76:79], v[196:203], v[230:237], v[76:79]
	v_mfma_f32_16x16x128_f8f6f4 v[68:71], v[196:203], v[238:245], v[68:71]
	v_mfma_f32_16x16x128_f8f6f4 v[72:75], v[178:185], v[238:245], v[72:75]
	v_mfma_f32_16x16x128_f8f6f4 v[64:67], v[10:17], v[210:217], v[64:67]
	v_mfma_f32_16x16x128_f8f6f4 v[60:63], v[2:9], v[210:217], v[60:63]
	v_mfma_f32_16x16x128_f8f6f4 v[52:55], v[2:9], v[222:229], v[52:55]
	v_mfma_f32_16x16x128_f8f6f4 v[56:59], v[10:17], v[222:229], v[56:59]
	v_mfma_f32_16x16x128_f8f6f4 v[48:51], v[10:17], v[230:237], v[48:51]
	v_mfma_f32_16x16x128_f8f6f4 v[44:47], v[2:9], v[230:237], v[44:47]
	v_mfma_f32_16x16x128_f8f6f4 v[36:39], v[2:9], v[238:245], v[36:39]
	s_barrier
	v_mfma_f32_16x16x128_f8f6f4 v[40:43], v[10:17], v[238:245], v[40:43]
	s_setprio 0
	s_add_i32 s86, s86, 2
	s_add_u32 s42, s42, 0x100
	s_addc_u32 s43, s43, 0
	s_cmp_gt_u32 s86, 25
	v_lshl_add_u64 v[18:19], v[18:19], 0, s[28:29]
	s_cbranch_scc0 .LBB0_900
	s_and_b64 vcc, exec, s[36:37]
	s_mov_b64 s[84:85], s[24:25]
	s_cbranch_vccz .LBB0_903
	s_barrier

.LBB0_953:
	s_add_u32 s95, s30, 0x200
	s_addc_u32 s96, s31, 0
	s_add_i32 s65, 0, 0x14000
	s_add_i32 s67, 0, 0x10000
	v_add_u32_e32 v199, s65, v167
	v_add_u32_e32 v200, s67, v167
	ds_read_b128 v[10:13], v199
	ds_read_b128 v[14:17], v199 offset:1024
	ds_read_b128 v[2:5], v199 offset:2048
	ds_read_b128 v[6:9], v199 offset:3072
	ds_read_b128 v[22:25], v200 offset:3072
	ds_read_b128 v[18:21], v200 offset:2048
	ds_read_b128 v[30:33], v200 offset:1024
	ds_read_b128 v[26:29], v200
	s_lshl_b32 s14, s94, 10
	s_add_i32 s97, s14, 0
	s_add_i32 s97, s97, 0x20400
	v_mov_b32_e32 v191, v35
	v_mov_b32_e32 v175, v35
	s_add_i32 s83, s52, 0xc000
	v_readlane_b32 s26, v253, 28
	s_mov_b32 m0, s83
	v_readlane_b32 s27, v253, 29
	s_add_i32 s53, s52, 0xe000
	ds_read_b128 v[178:181], v169
	ds_read_b128 v[182:185], v169 offset:1024
	ds_read_b128 v[202:205], v169 offset:2048
	ds_read_b128 v[206:209], v169 offset:3072
	ds_read_b128 v[210:213], v169 offset:4096
	ds_read_b128 v[214:217], v169 offset:5120
	ds_read_b128 v[222:225], v169 offset:6144
	ds_read_b128 v[226:229], v169 offset:7168
	global_load_lds_dwordx4 v190, s[26:27]
	s_mov_b32 m0, s53
	s_nop 0
	global_load_lds_dwordx4 v174, s[26:27]
	s_waitcnt vmcnt(8)
	s_waitcnt lgkmcnt(0)
	s_barrier
	v_mfma_f32_16x16x128_f8f6f4 v[160:163], v[26:33], v[178:185], 0
	s_setprio 1
	v_mfma_f32_16x16x128_f8f6f4 v[156:159], v[18:25], v[178:185], 0
	v_mfma_f32_16x16x128_f8f6f4 v[148:151], v[18:25], v[202:209], 0
	v_mfma_f32_16x16x128_f8f6f4 v[152:155], v[26:33], v[202:209], 0
	v_mfma_f32_16x16x128_f8f6f4 v[144:147], v[26:33], v[210:217], 0
	v_mfma_f32_16x16x128_f8f6f4 v[140:143], v[18:25], v[210:217], 0
	v_mfma_f32_16x16x128_f8f6f4 v[132:135], v[18:25], v[222:229], 0
	v_mfma_f32_16x16x128_f8f6f4 v[136:139], v[26:33], v[222:229], 0
	v_mfma_f32_16x16x128_f8f6f4 v[128:131], v[10:17], v[178:185], 0
	v_mfma_f32_16x16x128_f8f6f4 v[124:127], v[2:9], v[178:185], 0
	v_mfma_f32_16x16x128_f8f6f4 v[116:119], v[2:9], v[202:209], 0
	v_mfma_f32_16x16x128_f8f6f4 v[120:123], v[10:17], v[202:209], 0
	v_mfma_f32_16x16x128_f8f6f4 v[112:115], v[10:17], v[210:217], 0
	v_mfma_f32_16x16x128_f8f6f4 v[108:111], v[2:9], v[210:217], 0
	v_mfma_f32_16x16x128_f8f6f4 v[100:103], v[2:9], v[222:229], 0
	s_barrier
	v_mfma_f32_16x16x128_f8f6f4 v[104:107], v[10:17], v[222:229], 0
	s_setprio 0
	v_lshl_add_u64 v[194:195], s[30:31], 0, v[170:171]
	s_add_i32 s67, s67, s82
	v_lshl_add_u64 v[196:197], v[194:195], 0, s[28:29]
	s_mov_b32 m0, s67
	s_add_i32 s55, s67, 0x2000
	ds_read_b128 v[178:181], v169 offset:16384
	ds_read_b128 v[182:185], v169 offset:17408
	ds_read_b128 v[202:205], v169 offset:18432
	ds_read_b128 v[206:209], v169 offset:19456
	ds_read_b128 v[210:213], v169 offset:20480
	ds_read_b128 v[214:217], v169 offset:21504
	ds_read_b128 v[222:225], v169 offset:22528
	ds_read_b128 v[226:229], v169 offset:23552
	global_load_lds_dwordx4 v[196:197], off
	v_lshl_add_u64 v[196:197], s[30:31], 0, v[172:173]
	s_add_u32 s46, s30, 0x20100
	v_lshl_add_u64 v[218:219], v[196:197], 0, s[28:29]
	s_mov_b32 m0, s55
	s_addc_u32 s47, s31, 0
	s_add_i32 s65, s65, s82
	global_load_lds_dwordx4 v[218:219], off
	v_lshl_add_u64 v[218:219], s[46:47], 0, v[170:171]
	s_mov_b32 m0, s65
	s_add_i32 s54, s65, 0x2000
	global_load_lds_dwordx4 v[218:219], off
	v_lshl_add_u64 v[218:219], s[46:47], 0, v[172:173]
	s_mov_b32 m0, s54
	v_readlane_b32 s26, v253, 37
	global_load_lds_dwordx4 v[218:219], off
	s_mov_b32 m0, s52
	v_readlane_b32 s27, v253, 38
	s_nop 4
	global_load_lds_dwordx4 v34, s[26:27]
	s_mov_b32 m0, s84
	s_nop 0
	global_load_lds_dwordx4 v192, s[26:27]
	s_waitcnt vmcnt(8)
	s_waitcnt lgkmcnt(0)
	s_barrier
	v_mfma_f32_16x16x128_f8f6f4 v[96:99], v[26:33], v[178:185], 0
	s_setprio 1
	v_mfma_f32_16x16x128_f8f6f4 v[92:95], v[18:25], v[178:185], 0
	v_mfma_f32_16x16x128_f8f6f4 v[84:87], v[18:25], v[202:209], 0
	v_mfma_f32_16x16x128_f8f6f4 v[88:91], v[26:33], v[202:209], 0
	v_mfma_f32_16x16x128_f8f6f4 v[80:83], v[26:33], v[210:217], 0
	v_mfma_f32_16x16x128_f8f6f4 v[76:79], v[18:25], v[210:217], 0
	v_mfma_f32_16x16x128_f8f6f4 v[68:71], v[18:25], v[222:229], 0
	v_mfma_f32_16x16x128_f8f6f4 v[72:75], v[26:33], v[222:229], 0
	v_mfma_f32_16x16x128_f8f6f4 v[64:67], v[10:17], v[178:185], 0
	v_mfma_f32_16x16x128_f8f6f4 v[60:63], v[2:9], v[178:185], 0
	v_mfma_f32_16x16x128_f8f6f4 v[52:55], v[2:9], v[202:209], 0
	v_mfma_f32_16x16x128_f8f6f4 v[56:59], v[10:17], v[202:209], 0
	v_mfma_f32_16x16x128_f8f6f4 v[48:51], v[10:17], v[210:217], 0
	v_mfma_f32_16x16x128_f8f6f4 v[44:47], v[2:9], v[210:217], 0
	v_mfma_f32_16x16x128_f8f6f4 v[36:39], v[2:9], v[222:229], 0
	s_barrier
	v_mfma_f32_16x16x128_f8f6f4 v[40:43], v[10:17], v[222:229], 0
	s_setprio 0
	s_add_i32 s50, 0, 0x18000
	s_add_i32 s64, 0, 0x1c000
	v_add_u32_e32 v201, s50, v167
	v_add_u32_e32 v202, s64, v167
	ds_read_b128 v[26:29], v201
	ds_read_b128 v[30:33], v201 offset:1024
	ds_read_b128 v[18:21], v201 offset:2048
	ds_read_b128 v[22:25], v201 offset:3072
	ds_read_b128 v[10:13], v202
	ds_read_b128 v[14:17], v202 offset:1024
	ds_read_b128 v[2:5], v202 offset:2048
	ds_read_b128 v[6:9], v202 offset:3072
	s_mov_b32 m0, s85
	ds_read_b128 v[178:181], v169 offset:32768
	ds_read_b128 v[182:185], v169 offset:33792
	ds_read_b128 v[204:207], v169 offset:34816
	ds_read_b128 v[208:211], v169 offset:35840
	ds_read_b128 v[212:215], v169 offset:36864
	ds_read_b128 v[216:219], v169 offset:37888
	ds_read_b128 v[222:225], v169 offset:38912
	ds_read_b128 v[226:229], v169 offset:39936
	global_load_lds_dwordx4 v189, s[26:27]
	s_mov_b32 m0, s86
	s_nop 0
	global_load_lds_dwordx4 v198, s[26:27]
	s_waitcnt vmcnt(8)
	s_waitcnt lgkmcnt(0)
	s_barrier
	v_mfma_f32_16x16x128_f8f6f4 v[160:163], v[26:33], v[178:185], v[160:163]
	s_setprio 1
	v_mfma_f32_16x16x128_f8f6f4 v[156:159], v[18:25], v[178:185], v[156:159]
	v_mfma_f32_16x16x128_f8f6f4 v[148:151], v[18:25], v[204:211], v[148:151]
	v_mfma_f32_16x16x128_f8f6f4 v[152:155], v[26:33], v[204:211], v[152:155]
	v_mfma_f32_16x16x128_f8f6f4 v[144:147], v[26:33], v[212:219], v[144:147]
	v_mfma_f32_16x16x128_f8f6f4 v[140:143], v[18:25], v[212:219], v[140:143]
	v_mfma_f32_16x16x128_f8f6f4 v[132:135], v[18:25], v[222:229], v[132:135]
	v_mfma_f32_16x16x128_f8f6f4 v[136:139], v[26:33], v[222:229], v[136:139]
	v_mfma_f32_16x16x128_f8f6f4 v[128:131], v[10:17], v[178:185], v[128:131]
	v_mfma_f32_16x16x128_f8f6f4 v[124:127], v[2:9], v[178:185], v[124:127]
	v_mfma_f32_16x16x128_f8f6f4 v[116:119], v[2:9], v[204:211], v[116:119]
	v_mfma_f32_16x16x128_f8f6f4 v[120:123], v[10:17], v[204:211], v[120:123]
	v_mfma_f32_16x16x128_f8f6f4 v[112:115], v[10:17], v[212:219], v[112:115]
	v_mfma_f32_16x16x128_f8f6f4 v[108:111], v[2:9], v[212:219], v[108:111]
	v_mfma_f32_16x16x128_f8f6f4 v[100:103], v[2:9], v[222:229], v[100:103]
	s_barrier
	v_mfma_f32_16x16x128_f8f6f4 v[104:107], v[10:17], v[222:229], v[104:107]
	s_setprio 0
	s_add_i32 s50, s50, s82
	s_mov_b64 s[26:27], 0x180
	s_add_i32 s51, s50, 0x2000
	v_lshl_add_u64 v[194:195], v[194:195], 0, s[26:27]
	s_mov_b32 m0, s50
	s_add_u32 s30, s30, 0x20180
	ds_read_b128 v[178:181], v169 offset:49152
	ds_read_b128 v[182:185], v169 offset:50176
	ds_read_b128 v[204:207], v169 offset:51200
	ds_read_b128 v[208:211], v169 offset:52224
	ds_read_b128 v[212:215], v169 offset:53248
	ds_read_b128 v[216:219], v169 offset:54272
	ds_read_b128 v[222:225], v169 offset:55296
	ds_read_b128 v[226:229], v169 offset:56320
	global_load_lds_dwordx4 v[194:195], off
	v_lshl_add_u64 v[194:195], v[196:197], 0, s[26:27]
	s_mov_b32 m0, s51
	s_addc_u32 s31, s31, 0
	s_add_i32 s64, s64, s82
	global_load_lds_dwordx4 v[194:195], off
	v_lshl_add_u64 v[194:195], s[30:31], 0, v[170:171]
	s_mov_b32 m0, s64
	s_add_i32 s63, s64, 0x2000
	global_load_lds_dwordx4 v[194:195], off
	v_lshl_add_u64 v[194:195], s[30:31], 0, v[172:173]
	s_mov_b32 m0, s63
	v_readlane_b32 s26, v253, 39
	global_load_lds_dwordx4 v[194:195], off
	s_mov_b32 m0, s90
	v_readlane_b32 s27, v253, 40
	s_nop 4
	global_load_lds_dwordx4 v34, s[26:27]
	s_mov_b32 m0, s91
	s_nop 0
	global_load_lds_dwordx4 v192, s[26:27]
	s_waitcnt vmcnt(8)
	s_waitcnt lgkmcnt(0)
	s_barrier
	v_mfma_f32_16x16x128_f8f6f4 v[96:99], v[26:33], v[178:185], v[96:99]
	s_setprio 1
	v_mfma_f32_16x16x128_f8f6f4 v[92:95], v[18:25], v[178:185], v[92:95]
	v_mfma_f32_16x16x128_f8f6f4 v[84:87], v[18:25], v[204:211], v[84:87]
	v_mfma_f32_16x16x128_f8f6f4 v[88:91], v[26:33], v[204:211], v[88:91]
	v_mfma_f32_16x16x128_f8f6f4 v[80:83], v[26:33], v[212:219], v[80:83]
	v_mfma_f32_16x16x128_f8f6f4 v[76:79], v[18:25], v[212:219], v[76:79]
	v_mfma_f32_16x16x128_f8f6f4 v[68:71], v[18:25], v[222:229], v[68:71]
	v_mfma_f32_16x16x128_f8f6f4 v[72:75], v[26:33], v[222:229], v[72:75]
	v_mfma_f32_16x16x128_f8f6f4 v[64:67], v[10:17], v[178:185], v[64:67]
	v_mfma_f32_16x16x128_f8f6f4 v[60:63], v[2:9], v[178:185], v[60:63]
	v_mfma_f32_16x16x128_f8f6f4 v[52:55], v[2:9], v[204:211], v[52:55]
	v_mfma_f32_16x16x128_f8f6f4 v[56:59], v[10:17], v[204:211], v[56:59]
	v_mfma_f32_16x16x128_f8f6f4 v[48:51], v[10:17], v[212:219], v[48:51]
	v_mfma_f32_16x16x128_f8f6f4 v[44:47], v[2:9], v[212:219], v[44:47]
	v_mfma_f32_16x16x128_f8f6f4 v[36:39], v[2:9], v[222:229], v[36:39]
	s_barrier
	v_mfma_f32_16x16x128_f8f6f4 v[40:43], v[10:17], v[222:229], v[40:43]
	s_setprio 0
	v_lshl_add_u64 v[18:19], s[26:27], 0, v[174:175]
	v_lshl_add_u64 v[20:21], s[26:27], 0, v[190:191]
	s_mov_b32 s75, 0
	s_mov_b64 s[30:31], 0
	s_branch .LBB0_955
.LBB0_954:
	ds_read_b128 v[178:181], v200
	ds_read_b128 v[182:185], v200 offset:1024
	ds_read_b128 v[204:207], v200 offset:2048
	ds_read_b128 v[208:211], v200 offset:3072
	ds_read_b128 v[10:13], v199
	ds_read_b128 v[14:17], v199 offset:1024
	ds_read_b128 v[2:5], v199 offset:2048
	ds_read_b128 v[6:9], v199 offset:3072
	s_add_u32 s14, s30, 0x200
	s_addc_u32 vcc_lo, s31, 0
	s_and_b64 s[48:49], s[46:47], exec
	s_cselect_b32 s14, 0, s14
	s_cselect_b32 s49, 0, vcc_lo
	s_add_u32 s48, s20, s14
	s_addc_u32 s49, s21, s49
	s_add_u32 s14, s95, s30
	s_addc_u32 vcc_lo, s96, s31
	s_and_b64 s[46:47], s[46:47], exec
	s_cselect_b32 s47, s43, vcc_lo
	s_cselect_b32 s46, s42, s14
	s_mov_b32 m0, s83
	v_lshl_add_u64 v[30:31], v[20:21], 0, s[30:31]
	ds_read_b128 v[22:25], v169
	ds_read_b128 v[26:29], v169 offset:1024
	ds_read_b128 v[212:215], v169 offset:2048
	ds_read_b128 v[216:219], v169 offset:3072
	ds_read_b128 v[222:225], v169 offset:4096
	ds_read_b128 v[226:229], v169 offset:5120
	ds_read_b128 v[230:233], v169 offset:6144
	ds_read_b128 v[234:237], v169 offset:7168
	global_load_lds_dwordx4 v[30:31], off
	v_lshl_add_u64 v[30:31], v[18:19], 0, s[30:31]
	s_mov_b32 m0, s53
	s_nop 0
	global_load_lds_dwordx4 v[30:31], off
	s_waitcnt vmcnt(8)
	s_waitcnt lgkmcnt(0)
	s_barrier
	v_mfma_f32_16x16x128_f8f6f4 v[160:163], v[178:185], v[22:29], v[160:163]
	s_setprio 1
	v_mfma_f32_16x16x128_f8f6f4 v[156:159], v[204:211], v[22:29], v[156:159]
	v_mfma_f32_16x16x128_f8f6f4 v[148:151], v[204:211], v[212:219], v[148:151]
	v_mfma_f32_16x16x128_f8f6f4 v[152:155], v[178:185], v[212:219], v[152:155]
	v_mfma_f32_16x16x128_f8f6f4 v[144:147], v[178:185], v[222:229], v[144:147]
	v_mfma_f32_16x16x128_f8f6f4 v[140:143], v[204:211], v[222:229], v[140:143]
	v_mfma_f32_16x16x128_f8f6f4 v[132:135], v[204:211], v[230:237], v[132:135]
	v_mfma_f32_16x16x128_f8f6f4 v[136:139], v[178:185], v[230:237], v[136:139]
	v_mfma_f32_16x16x128_f8f6f4 v[128:131], v[10:17], v[22:29], v[128:131]
	v_mfma_f32_16x16x128_f8f6f4 v[124:127], v[2:9], v[22:29], v[124:127]
	v_mfma_f32_16x16x128_f8f6f4 v[116:119], v[2:9], v[212:219], v[116:119]
	v_mfma_f32_16x16x128_f8f6f4 v[120:123], v[10:17], v[212:219], v[120:123]
	v_mfma_f32_16x16x128_f8f6f4 v[112:115], v[10:17], v[222:229], v[112:115]
	v_mfma_f32_16x16x128_f8f6f4 v[108:111], v[2:9], v[222:229], v[108:111]
	v_mfma_f32_16x16x128_f8f6f4 v[100:103], v[2:9], v[230:237], v[100:103]
	s_barrier
	v_mfma_f32_16x16x128_f8f6f4 v[104:107], v[10:17], v[230:237], v[104:107]
	s_setprio 0
	s_mov_b32 m0, s67
	v_lshl_add_u64 v[22:23], s[46:47], 0, v[170:171]
	s_add_u32 vcc_lo, s46, 0x20000
	ds_read_b128 v[212:215], v169 offset:16384
	ds_read_b128 v[216:219], v169 offset:17408
	ds_read_b128 v[222:225], v169 offset:18432
	ds_read_b128 v[226:229], v169 offset:19456
	ds_read_b128 v[230:233], v169 offset:20480
	ds_read_b128 v[234:237], v169 offset:21504
	ds_read_b128 v[238:241], v169 offset:22528
	ds_read_b128 v[242:245], v169 offset:23552
	global_load_lds_dwordx4 v[22:23], off
	v_lshl_add_u64 v[24:25], s[46:47], 0, v[172:173]
	s_mov_b32 m0, s55
	s_addc_u32 vcc_hi, s47, 0
	global_load_lds_dwordx4 v[24:25], off
	v_lshl_add_u64 v[26:27], vcc, 0, v[170:171]
	s_mov_b32 m0, s65
	v_mov_b32_e32 v193, v35
	global_load_lds_dwordx4 v[26:27], off
	v_lshl_add_u64 v[26:27], vcc, 0, v[172:173]
	s_mov_b32 m0, s54
	v_lshl_add_u64 v[28:29], s[48:49], 0, v[34:35]
	global_load_lds_dwordx4 v[26:27], off
	s_mov_b32 m0, s52
	v_lshl_add_u64 v[26:27], s[48:49], 0, v[192:193]
	global_load_lds_dwordx4 v34, s[48:49]
	s_mov_b32 m0, s84
	s_nop 0
	global_load_lds_dwordx4 v192, s[48:49]
	s_waitcnt vmcnt(8)
	s_waitcnt lgkmcnt(0)
	s_barrier
	v_mfma_f32_16x16x128_f8f6f4 v[96:99], v[178:185], v[212:219], v[96:99]
	s_setprio 1
	v_mfma_f32_16x16x128_f8f6f4 v[92:95], v[204:211], v[212:219], v[92:95]
	v_mfma_f32_16x16x128_f8f6f4 v[84:87], v[204:211], v[222:229], v[84:87]
	v_mfma_f32_16x16x128_f8f6f4 v[88:91], v[178:185], v[222:229], v[88:91]
	v_mfma_f32_16x16x128_f8f6f4 v[80:83], v[178:185], v[230:237], v[80:83]
	v_mfma_f32_16x16x128_f8f6f4 v[76:79], v[204:211], v[230:237], v[76:79]
	v_mfma_f32_16x16x128_f8f6f4 v[68:71], v[204:211], v[238:245], v[68:71]
	v_mfma_f32_16x16x128_f8f6f4 v[72:75], v[178:185], v[238:245], v[72:75]
	v_mfma_f32_16x16x128_f8f6f4 v[64:67], v[10:17], v[212:219], v[64:67]
	v_mfma_f32_16x16x128_f8f6f4 v[60:63], v[2:9], v[212:219], v[60:63]
	v_mfma_f32_16x16x128_f8f6f4 v[52:55], v[2:9], v[222:229], v[52:55]
	v_mfma_f32_16x16x128_f8f6f4 v[56:59], v[10:17], v[222:229], v[56:59]
	v_mfma_f32_16x16x128_f8f6f4 v[48:51], v[10:17], v[230:237], v[48:51]
	v_mfma_f32_16x16x128_f8f6f4 v[44:47], v[2:9], v[230:237], v[44:47]
	v_mfma_f32_16x16x128_f8f6f4 v[36:39], v[2:9], v[238:245], v[36:39]
	s_barrier
	v_mfma_f32_16x16x128_f8f6f4 v[40:43], v[10:17], v[238:245], v[40:43]
	s_setprio 0
	ds_read_b128 v[178:181], v201
	ds_read_b128 v[182:185], v201 offset:1024
	ds_read_b128 v[204:207], v201 offset:2048
	ds_read_b128 v[208:211], v201 offset:3072
	ds_read_b128 v[10:13], v202
	ds_read_b128 v[14:17], v202 offset:1024
	ds_read_b128 v[2:5], v202 offset:2048
	ds_read_b128 v[6:9], v202 offset:3072
	s_mov_b32 m0, s85
	ds_read_b128 v[212:215], v169 offset:32768
	ds_read_b128 v[216:219], v169 offset:33792
	ds_read_b128 v[222:225], v169 offset:34816
	ds_read_b128 v[226:229], v169 offset:35840
	ds_read_b128 v[230:233], v169 offset:36864
	ds_read_b128 v[234:237], v169 offset:37888
	ds_read_b128 v[238:241], v169 offset:38912
	ds_read_b128 v[242:245], v169 offset:39936
	global_load_lds_dwordx4 v189, s[48:49]
	s_mov_b32 m0, s86
	s_nop 0
	global_load_lds_dwordx4 v198, s[48:49]
	s_waitcnt vmcnt(8)
	s_waitcnt lgkmcnt(0)
	s_barrier
	v_mfma_f32_16x16x128_f8f6f4 v[160:163], v[178:185], v[212:219], v[160:163]
	s_setprio 1
	v_mfma_f32_16x16x128_f8f6f4 v[156:159], v[204:211], v[212:219], v[156:159]
	v_mfma_f32_16x16x128_f8f6f4 v[148:151], v[204:211], v[222:229], v[148:151]
	v_mfma_f32_16x16x128_f8f6f4 v[152:155], v[178:185], v[222:229], v[152:155]
	v_mfma_f32_16x16x128_f8f6f4 v[144:147], v[178:185], v[230:237], v[144:147]
	v_mfma_f32_16x16x128_f8f6f4 v[140:143], v[204:211], v[230:237], v[140:143]
	v_mfma_f32_16x16x128_f8f6f4 v[132:135], v[204:211], v[238:245], v[132:135]
	v_mfma_f32_16x16x128_f8f6f4 v[136:139], v[178:185], v[238:245], v[136:139]
	v_mfma_f32_16x16x128_f8f6f4 v[128:131], v[10:17], v[212:219], v[128:131]
	v_mfma_f32_16x16x128_f8f6f4 v[124:127], v[2:9], v[212:219], v[124:127]
	v_mfma_f32_16x16x128_f8f6f4 v[116:119], v[2:9], v[222:229], v[116:119]
	v_mfma_f32_16x16x128_f8f6f4 v[120:123], v[10:17], v[222:229], v[120:123]
	v_mfma_f32_16x16x128_f8f6f4 v[112:115], v[10:17], v[230:237], v[112:115]
	v_mfma_f32_16x16x128_f8f6f4 v[108:111], v[2:9], v[230:237], v[108:111]
	v_mfma_f32_16x16x128_f8f6f4 v[100:103], v[2:9], v[238:245], v[100:103]
	s_barrier
	v_mfma_f32_16x16x128_f8f6f4 v[104:107], v[10:17], v[238:245], v[104:107]
	s_setprio 0
	s_mov_b32 m0, s50
	v_lshl_add_u64 v[22:23], v[22:23], 0, s[18:19]
	s_add_u32 s46, s46, 0x20080
	ds_read_b128 v[212:215], v169 offset:49152
	ds_read_b128 v[216:219], v169 offset:50176
	ds_read_b128 v[222:225], v169 offset:51200
	ds_read_b128 v[226:229], v169 offset:52224
	ds_read_b128 v[230:233], v169 offset:53248
	ds_read_b128 v[234:237], v169 offset:54272
	ds_read_b128 v[238:241], v169 offset:55296
	ds_read_b128 v[242:245], v169 offset:56320
	global_load_lds_dwordx4 v[22:23], off
	v_lshl_add_u64 v[22:23], v[24:25], 0, s[18:19]
	s_mov_b32 m0, s51
	s_addc_u32 s47, s47, 0
	global_load_lds_dwordx4 v[22:23], off
	v_lshl_add_u64 v[22:23], s[46:47], 0, v[170:171]
	s_mov_b32 m0, s64
	s_nop 0
	global_load_lds_dwordx4 v[22:23], off
	v_lshl_add_u64 v[22:23], s[46:47], 0, v[172:173]
	s_mov_b32 m0, s63
	s_nop 0
	global_load_lds_dwordx4 v[22:23], off
	v_lshl_add_u64 v[22:23], v[28:29], 0, s[18:19]
	s_mov_b32 m0, s90
	s_nop 0
	global_load_lds_dwordx4 v[22:23], off
	v_lshl_add_u64 v[22:23], v[26:27], 0, s[18:19]
	s_mov_b32 m0, s91
	s_nop 0
	global_load_lds_dwordx4 v[22:23], off
	s_waitcnt vmcnt(8)
	s_waitcnt lgkmcnt(0)
	s_barrier
	v_mfma_f32_16x16x128_f8f6f4 v[96:99], v[178:185], v[212:219], v[96:99]
	s_setprio 1
	v_mfma_f32_16x16x128_f8f6f4 v[92:95], v[204:211], v[212:219], v[92:95]
	v_mfma_f32_16x16x128_f8f6f4 v[84:87], v[204:211], v[222:229], v[84:87]
	v_mfma_f32_16x16x128_f8f6f4 v[88:91], v[178:185], v[222:229], v[88:91]
	v_mfma_f32_16x16x128_f8f6f4 v[80:83], v[178:185], v[230:237], v[80:83]
	v_mfma_f32_16x16x128_f8f6f4 v[76:79], v[204:211], v[230:237], v[76:79]
	v_mfma_f32_16x16x128_f8f6f4 v[68:71], v[204:211], v[238:245], v[68:71]
	v_mfma_f32_16x16x128_f8f6f4 v[72:75], v[178:185], v[238:245], v[72:75]
	v_mfma_f32_16x16x128_f8f6f4 v[64:67], v[10:17], v[212:219], v[64:67]
	v_mfma_f32_16x16x128_f8f6f4 v[60:63], v[2:9], v[212:219], v[60:63]
	v_mfma_f32_16x16x128_f8f6f4 v[52:55], v[2:9], v[222:229], v[52:55]
	v_mfma_f32_16x16x128_f8f6f4 v[56:59], v[10:17], v[222:229], v[56:59]
	v_mfma_f32_16x16x128_f8f6f4 v[48:51], v[10:17], v[230:237], v[48:51]
	v_mfma_f32_16x16x128_f8f6f4 v[44:47], v[2:9], v[230:237], v[44:47]
	v_mfma_f32_16x16x128_f8f6f4 v[36:39], v[2:9], v[238:245], v[36:39]
	s_barrier
	v_mfma_f32_16x16x128_f8f6f4 v[40:43], v[10:17], v[238:245], v[40:43]
	s_setprio 0
	s_add_i32 s75, s75, 2
	s_add_u32 s30, s30, 0x100
	s_addc_u32 s31, s31, 0
	s_cmp_gt_u32 s75, 5
	s_cbranch_scc1 .LBB0_957

.LBB0_1086:
	s_lshl_b32 s10, s51, 18
	s_add_u32 s10, s20, s10
	s_addc_u32 s11, s21, 0
	s_and_b64 s[16:17], s[4:5], exec
	s_cselect_b32 s54, s11, s31
	s_cselect_b32 s55, s10, s30
	s_lshl_b32 s14, s50, 18
	s_add_u32 s16, s15, s14
	s_addc_u32 s17, s26, 0
	s_and_b64 s[36:37], s[4:5], exec
	s_cselect_b32 s56, s17, s23
	s_cselect_b32 s57, s16, s22
	s_add_i32 s60, 0, 0x10000
	s_add_i32 s62, 0, 0x14000
	v_add_u32_e32 v198, s60, v196
	v_add_u32_e32 v199, s62, v196
	ds_read_b128 v[26:29], v198
	ds_read_b128 v[30:33], v198 offset:1024
	ds_read_b128 v[18:21], v198 offset:2048
	ds_read_b128 v[22:25], v198 offset:3072
	ds_read_b128 v[10:13], v199
	ds_read_b128 v[14:17], v199 offset:1024
	ds_read_b128 v[2:5], v199 offset:2048
	ds_read_b128 v[6:9], v199 offset:3072
	s_add_u32 s36, s30, 0x20080
	s_addc_u32 s37, s31, 0
	s_add_i32 s58, s41, 0xc000
	v_lshl_add_u64 v[174:175], s[36:37], 0, v[168:169]
	s_mov_b32 m0, s58
	s_add_i32 s59, s41, 0xe000
	ds_read_b128 v[200:203], v197
	ds_read_b128 v[204:207], v197 offset:1024
	ds_read_b128 v[222:225], v197 offset:2048
	ds_read_b128 v[226:229], v197 offset:3072
	ds_read_b128 v[230:233], v197 offset:4096
	ds_read_b128 v[234:237], v197 offset:5120
	ds_read_b128 v[238:241], v197 offset:6144
	ds_read_b128 v[242:245], v197 offset:7168
	global_load_lds_dwordx4 v[174:175], off
	v_lshl_add_u64 v[174:175], s[36:37], 0, v[166:167]
	s_mov_b32 m0, s59
	s_nop 0
	global_load_lds_dwordx4 v[174:175], off
	s_waitcnt vmcnt(8)
	s_waitcnt lgkmcnt(0)
	s_barrier
	v_mfma_f32_16x16x128_f8f6f4 v[160:163], v[26:33], v[200:207], 0
	s_setprio 1
	v_mfma_f32_16x16x128_f8f6f4 v[156:159], v[18:25], v[200:207], 0
	v_mfma_f32_16x16x128_f8f6f4 v[148:151], v[18:25], v[222:229], 0
	v_mfma_f32_16x16x128_f8f6f4 v[152:155], v[26:33], v[222:229], 0
	v_mfma_f32_16x16x128_f8f6f4 v[144:147], v[26:33], v[230:237], 0
	v_mfma_f32_16x16x128_f8f6f4 v[140:143], v[18:25], v[230:237], 0
	v_mfma_f32_16x16x128_f8f6f4 v[132:135], v[18:25], v[238:245], 0
	v_mfma_f32_16x16x128_f8f6f4 v[136:139], v[26:33], v[238:245], 0
	v_mfma_f32_16x16x128_f8f6f4 v[128:131], v[10:17], v[200:207], 0
	v_mfma_f32_16x16x128_f8f6f4 v[124:127], v[2:9], v[200:207], 0
	v_mfma_f32_16x16x128_f8f6f4 v[116:119], v[2:9], v[222:229], 0
	v_mfma_f32_16x16x128_f8f6f4 v[120:123], v[10:17], v[222:229], 0
	v_mfma_f32_16x16x128_f8f6f4 v[112:115], v[10:17], v[230:237], 0
	v_mfma_f32_16x16x128_f8f6f4 v[108:111], v[2:9], v[230:237], 0
	v_mfma_f32_16x16x128_f8f6f4 v[100:103], v[2:9], v[238:245], 0
	s_barrier
	v_mfma_f32_16x16x128_f8f6f4 v[104:107], v[10:17], v[238:245], 0
	s_setprio 0
	s_add_i32 s60, s60, s40
	v_lshl_add_u64 v[174:175], s[22:23], 0, v[34:35]
	s_add_i32 s61, s60, 0x2000
	v_lshl_add_u64 v[178:179], v[174:175], 0, s[28:29]
	s_mov_b32 m0, s60
	v_lshl_add_u64 v[190:191], s[22:23], 0, v[164:165]
	s_add_u32 s36, s22, 0x20100
	ds_read_b128 v[200:203], v197 offset:16384
	ds_read_b128 v[204:207], v197 offset:17408
	ds_read_b128 v[222:225], v197 offset:18432
	ds_read_b128 v[226:229], v197 offset:19456
	ds_read_b128 v[230:233], v197 offset:20480
	ds_read_b128 v[234:237], v197 offset:21504
	ds_read_b128 v[238:241], v197 offset:22528
	ds_read_b128 v[242:245], v197 offset:23552
	global_load_lds_dwordx4 v[178:179], off
	v_lshl_add_u64 v[178:179], v[190:191], 0, s[28:29]
	s_mov_b32 m0, s61
	s_addc_u32 s37, s23, 0
	s_add_i32 s62, s62, s40
	global_load_lds_dwordx4 v[178:179], off
	v_lshl_add_u64 v[178:179], s[36:37], 0, v[34:35]
	s_mov_b32 m0, s62
	s_add_i32 s63, s62, 0x2000
	global_load_lds_dwordx4 v[178:179], off
	v_lshl_add_u64 v[178:179], s[36:37], 0, v[164:165]
	s_mov_b32 m0, s63
	v_lshl_add_u64 v[192:193], s[30:31], 0, v[168:169]
	global_load_lds_dwordx4 v[178:179], off
	v_lshl_add_u64 v[178:179], v[192:193], 0, s[28:29]
	s_mov_b32 m0, s41
	v_lshl_add_u64 v[194:195], s[30:31], 0, v[166:167]
	global_load_lds_dwordx4 v[178:179], off
	v_lshl_add_u64 v[178:179], v[194:195], 0, s[28:29]
	s_mov_b32 m0, s42
	s_nop 0
	global_load_lds_dwordx4 v[178:179], off
	s_waitcnt vmcnt(8)
	s_waitcnt lgkmcnt(0)
	s_barrier
	v_mfma_f32_16x16x128_f8f6f4 v[96:99], v[26:33], v[200:207], 0
	s_setprio 1
	v_mfma_f32_16x16x128_f8f6f4 v[92:95], v[18:25], v[200:207], 0
	v_mfma_f32_16x16x128_f8f6f4 v[84:87], v[18:25], v[222:229], 0
	v_mfma_f32_16x16x128_f8f6f4 v[88:91], v[26:33], v[222:229], 0
	v_mfma_f32_16x16x128_f8f6f4 v[80:83], v[26:33], v[230:237], 0
	v_mfma_f32_16x16x128_f8f6f4 v[76:79], v[18:25], v[230:237], 0
	v_mfma_f32_16x16x128_f8f6f4 v[68:71], v[18:25], v[238:245], 0
	v_mfma_f32_16x16x128_f8f6f4 v[72:75], v[26:33], v[238:245], 0
	v_mfma_f32_16x16x128_f8f6f4 v[64:67], v[10:17], v[200:207], 0
	v_mfma_f32_16x16x128_f8f6f4 v[60:63], v[2:9], v[200:207], 0
	v_mfma_f32_16x16x128_f8f6f4 v[52:55], v[2:9], v[222:229], 0
	v_mfma_f32_16x16x128_f8f6f4 v[56:59], v[10:17], v[222:229], 0
	v_mfma_f32_16x16x128_f8f6f4 v[48:51], v[10:17], v[230:237], 0
	v_mfma_f32_16x16x128_f8f6f4 v[44:47], v[2:9], v[230:237], 0
	v_mfma_f32_16x16x128_f8f6f4 v[36:39], v[2:9], v[238:245], 0
	s_barrier
	v_mfma_f32_16x16x128_f8f6f4 v[40:43], v[10:17], v[238:245], 0
	s_setprio 0
	s_add_i32 s64, 0, 0x18000
	s_add_i32 s66, 0, 0x1c000
	v_add_u32_e32 v200, s64, v196
	v_add_u32_e32 v201, s66, v196
	ds_read_b128 v[26:29], v200
	ds_read_b128 v[30:33], v200 offset:1024
	ds_read_b128 v[18:21], v200 offset:2048
	ds_read_b128 v[22:25], v200 offset:3072
	ds_read_b128 v[10:13], v201
	ds_read_b128 v[14:17], v201 offset:1024
	ds_read_b128 v[2:5], v201 offset:2048
	ds_read_b128 v[6:9], v201 offset:3072
	s_add_u32 s36, s30, 0x20100
	s_addc_u32 s37, s31, 0
	s_mov_b32 m0, s43
	v_lshl_add_u64 v[178:179], s[36:37], 0, v[168:169]
	ds_read_b128 v[202:205], v197 offset:32768
	ds_read_b128 v[206:209], v197 offset:33792
	ds_read_b128 v[222:225], v197 offset:34816
	ds_read_b128 v[226:229], v197 offset:35840
	ds_read_b128 v[230:233], v197 offset:36864
	ds_read_b128 v[234:237], v197 offset:37888
	ds_read_b128 v[238:241], v197 offset:38912
	ds_read_b128 v[242:245], v197 offset:39936
	global_load_lds_dwordx4 v[178:179], off
	v_lshl_add_u64 v[178:179], s[36:37], 0, v[166:167]
	s_mov_b32 m0, s44
	s_nop 0
	global_load_lds_dwordx4 v[178:179], off
	s_waitcnt vmcnt(8)
	s_waitcnt lgkmcnt(0)
	s_barrier
	v_mfma_f32_16x16x128_f8f6f4 v[160:163], v[26:33], v[202:209], v[160:163]
	s_setprio 1
	v_mfma_f32_16x16x128_f8f6f4 v[156:159], v[18:25], v[202:209], v[156:159]
	v_mfma_f32_16x16x128_f8f6f4 v[148:151], v[18:25], v[222:229], v[148:151]
	v_mfma_f32_16x16x128_f8f6f4 v[152:155], v[26:33], v[222:229], v[152:155]
	v_mfma_f32_16x16x128_f8f6f4 v[144:147], v[26:33], v[230:237], v[144:147]
	v_mfma_f32_16x16x128_f8f6f4 v[140:143], v[18:25], v[230:237], v[140:143]
	v_mfma_f32_16x16x128_f8f6f4 v[132:135], v[18:25], v[238:245], v[132:135]
	v_mfma_f32_16x16x128_f8f6f4 v[136:139], v[26:33], v[238:245], v[136:139]
	v_mfma_f32_16x16x128_f8f6f4 v[128:131], v[10:17], v[202:209], v[128:131]
	v_mfma_f32_16x16x128_f8f6f4 v[124:127], v[2:9], v[202:209], v[124:127]
	v_mfma_f32_16x16x128_f8f6f4 v[116:119], v[2:9], v[222:229], v[116:119]
	v_mfma_f32_16x16x128_f8f6f4 v[120:123], v[10:17], v[222:229], v[120:123]
	v_mfma_f32_16x16x128_f8f6f4 v[112:115], v[10:17], v[230:237], v[112:115]
	v_mfma_f32_16x16x128_f8f6f4 v[108:111], v[2:9], v[230:237], v[108:111]
	v_mfma_f32_16x16x128_f8f6f4 v[100:103], v[2:9], v[238:245], v[100:103]
	s_barrier
	v_mfma_f32_16x16x128_f8f6f4 v[104:107], v[10:17], v[238:245], v[104:107]
	s_setprio 0
	s_add_i32 s64, s64, s40
	s_mov_b64 s[24:25], 0x180
	s_add_i32 s65, s64, 0x2000
	v_lshl_add_u64 v[174:175], v[174:175], 0, s[24:25]
	s_mov_b32 m0, s64
	s_add_u32 s36, s22, 0x20180
	ds_read_b128 v[202:205], v197 offset:49152
	ds_read_b128 v[206:209], v197 offset:50176
	ds_read_b128 v[222:225], v197 offset:51200
	ds_read_b128 v[226:229], v197 offset:52224
	ds_read_b128 v[230:233], v197 offset:53248
	ds_read_b128 v[234:237], v197 offset:54272
	ds_read_b128 v[238:241], v197 offset:55296
	ds_read_b128 v[242:245], v197 offset:56320
	global_load_lds_dwordx4 v[174:175], off
	v_lshl_add_u64 v[174:175], v[190:191], 0, s[24:25]
	s_mov_b32 m0, s65
	s_addc_u32 s37, s23, 0
	s_add_i32 s66, s66, s40
	global_load_lds_dwordx4 v[174:175], off
	v_lshl_add_u64 v[174:175], s[36:37], 0, v[34:35]
	s_mov_b32 m0, s66
	s_add_i32 s67, s66, 0x2000
	global_load_lds_dwordx4 v[174:175], off
	v_lshl_add_u64 v[174:175], s[36:37], 0, v[164:165]
	s_mov_b32 m0, s67
	s_nop 0
	global_load_lds_dwordx4 v[174:175], off
	v_lshl_add_u64 v[174:175], v[192:193], 0, s[24:25]
	s_mov_b32 m0, s47
	s_nop 0
	global_load_lds_dwordx4 v[174:175], off
	v_lshl_add_u64 v[174:175], v[194:195], 0, s[24:25]
	s_mov_b32 m0, s48
	s_nop 0
	global_load_lds_dwordx4 v[174:175], off
	s_waitcnt vmcnt(8)
	s_waitcnt lgkmcnt(0)
	s_barrier
	v_mfma_f32_16x16x128_f8f6f4 v[96:99], v[26:33], v[202:209], v[96:99]
	s_setprio 1
	v_mfma_f32_16x16x128_f8f6f4 v[92:95], v[18:25], v[202:209], v[92:95]
	v_mfma_f32_16x16x128_f8f6f4 v[84:87], v[18:25], v[222:229], v[84:87]
	v_mfma_f32_16x16x128_f8f6f4 v[88:91], v[26:33], v[222:229], v[88:91]
	v_mfma_f32_16x16x128_f8f6f4 v[80:83], v[26:33], v[230:237], v[80:83]
	v_mfma_f32_16x16x128_f8f6f4 v[76:79], v[18:25], v[230:237], v[76:79]
	v_mfma_f32_16x16x128_f8f6f4 v[68:71], v[18:25], v[238:245], v[68:71]
	v_mfma_f32_16x16x128_f8f6f4 v[72:75], v[26:33], v[238:245], v[72:75]
	v_mfma_f32_16x16x128_f8f6f4 v[64:67], v[10:17], v[202:209], v[64:67]
	v_mfma_f32_16x16x128_f8f6f4 v[60:63], v[2:9], v[202:209], v[60:63]
	v_mfma_f32_16x16x128_f8f6f4 v[52:55], v[2:9], v[222:229], v[52:55]
	v_mfma_f32_16x16x128_f8f6f4 v[56:59], v[10:17], v[222:229], v[56:59]
	v_mfma_f32_16x16x128_f8f6f4 v[48:51], v[10:17], v[230:237], v[48:51]
	v_mfma_f32_16x16x128_f8f6f4 v[44:47], v[2:9], v[230:237], v[44:47]
	v_mfma_f32_16x16x128_f8f6f4 v[36:39], v[2:9], v[238:245], v[36:39]
	s_barrier
	v_mfma_f32_16x16x128_f8f6f4 v[40:43], v[10:17], v[238:245], v[40:43]
	s_setprio 0
	s_add_u32 s30, s30, 0x20180
	s_addc_u32 s31, s31, 0
	s_add_u32 s68, s22, 0x200
	s_addc_u32 s69, s23, 0
	s_mov_b32 s70, 0
.LBB0_1087:
	ds_read_b128 v[2:5], v198
	ds_read_b128 v[6:9], v198 offset:1024
	ds_read_b128 v[10:13], v198 offset:2048
	ds_read_b128 v[14:17], v198 offset:3072
	ds_read_b128 v[18:21], v199
	ds_read_b128 v[22:25], v199 offset:1024
	ds_read_b128 v[26:29], v199 offset:2048
	ds_read_b128 v[30:33], v199 offset:3072
	s_add_u32 s14, s30, 0xfffe0080
	s_addc_u32 s22, s31, -1
	s_cmp_eq_u32 s70, 4
	s_cselect_b32 s37, s54, s22
	s_cselect_b32 s36, s55, s14
	s_cselect_b32 s23, s56, s69
	s_cselect_b32 s22, s57, s68
	s_mov_b32 m0, s58
	v_lshl_add_u64 v[174:175], s[30:31], 0, v[170:171]
	ds_read_b128 v[202:205], v197
	ds_read_b128 v[206:209], v197 offset:1024
	ds_read_b128 v[222:225], v197 offset:2048
	ds_read_b128 v[226:229], v197 offset:3072
	ds_read_b128 v[230:233], v197 offset:4096
	ds_read_b128 v[234:237], v197 offset:5120
	ds_read_b128 v[238:241], v197 offset:6144
	ds_read_b128 v[242:245], v197 offset:7168
	global_load_lds_dwordx4 v[174:175], off
	v_lshl_add_u64 v[174:175], s[30:31], 0, v[172:173]
	s_mov_b32 m0, s59
	s_nop 0
	global_load_lds_dwordx4 v[174:175], off
	s_waitcnt vmcnt(8)
	s_waitcnt lgkmcnt(0)
	s_barrier
	v_mfma_f32_16x16x128_f8f6f4 v[160:163], v[2:9], v[202:209], v[160:163]
	s_setprio 1
	v_mfma_f32_16x16x128_f8f6f4 v[156:159], v[10:17], v[202:209], v[156:159]
	v_mfma_f32_16x16x128_f8f6f4 v[148:151], v[10:17], v[222:229], v[148:151]
	v_mfma_f32_16x16x128_f8f6f4 v[152:155], v[2:9], v[222:229], v[152:155]
	v_mfma_f32_16x16x128_f8f6f4 v[144:147], v[2:9], v[230:237], v[144:147]
	v_mfma_f32_16x16x128_f8f6f4 v[140:143], v[10:17], v[230:237], v[140:143]
	v_mfma_f32_16x16x128_f8f6f4 v[132:135], v[10:17], v[238:245], v[132:135]
	v_mfma_f32_16x16x128_f8f6f4 v[136:139], v[2:9], v[238:245], v[136:139]
	v_mfma_f32_16x16x128_f8f6f4 v[128:131], v[18:25], v[202:209], v[128:131]
	v_mfma_f32_16x16x128_f8f6f4 v[124:127], v[26:33], v[202:209], v[124:127]
	v_mfma_f32_16x16x128_f8f6f4 v[116:119], v[26:33], v[222:229], v[116:119]
	v_mfma_f32_16x16x128_f8f6f4 v[120:123], v[18:25], v[222:229], v[120:123]
	v_mfma_f32_16x16x128_f8f6f4 v[112:115], v[18:25], v[230:237], v[112:115]
	v_mfma_f32_16x16x128_f8f6f4 v[108:111], v[26:33], v[230:237], v[108:111]
	v_mfma_f32_16x16x128_f8f6f4 v[100:103], v[26:33], v[238:245], v[100:103]
	s_barrier
	v_mfma_f32_16x16x128_f8f6f4 v[104:107], v[18:25], v[238:245], v[104:107]
	s_setprio 0
	s_mov_b32 m0, s60
	v_lshl_add_u64 v[174:175], s[22:23], 0, v[34:35]
	s_add_u32 s72, s22, 0x20000
	ds_read_b128 v[202:205], v197 offset:16384
	ds_read_b128 v[206:209], v197 offset:17408
	ds_read_b128 v[222:225], v197 offset:18432
	ds_read_b128 v[226:229], v197 offset:19456
	ds_read_b128 v[230:233], v197 offset:20480
	ds_read_b128 v[234:237], v197 offset:21504
	ds_read_b128 v[238:241], v197 offset:22528
	ds_read_b128 v[242:245], v197 offset:23552
	global_load_lds_dwordx4 v[174:175], off
	v_lshl_add_u64 v[190:191], s[22:23], 0, v[164:165]
	s_mov_b32 m0, s61
	s_addc_u32 s73, s23, 0
	global_load_lds_dwordx4 v[190:191], off
	v_lshl_add_u64 v[178:179], s[72:73], 0, v[34:35]
	s_mov_b32 m0, s62
	v_lshl_add_u64 v[192:193], s[36:37], 0, v[168:169]
	global_load_lds_dwordx4 v[178:179], off
	v_lshl_add_u64 v[178:179], s[72:73], 0, v[164:165]
	s_mov_b32 m0, s63
	v_lshl_add_u64 v[194:195], s[36:37], 0, v[166:167]
	global_load_lds_dwordx4 v[178:179], off
	s_mov_b32 m0, s41
	s_nop 0
	global_load_lds_dwordx4 v[192:193], off
	s_mov_b32 m0, s42
	s_nop 0
	global_load_lds_dwordx4 v[194:195], off
	s_waitcnt vmcnt(8)
	s_waitcnt lgkmcnt(0)
	s_barrier
	v_mfma_f32_16x16x128_f8f6f4 v[96:99], v[2:9], v[202:209], v[96:99]
	s_setprio 1
	v_mfma_f32_16x16x128_f8f6f4 v[92:95], v[10:17], v[202:209], v[92:95]
	v_mfma_f32_16x16x128_f8f6f4 v[84:87], v[10:17], v[222:229], v[84:87]
	v_mfma_f32_16x16x128_f8f6f4 v[88:91], v[2:9], v[222:229], v[88:91]
	v_mfma_f32_16x16x128_f8f6f4 v[80:83], v[2:9], v[230:237], v[80:83]
	v_mfma_f32_16x16x128_f8f6f4 v[76:79], v[10:17], v[230:237], v[76:79]
	v_mfma_f32_16x16x128_f8f6f4 v[68:71], v[10:17], v[238:245], v[68:71]
	v_mfma_f32_16x16x128_f8f6f4 v[72:75], v[2:9], v[238:245], v[72:75]
	v_mfma_f32_16x16x128_f8f6f4 v[64:67], v[18:25], v[202:209], v[64:67]
	v_mfma_f32_16x16x128_f8f6f4 v[60:63], v[26:33], v[202:209], v[60:63]
	v_mfma_f32_16x16x128_f8f6f4 v[52:55], v[26:33], v[222:229], v[52:55]
	v_mfma_f32_16x16x128_f8f6f4 v[56:59], v[18:25], v[222:229], v[56:59]
	v_mfma_f32_16x16x128_f8f6f4 v[48:51], v[18:25], v[230:237], v[48:51]
	v_mfma_f32_16x16x128_f8f6f4 v[44:47], v[26:33], v[230:237], v[44:47]
	v_mfma_f32_16x16x128_f8f6f4 v[36:39], v[26:33], v[238:245], v[36:39]
	s_barrier
	v_mfma_f32_16x16x128_f8f6f4 v[40:43], v[18:25], v[238:245], v[40:43]
	s_setprio 0
	ds_read_b128 v[26:29], v200
	ds_read_b128 v[30:33], v200 offset:1024
	ds_read_b128 v[18:21], v200 offset:2048
	ds_read_b128 v[22:25], v200 offset:3072
	ds_read_b128 v[10:13], v201
	ds_read_b128 v[14:17], v201 offset:1024
	ds_read_b128 v[2:5], v201 offset:2048
	ds_read_b128 v[6:9], v201 offset:3072
	s_add_u32 s36, s36, 0x20000
	s_addc_u32 s37, s37, 0
	s_mov_b32 m0, s43
	v_lshl_add_u64 v[178:179], s[36:37], 0, v[168:169]
	ds_read_b128 v[202:205], v197 offset:32768
	ds_read_b128 v[206:209], v197 offset:33792
	ds_read_b128 v[222:225], v197 offset:34816
	ds_read_b128 v[226:229], v197 offset:35840
	ds_read_b128 v[230:233], v197 offset:36864
	ds_read_b128 v[234:237], v197 offset:37888
	ds_read_b128 v[238:241], v197 offset:38912
	ds_read_b128 v[242:245], v197 offset:39936
	global_load_lds_dwordx4 v[178:179], off
	v_lshl_add_u64 v[178:179], s[36:37], 0, v[166:167]
	s_mov_b32 m0, s44
	s_nop 0
	global_load_lds_dwordx4 v[178:179], off
	s_waitcnt vmcnt(8)
	s_waitcnt lgkmcnt(0)
	s_barrier
	v_mfma_f32_16x16x128_f8f6f4 v[160:163], v[26:33], v[202:209], v[160:163]
	s_setprio 1
	v_mfma_f32_16x16x128_f8f6f4 v[156:159], v[18:25], v[202:209], v[156:159]
	v_mfma_f32_16x16x128_f8f6f4 v[148:151], v[18:25], v[222:229], v[148:151]
	v_mfma_f32_16x16x128_f8f6f4 v[152:155], v[26:33], v[222:229], v[152:155]
	v_mfma_f32_16x16x128_f8f6f4 v[144:147], v[26:33], v[230:237], v[144:147]
	v_mfma_f32_16x16x128_f8f6f4 v[140:143], v[18:25], v[230:237], v[140:143]
	v_mfma_f32_16x16x128_f8f6f4 v[132:135], v[18:25], v[238:245], v[132:135]
	v_mfma_f32_16x16x128_f8f6f4 v[136:139], v[26:33], v[238:245], v[136:139]
	v_mfma_f32_16x16x128_f8f6f4 v[128:131], v[10:17], v[202:209], v[128:131]
	v_mfma_f32_16x16x128_f8f6f4 v[124:127], v[2:9], v[202:209], v[124:127]
	v_mfma_f32_16x16x128_f8f6f4 v[116:119], v[2:9], v[222:229], v[116:119]
	v_mfma_f32_16x16x128_f8f6f4 v[120:123], v[10:17], v[222:229], v[120:123]
	v_mfma_f32_16x16x128_f8f6f4 v[112:115], v[10:17], v[230:237], v[112:115]
	v_mfma_f32_16x16x128_f8f6f4 v[108:111], v[2:9], v[230:237], v[108:111]
	v_mfma_f32_16x16x128_f8f6f4 v[100:103], v[2:9], v[238:245], v[100:103]
	s_barrier
	v_mfma_f32_16x16x128_f8f6f4 v[104:107], v[10:17], v[238:245], v[104:107]
	s_setprio 0
	s_mov_b32 m0, s64
	v_lshl_add_u64 v[174:175], v[174:175], 0, s[18:19]
	s_add_u32 s22, s22, 0x20080
	ds_read_b128 v[202:205], v197 offset:49152
	ds_read_b128 v[206:209], v197 offset:50176
	ds_read_b128 v[222:225], v197 offset:51200
	ds_read_b128 v[226:229], v197 offset:52224
	ds_read_b128 v[230:233], v197 offset:53248
	ds_read_b128 v[234:237], v197 offset:54272
	ds_read_b128 v[238:241], v197 offset:55296
	ds_read_b128 v[242:245], v197 offset:56320
	global_load_lds_dwordx4 v[174:175], off
	v_lshl_add_u64 v[174:175], v[190:191], 0, s[18:19]
	s_mov_b32 m0, s65
	s_addc_u32 s23, s23, 0
	global_load_lds_dwordx4 v[174:175], off
	v_lshl_add_u64 v[174:175], s[22:23], 0, v[34:35]
	s_mov_b32 m0, s66
	s_nop 0
	global_load_lds_dwordx4 v[174:175], off
	v_lshl_add_u64 v[174:175], s[22:23], 0, v[164:165]
	s_mov_b32 m0, s67
	s_nop 0
	global_load_lds_dwordx4 v[174:175], off
	v_lshl_add_u64 v[174:175], v[192:193], 0, s[18:19]
	s_mov_b32 m0, s47
	s_nop 0
	global_load_lds_dwordx4 v[174:175], off
	v_lshl_add_u64 v[174:175], v[194:195], 0, s[18:19]
	s_mov_b32 m0, s48
	s_nop 0
	global_load_lds_dwordx4 v[174:175], off
	s_waitcnt vmcnt(8)
	s_waitcnt lgkmcnt(0)
	s_barrier
	v_mfma_f32_16x16x128_f8f6f4 v[96:99], v[26:33], v[202:209], v[96:99]
	s_setprio 1
	v_mfma_f32_16x16x128_f8f6f4 v[92:95], v[18:25], v[202:209], v[92:95]
	v_mfma_f32_16x16x128_f8f6f4 v[84:87], v[18:25], v[222:229], v[84:87]
	v_mfma_f32_16x16x128_f8f6f4 v[88:91], v[26:33], v[222:229], v[88:91]
	v_mfma_f32_16x16x128_f8f6f4 v[80:83], v[26:33], v[230:237], v[80:83]
	v_mfma_f32_16x16x128_f8f6f4 v[76:79], v[18:25], v[230:237], v[76:79]
	v_mfma_f32_16x16x128_f8f6f4 v[68:71], v[18:25], v[238:245], v[68:71]
	v_mfma_f32_16x16x128_f8f6f4 v[72:75], v[26:33], v[238:245], v[72:75]
	v_mfma_f32_16x16x128_f8f6f4 v[64:67], v[10:17], v[202:209], v[64:67]
	v_mfma_f32_16x16x128_f8f6f4 v[60:63], v[2:9], v[202:209], v[60:63]
	v_mfma_f32_16x16x128_f8f6f4 v[52:55], v[2:9], v[222:229], v[52:55]
	v_mfma_f32_16x16x128_f8f6f4 v[56:59], v[10:17], v[222:229], v[56:59]
	v_mfma_f32_16x16x128_f8f6f4 v[48:51], v[10:17], v[230:237], v[48:51]
	v_mfma_f32_16x16x128_f8f6f4 v[44:47], v[2:9], v[230:237], v[44:47]
	v_mfma_f32_16x16x128_f8f6f4 v[36:39], v[2:9], v[238:245], v[36:39]
	s_barrier
	v_mfma_f32_16x16x128_f8f6f4 v[40:43], v[10:17], v[238:245], v[40:43]
	s_setprio 0
	s_add_i32 s70, s70, 2
	s_add_u32 s30, s30, 0x100
	s_addc_u32 s31, s31, 0
	s_add_u32 s68, s68, 0x100
	s_addc_u32 s69, s69, 0
	s_cmp_gt_u32 s70, 5
	s_cbranch_scc0 .LBB0_1087

.LBB0_1160:
	s_add_u32 s22, s30, 0x100
	s_addc_u32 s23, s31, 0
	s_add_i32 s65, 0, 0x10000
	s_cmp_eq_u32 s64, 18
	s_cselect_b32 s41, s58, s23
	s_cselect_b32 s40, s59, s22
	s_cselect_b32 s37, s60, s63
	s_cselect_b32 s36, s61, s62
	s_add_i32 s66, 0, 0x14000
	v_add_u32_e32 v2, s65, v222
	v_add_u32_e32 v6, s66, v222
	ds_read_b128 v[26:29], v2
	ds_read_b128 v[30:33], v2 offset:1024
	ds_read_b128 v[18:21], v2 offset:2048
	ds_read_b128 v[22:25], v2 offset:3072
	ds_read_b128 v[10:13], v6
	ds_read_b128 v[14:17], v6 offset:1024
	ds_read_b128 v[2:5], v6 offset:2048
	ds_read_b128 v[6:9], v6 offset:3072
	v_lshl_add_u64 v[174:175], s[30:31], 0, v[170:171]
	s_add_i32 m0, s43, 0xc000
	ds_read_b128 v[190:193], v223
	ds_read_b128 v[194:197], v223 offset:1024
	ds_read_b128 v[198:201], v223 offset:2048
	ds_read_b128 v[202:205], v223 offset:3072
	ds_read_b128 v[224:227], v223 offset:4096
	ds_read_b128 v[228:231], v223 offset:5120
	ds_read_b128 v[232:235], v223 offset:6144
	ds_read_b128 v[236:239], v223 offset:7168
	global_load_lds_dwordx4 v[174:175], off
	v_lshl_add_u64 v[174:175], s[30:31], 0, v[172:173]
	s_add_i32 m0, s43, 0xe000
	s_nop 0
	global_load_lds_dwordx4 v[174:175], off
	s_waitcnt vmcnt(8)
	s_waitcnt lgkmcnt(0)
	s_barrier
	v_mfma_f32_16x16x128_f8f6f4 v[160:163], v[26:33], v[190:197], v[160:163]
	s_setprio 1
	v_mfma_f32_16x16x128_f8f6f4 v[156:159], v[18:25], v[190:197], v[156:159]
	v_mfma_f32_16x16x128_f8f6f4 v[140:143], v[18:25], v[198:205], v[140:143]
	v_mfma_f32_16x16x128_f8f6f4 v[144:147], v[26:33], v[198:205], v[144:147]
	v_mfma_f32_16x16x128_f8f6f4 v[132:135], v[26:33], v[224:231], v[132:135]
	v_mfma_f32_16x16x128_f8f6f4 v[124:127], v[18:25], v[224:231], v[124:127]
	v_mfma_f32_16x16x128_f8f6f4 v[108:111], v[18:25], v[232:239], v[108:111]
	v_mfma_f32_16x16x128_f8f6f4 v[116:119], v[26:33], v[232:239], v[116:119]
	v_mfma_f32_16x16x128_f8f6f4 v[152:155], v[10:17], v[190:197], v[152:155]
	v_mfma_f32_16x16x128_f8f6f4 v[148:151], v[2:9], v[190:197], v[148:151]
	v_mfma_f32_16x16x128_f8f6f4 v[128:131], v[2:9], v[198:205], v[128:131]
	v_mfma_f32_16x16x128_f8f6f4 v[136:139], v[10:17], v[198:205], v[136:139]
	v_mfma_f32_16x16x128_f8f6f4 v[120:123], v[10:17], v[224:231], v[120:123]
	v_mfma_f32_16x16x128_f8f6f4 v[112:115], v[2:9], v[224:231], v[112:115]
	v_mfma_f32_16x16x128_f8f6f4 v[100:103], v[2:9], v[232:239], v[100:103]
	s_barrier
	v_mfma_f32_16x16x128_f8f6f4 v[104:107], v[10:17], v[232:239], v[104:107]
	s_setprio 0
	s_add_i32 s14, s65, s42
	v_lshl_add_u64 v[174:175], s[36:37], 0, v[34:35]
	s_mov_b32 m0, s14
	ds_read_b128 v[196:199], v223 offset:16384
	ds_read_b128 v[200:203], v223 offset:17408
	ds_read_b128 v[204:207], v223 offset:18432
	ds_read_b128 v[208:211], v223 offset:19456
	ds_read_b128 v[224:227], v223 offset:20480
	ds_read_b128 v[228:231], v223 offset:21504
	ds_read_b128 v[232:235], v223 offset:22528
	ds_read_b128 v[236:239], v223 offset:23552
	global_load_lds_dwordx4 v[174:175], off
	s_add_i32 m0, s14, 0x2000
	s_add_u32 s30, s36, 0x58000
	v_lshl_add_u64 v[190:191], s[36:37], 0, v[164:165]
	s_addc_u32 s31, s37, 0
	s_add_i32 s14, s66, s42
	global_load_lds_dwordx4 v[190:191], off
	v_lshl_add_u64 v[178:179], s[30:31], 0, v[34:35]
	s_mov_b32 m0, s14
	v_lshl_add_u64 v[192:193], s[40:41], 0, v[168:169]
	global_load_lds_dwordx4 v[178:179], off
	v_lshl_add_u64 v[178:179], s[30:31], 0, v[164:165]
	s_add_i32 m0, s14, 0x2000
	v_lshl_add_u64 v[194:195], s[40:41], 0, v[166:167]
	global_load_lds_dwordx4 v[178:179], off
	s_mov_b32 m0, s43
	s_nop 0
	global_load_lds_dwordx4 v[192:193], off
	s_mov_b32 m0, s44
	s_nop 0
	global_load_lds_dwordx4 v[194:195], off
	s_waitcnt vmcnt(8)
	s_waitcnt lgkmcnt(0)
	s_barrier
	v_mfma_f32_16x16x128_f8f6f4 v[96:99], v[26:33], v[196:203], v[96:99]
	s_setprio 1
	v_mfma_f32_16x16x128_f8f6f4 v[92:95], v[18:25], v[196:203], v[92:95]
	v_mfma_f32_16x16x128_f8f6f4 v[76:79], v[18:25], v[204:211], v[76:79]
	v_mfma_f32_16x16x128_f8f6f4 v[84:87], v[26:33], v[204:211], v[84:87]
	v_mfma_f32_16x16x128_f8f6f4 v[68:71], v[26:33], v[224:231], v[68:71]
	v_mfma_f32_16x16x128_f8f6f4 v[60:63], v[18:25], v[224:231], v[60:63]
	v_mfma_f32_16x16x128_f8f6f4 v[44:47], v[18:25], v[232:239], v[44:47]
	v_mfma_f32_16x16x128_f8f6f4 v[52:55], v[26:33], v[232:239], v[52:55]
	v_mfma_f32_16x16x128_f8f6f4 v[88:91], v[10:17], v[196:203], v[88:91]
	v_mfma_f32_16x16x128_f8f6f4 v[80:83], v[2:9], v[196:203], v[80:83]
	v_mfma_f32_16x16x128_f8f6f4 v[64:67], v[2:9], v[204:211], v[64:67]
	v_mfma_f32_16x16x128_f8f6f4 v[72:75], v[10:17], v[204:211], v[72:75]
	v_mfma_f32_16x16x128_f8f6f4 v[56:59], v[10:17], v[224:231], v[56:59]
	v_mfma_f32_16x16x128_f8f6f4 v[48:51], v[2:9], v[224:231], v[48:51]
	v_mfma_f32_16x16x128_f8f6f4 v[36:39], v[2:9], v[232:239], v[36:39]
	s_barrier
	v_mfma_f32_16x16x128_f8f6f4 v[40:43], v[10:17], v[232:239], v[40:43]
	s_setprio 0
	s_add_i32 s14, 0, 0x18000
	s_add_i32 s65, 0, 0x1c000
	v_add_u32_e32 v14, s14, v222
	v_add_u32_e32 v30, s65, v222
	ds_read_b128 v[2:5], v14
	ds_read_b128 v[6:9], v14 offset:1024
	ds_read_b128 v[10:13], v14 offset:2048
	ds_read_b128 v[14:17], v14 offset:3072
	ds_read_b128 v[18:21], v30
	ds_read_b128 v[22:25], v30 offset:1024
	ds_read_b128 v[26:29], v30 offset:2048
	ds_read_b128 v[30:33], v30 offset:3072
	s_add_u32 s30, s40, 0x58000
	s_addc_u32 s31, s41, 0
	s_mov_b32 m0, s45
	v_lshl_add_u64 v[178:179], s[30:31], 0, v[168:169]
	ds_read_b128 v[196:199], v223 offset:32768
	ds_read_b128 v[200:203], v223 offset:33792
	ds_read_b128 v[204:207], v223 offset:34816
	ds_read_b128 v[208:211], v223 offset:35840
	ds_read_b128 v[224:227], v223 offset:36864
	ds_read_b128 v[228:231], v223 offset:37888
	ds_read_b128 v[232:235], v223 offset:38912
	ds_read_b128 v[236:239], v223 offset:39936
	global_load_lds_dwordx4 v[178:179], off
	v_lshl_add_u64 v[178:179], s[30:31], 0, v[166:167]
	s_mov_b32 m0, s46
	s_nop 0
	global_load_lds_dwordx4 v[178:179], off
	s_waitcnt vmcnt(8)
	s_waitcnt lgkmcnt(0)
	s_barrier
	v_mfma_f32_16x16x128_f8f6f4 v[160:163], v[2:9], v[196:203], v[160:163]
	s_setprio 1
	v_mfma_f32_16x16x128_f8f6f4 v[156:159], v[10:17], v[196:203], v[156:159]
	v_mfma_f32_16x16x128_f8f6f4 v[140:143], v[10:17], v[204:211], v[140:143]
	v_mfma_f32_16x16x128_f8f6f4 v[144:147], v[2:9], v[204:211], v[144:147]
	v_mfma_f32_16x16x128_f8f6f4 v[132:135], v[2:9], v[224:231], v[132:135]
	v_mfma_f32_16x16x128_f8f6f4 v[124:127], v[10:17], v[224:231], v[124:127]
	v_mfma_f32_16x16x128_f8f6f4 v[108:111], v[10:17], v[232:239], v[108:111]
	v_mfma_f32_16x16x128_f8f6f4 v[116:119], v[2:9], v[232:239], v[116:119]
	v_mfma_f32_16x16x128_f8f6f4 v[152:155], v[18:25], v[196:203], v[152:155]
	v_mfma_f32_16x16x128_f8f6f4 v[148:151], v[26:33], v[196:203], v[148:151]
	v_mfma_f32_16x16x128_f8f6f4 v[128:131], v[26:33], v[204:211], v[128:131]
	v_mfma_f32_16x16x128_f8f6f4 v[136:139], v[18:25], v[204:211], v[136:139]
	v_mfma_f32_16x16x128_f8f6f4 v[120:123], v[18:25], v[224:231], v[120:123]
	v_mfma_f32_16x16x128_f8f6f4 v[112:115], v[26:33], v[224:231], v[112:115]
	v_mfma_f32_16x16x128_f8f6f4 v[100:103], v[26:33], v[232:239], v[100:103]
	s_barrier
	v_mfma_f32_16x16x128_f8f6f4 v[104:107], v[18:25], v[232:239], v[104:107]
	s_setprio 0
	s_add_i32 s14, s14, s42
	v_lshl_add_u64 v[174:175], v[174:175], 0, s[18:19]
	s_mov_b32 m0, s14
	ds_read_b128 v[196:199], v223 offset:49152
	ds_read_b128 v[200:203], v223 offset:50176
	ds_read_b128 v[204:207], v223 offset:51200
	ds_read_b128 v[208:211], v223 offset:52224
	ds_read_b128 v[224:227], v223 offset:53248
	ds_read_b128 v[228:231], v223 offset:54272
	ds_read_b128 v[232:235], v223 offset:55296
	ds_read_b128 v[236:239], v223 offset:56320
	global_load_lds_dwordx4 v[174:175], off
	s_add_i32 m0, s14, 0x2000
	s_add_u32 s30, s36, 0x58080
	v_lshl_add_u64 v[174:175], v[190:191], 0, s[18:19]
	s_addc_u32 s31, s37, 0
	s_add_i32 s14, s65, s42
	global_load_lds_dwordx4 v[174:175], off
	v_lshl_add_u64 v[174:175], s[30:31], 0, v[34:35]
	s_mov_b32 m0, s14
	s_nop 0
	global_load_lds_dwordx4 v[174:175], off
	v_lshl_add_u64 v[174:175], s[30:31], 0, v[164:165]
	s_add_i32 m0, s14, 0x2000
	s_nop 0
	global_load_lds_dwordx4 v[174:175], off
	v_lshl_add_u64 v[174:175], v[192:193], 0, s[18:19]
	s_mov_b32 m0, s51
	s_nop 0
	global_load_lds_dwordx4 v[174:175], off
	v_lshl_add_u64 v[174:175], v[194:195], 0, s[18:19]
	s_mov_b32 m0, s52
	s_nop 0
	global_load_lds_dwordx4 v[174:175], off
	s_waitcnt vmcnt(8)
	s_waitcnt lgkmcnt(0)
	s_barrier
	v_mfma_f32_16x16x128_f8f6f4 v[96:99], v[2:9], v[196:203], v[96:99]
	s_setprio 1
	v_mfma_f32_16x16x128_f8f6f4 v[92:95], v[10:17], v[196:203], v[92:95]
	v_mfma_f32_16x16x128_f8f6f4 v[76:79], v[10:17], v[204:211], v[76:79]
	v_mfma_f32_16x16x128_f8f6f4 v[84:87], v[2:9], v[204:211], v[84:87]
	v_mfma_f32_16x16x128_f8f6f4 v[68:71], v[2:9], v[224:231], v[68:71]
	v_mfma_f32_16x16x128_f8f6f4 v[60:63], v[10:17], v[224:231], v[60:63]
	v_mfma_f32_16x16x128_f8f6f4 v[44:47], v[10:17], v[232:239], v[44:47]
	v_mfma_f32_16x16x128_f8f6f4 v[52:55], v[2:9], v[232:239], v[52:55]
	v_mfma_f32_16x16x128_f8f6f4 v[88:91], v[18:25], v[196:203], v[88:91]
	v_mfma_f32_16x16x128_f8f6f4 v[80:83], v[26:33], v[196:203], v[80:83]
	v_mfma_f32_16x16x128_f8f6f4 v[64:67], v[26:33], v[204:211], v[64:67]
	v_mfma_f32_16x16x128_f8f6f4 v[72:75], v[18:25], v[204:211], v[72:75]
	v_mfma_f32_16x16x128_f8f6f4 v[56:59], v[18:25], v[224:231], v[56:59]
	v_mfma_f32_16x16x128_f8f6f4 v[48:51], v[26:33], v[224:231], v[48:51]
	v_mfma_f32_16x16x128_f8f6f4 v[36:39], v[26:33], v[232:239], v[36:39]
	s_barrier
	v_mfma_f32_16x16x128_f8f6f4 v[40:43], v[18:25], v[232:239], v[40:43]
	s_setprio 0
	s_add_i32 s64, s64, 2
	s_add_u32 s62, s62, 0x100
	s_addc_u32 s63, s63, 0
	s_cmp_gt_u32 s64, 19
	s_mov_b64 s[30:31], s[22:23]
	s_cbranch_scc0 .LBB0_1160
	s_and_b64 vcc, exec, s[8:9]
	s_mov_b32 s58, 0x19b00000
	v_readlane_b32 s59, v255, 10
	s_mov_b32 s60, 0xff61b1e6
	s_mov_b64 s[62:63], 0x800
	s_cbranch_vccz .LBB0_1163
	s_barrier
